# counted vmcnt(12) waits in the 11 weight-conversion tile loops instead of a full drain every 4th tile (+ v1 parallel expert search)
# speedup vs baseline: 1.0304x; 1.0095x over previous
.LBB0_104:
	s_cmp_lt_i32 s94, 3
	s_cselect_b64 s[0:1], -1, 0
	s_ashr_i32 s6, s33, 1
	v_writelane_b32 v250, s6, 3
	s_and_b32 s6, s6, -8
	s_and_b32 s7, s33, 7
	s_waitcnt lgkmcnt(0)
	s_or_b32 s76, s6, s7
	s_add_u32 s74, s90, 0x24a20000
	s_addc_u32 s75, s91, 0
	s_and_b64 s[0:1], s[0:1], s[4:5]
	s_bitcmp0_b32 s33, 3
	s_cselect_b64 s[72:73], -1, 0
	s_and_b64 s[4:5], s[72:73], s[0:1]
	s_andn2_b64 vcc, exec, s[4:5]
	v_writelane_b32 v250, s7, 4
	s_cbranch_vccnz .LBB0_129
	s_lshr_b32 s4, s96, 31
	s_add_i32 s4, s96, s4
	s_ashr_i32 s6, s4, 1
	s_mul_i32 s7, s6, 56
	v_lshrrev_b32_e32 v3, 4, v178
	v_and_b32_e32 v68, 15, v178
	s_cmp_lt_i32 s76, s7
	v_mov_b32_e32 v2, 0
	s_cselect_b64 s[4:5], -1, 0
	s_cmp_ge_i32 s76, s7
	v_lshlrev_b32_e32 v71, 2, v3
	v_lshlrev_b32_e32 v66, 4, v68
	v_mov_b32_e32 v6, 0
	v_mov_b32_e32 v7, 0
	v_mov_b32_e32 v8, 0
	v_mov_b32_e32 v9, 0
	v_mov_b32_e32 v10, 0
	v_mov_b32_e32 v11, 0
	v_mov_b32_e32 v12, 0
	v_mov_b32_e32 v13, 0
	v_mov_b32_e32 v14, 0
	v_mov_b32_e32 v15, 0
	v_mov_b32_e32 v16, 0
	v_mov_b32_e32 v17, 0
	v_mov_b32_e32 v18, 0
	v_mov_b32_e32 v19, 0
	v_mov_b32_e32 v20, 0
	v_mov_b32_e32 v21, 0
	s_mov_b32 s98, 0
	s_barrier
	s_cbranch_scc1 .LBB0_107
	s_ashr_i32 s10, s76, 31
	s_lshr_b32 s10, s10, 22
	s_add_i32 s11, s76, s10
	s_ashr_i32 s10, s11, 10
	s_and_b32 s11, s11, 0xfffffc00
	s_sub_i32 s12, s76, s11
	s_ashr_i32 s11, s12, 31
	s_lshr_b32 s11, s11, 26
	s_add_i32 s11, s12, s11
	s_ashr_i32 s13, s11, 6
	s_ashr_i32 s11, s10, 31
	s_lshl_b64 s[10:11], s[10:11], 25
	v_lshl_add_u32 v4, s13, 7, v71
	s_add_u32 s10, s80, s10
	v_ashrrev_i32_e32 v5, 31, v4
	s_addc_u32 s11, s81, s11
	v_lshlrev_b64 v[4:5], 14, v[4:5]
	v_lshl_add_u64 v[4:5], s[10:11], 0, v[4:5]
	s_lshl_b32 s10, s13, 12
	s_lshl_b32 s11, s12, 6
	s_sub_i32 s10, s11, s10
	s_ashr_i32 s11, s10, 31
	v_lshl_add_u64 v[4:5], s[10:11], 2, v[4:5]
	v_mov_b32_e32 v67, 0
	v_lshl_add_u64 v[4:5], v[4:5], 0, v[66:67]
	s_movk_i32 s10, 0x4000
	v_add_co_u32_e32 v14, vcc, s10, v4
	s_mov_b32 s10, 0x8000
	s_nop 0
	v_addc_co_u32_e32 v15, vcc, 0, v5, vcc
	global_load_dwordx4 v[6:9], v[4:5], off nt
	global_load_dwordx4 v[10:13], v[14:15], off nt
	v_add_co_u32_e32 v14, vcc, s10, v4
	s_mov_b32 s10, 0xc000
	s_nop 0
	v_addc_co_u32_e32 v15, vcc, 0, v5, vcc
	v_add_co_u32_e32 v4, vcc, s10, v4
	s_nop 1
	v_addc_co_u32_e32 v5, vcc, 0, v5, vcc
	global_load_dwordx4 v[14:17], v[14:15], off nt
	s_nop 0
	global_load_dwordx4 v[18:21], v[4:5], off nt
	s_bitset1_b32 s98, 0
.LBB0_107:
	s_add_i32 s10, s6, s76
	s_cmp_ge_i32 s10, s7
	v_mov_b32_e32 v3, 0
	v_mov_b32_e32 v4, 0
	v_mov_b32_e32 v5, 0
	v_mov_b32_e32 v22, 0
	v_mov_b32_e32 v23, 0
	v_mov_b32_e32 v24, 0
	v_mov_b32_e32 v25, 0
	v_mov_b32_e32 v26, 0
	v_mov_b32_e32 v27, 0
	v_mov_b32_e32 v28, 0
	v_mov_b32_e32 v29, 0
	v_mov_b32_e32 v30, 0
	v_mov_b32_e32 v31, 0
	v_mov_b32_e32 v32, 0
	v_mov_b32_e32 v33, 0
	s_cbranch_scc1 .LBB0_109
	s_ashr_i32 s11, s10, 31
	s_lshr_b32 s11, s11, 22
	s_add_i32 s11, s10, s11
	s_ashr_i32 s12, s11, 10
	s_and_b32 s11, s11, 0xfffffc00
	s_sub_i32 s11, s10, s11
	s_ashr_i32 s13, s11, 31
	s_lshr_b32 s13, s13, 26
	s_add_i32 s13, s11, s13
	s_ashr_i32 s16, s13, 6
	s_ashr_i32 s13, s12, 31
	s_lshl_b64 s[12:13], s[12:13], 25
	v_lshl_add_u32 v2, s16, 7, v71
	s_add_u32 s12, s80, s12
	v_ashrrev_i32_e32 v3, 31, v2
	s_addc_u32 s13, s81, s13
	v_lshlrev_b64 v[2:3], 14, v[2:3]
	v_lshl_add_u64 v[2:3], s[12:13], 0, v[2:3]
	s_lshl_b32 s12, s16, 12
	s_lshl_b32 s11, s11, 6
	s_sub_i32 s12, s11, s12
	s_ashr_i32 s13, s12, 31
	v_lshl_add_u64 v[2:3], s[12:13], 2, v[2:3]
	v_mov_b32_e32 v67, 0
	v_lshl_add_u64 v[26:27], v[2:3], 0, v[66:67]
	s_movk_i32 s11, 0x4000
	v_add_co_u32_e32 v22, vcc, s11, v26
	s_mov_b32 s11, 0x8000
	s_nop 0
	v_addc_co_u32_e32 v23, vcc, 0, v27, vcc
	v_add_co_u32_e32 v28, vcc, s11, v26
	s_mov_b32 s11, 0xc000
	s_nop 0
	v_addc_co_u32_e32 v29, vcc, 0, v27, vcc
	v_add_co_u32_e32 v30, vcc, s11, v26
	global_load_dwordx4 v[2:5], v[26:27], off nt
	s_nop 0
	global_load_dwordx4 v[22:25], v[22:23], off nt
	v_addc_co_u32_e32 v31, vcc, 0, v27, vcc
	global_load_dwordx4 v[26:29], v[28:29], off nt
	s_nop 0
	global_load_dwordx4 v[30:33], v[30:31], off nt
	s_bitset1_b32 s98, 1
.LBB0_109:
	s_add_i32 s10, s10, s6
	s_cmp_ge_i32 s10, s7
	s_cbranch_scc1 .LBB0_111
	s_ashr_i32 s11, s10, 31
	s_lshr_b32 s11, s11, 22
	s_add_i32 s11, s10, s11
	s_ashr_i32 s12, s11, 10
	s_and_b32 s11, s11, 0xfffffc00
	s_sub_i32 s11, s10, s11
	s_ashr_i32 s13, s11, 31
	s_lshr_b32 s13, s13, 26
	s_add_i32 s13, s11, s13
	s_ashr_i32 s16, s13, 6
	s_ashr_i32 s13, s12, 31
	s_lshl_b64 s[12:13], s[12:13], 25
	v_lshl_add_u32 v34, s16, 7, v71
	s_add_u32 s12, s80, s12
	v_ashrrev_i32_e32 v35, 31, v34
	s_addc_u32 s13, s81, s13
	v_lshlrev_b64 v[34:35], 14, v[34:35]
	v_lshl_add_u64 v[34:35], s[12:13], 0, v[34:35]
	s_lshl_b32 s12, s16, 12
	s_lshl_b32 s11, s11, 6
	s_sub_i32 s12, s11, s12
	s_ashr_i32 s13, s12, 31
	v_lshl_add_u64 v[34:35], s[12:13], 2, v[34:35]
	v_mov_b32_e32 v67, 0
	v_lshl_add_u64 v[42:43], v[34:35], 0, v[66:67]
	s_movk_i32 s11, 0x4000
	v_add_co_u32_e32 v38, vcc, s11, v42
	s_nop 1
	v_addc_co_u32_e32 v39, vcc, 0, v43, vcc
	v_add_co_u32_e32 v44, vcc, 0x8000, v42
	global_load_dwordx4 v[34:37], v[42:43], off nt
	s_nop 0
	global_load_dwordx4 v[38:41], v[38:39], off nt
	v_addc_co_u32_e32 v45, vcc, 0, v43, vcc
	v_add_co_u32_e32 v46, vcc, 0xc000, v42
	s_nop 1
	v_addc_co_u32_e32 v47, vcc, 0, v43, vcc
	global_load_dwordx4 v[42:45], v[44:45], off nt
	s_nop 0
	global_load_dwordx4 v[46:49], v[46:47], off nt
	s_bitset1_b32 s98, 2
.LBB0_111:
	s_add_i32 s10, s10, s6
	s_cmp_ge_i32 s10, s7
	s_cbranch_scc1 .LBB0_113
	s_ashr_i32 s11, s10, 31
	s_lshr_b32 s11, s11, 22
	s_add_i32 s11, s10, s11
	s_ashr_i32 s12, s11, 10
	s_and_b32 s11, s11, 0xfffffc00
	s_sub_i32 s16, s10, s11
	s_ashr_i32 s10, s16, 31
	s_lshr_b32 s10, s10, 26
	s_add_i32 s10, s16, s10
	s_ashr_i32 s17, s10, 6
	s_ashr_i32 s13, s12, 31
	s_lshl_b64 s[10:11], s[12:13], 25
	v_lshl_add_u32 v50, s17, 7, v71
	s_add_u32 s10, s80, s10
	v_ashrrev_i32_e32 v51, 31, v50
	s_addc_u32 s11, s81, s11
	v_lshlrev_b64 v[50:51], 14, v[50:51]
	v_lshl_add_u64 v[50:51], s[10:11], 0, v[50:51]
	s_lshl_b32 s10, s17, 12
	s_lshl_b32 s11, s16, 6
	s_sub_i32 s10, s11, s10
	s_ashr_i32 s11, s10, 31
	v_lshl_add_u64 v[50:51], s[10:11], 2, v[50:51]
	v_mov_b32_e32 v67, 0
	v_lshl_add_u64 v[58:59], v[50:51], 0, v[66:67]
	s_movk_i32 s10, 0x4000
	v_add_co_u32_e32 v60, vcc, s10, v58
	s_nop 1
	v_addc_co_u32_e32 v61, vcc, 0, v59, vcc
	global_load_dwordx4 v[50:53], v[58:59], off nt
	global_load_dwordx4 v[54:57], v[60:61], off nt
	v_add_co_u32_e32 v60, vcc, 0x8000, v58
	s_nop 1
	v_addc_co_u32_e32 v61, vcc, 0, v59, vcc
	v_add_co_u32_e32 v62, vcc, 0xc000, v58
	s_nop 1
	v_addc_co_u32_e32 v63, vcc, 0, v59, vcc
	global_load_dwordx4 v[58:61], v[60:61], off nt
	s_nop 0
	global_load_dwordx4 v[62:65], v[62:63], off nt
	s_bitset1_b32 s98, 3
	s_andn2_b64 vcc, exec, s[4:5]
	s_cbranch_vccnz .LBB0_128
	s_branch .LBB0_114

.LBB0_117:
	s_waitcnt vmcnt(12)
	s_cmp_eq_u32 s98, 15
	s_cbranch_scc1 .Lcvw_1
	s_waitcnt vmcnt(0)
.Lcvw_1:
	s_bitset0_b32 s98, 0
	s_ashr_i32 s4, s38, 31
	s_lshr_b32 s4, s4, 22
	v_mul_f32_e32 v68, 0x42800000, v6
	v_mul_f32_e32 v75, 0x42800000, v10
	v_mov_b32_e32 v78, 0
	s_add_i32 s5, s38, s4
	v_cvt_pk_fp8_f32 v78, v68, v75
	v_mul_f32_e32 v68, 0x42800000, v7
	v_mul_f32_e32 v75, 0x42800000, v11
	v_mov_b32_e32 v79, 0
	s_ashr_i32 s4, s5, 10
	s_and_b32 s5, s5, 0xfffffc00
	v_cvt_pk_fp8_f32 v79, v68, v75
	s_sub_i32 s5, s38, s5
	s_ashr_i32 s39, s5, 31
	s_lshr_b32 s39, s39, 26
	v_mul_f32_e32 v68, 0x42800000, v15
	v_mul_f32_e32 v75, 0x42800000, v19
	s_add_i32 s5, s5, s39
	v_cvt_pk_fp8_f32 v79, v68, v75 op_sel:[0,0,1]
	v_mul_f32_e32 v68, 0x42800000, v8
	v_mul_f32_e32 v75, 0x42800000, v12
	v_mov_b32_e32 v80, 0
	s_ashr_i32 s39, s5, 6
	s_ashr_i32 s5, s4, 31
	v_cvt_pk_fp8_f32 v80, v68, v75
	v_mul_f32_e32 v68, 0x42800000, v9
	v_mul_f32_e32 v75, 0x42800000, v13
	v_mov_b32_e32 v81, 0
	s_lshl_b64 s[40:41], s[4:5], 23
	v_cvt_pk_fp8_f32 v81, v68, v75
	s_add_u32 s40, s74, s40
	s_addc_u32 s41, s75, s41
	s_lshl_b32 s5, s39, 9
	s_lshl_b32 s4, s4, 13
	v_mul_f32_e32 v76, 0x42800000, v14
	v_mul_f32_e32 v77, 0x42800000, v18
	s_add_i32 s5, s5, s4
	v_cvt_pk_fp8_f32 v78, v76, v77 op_sel:[0,0,1]
	v_mul_f32_e32 v76, 0x42800000, v16
	v_mul_f32_e32 v77, 0x42800000, v20
	v_mul_f32_e32 v68, 0x42800000, v17
	v_mul_f32_e32 v75, 0x42800000, v21
	s_sub_i32 s4, s16, s5
	v_cvt_pk_fp8_f32 v80, v76, v77 op_sel:[0,0,1]
	v_cvt_pk_fp8_f32 v81, v68, v75 op_sel:[0,0,1]
	s_and_b32 s4, s4, -16
	s_add_i32 s4, s4, s39
	s_ashr_i32 s5, s4, 31
	ds_write2_b32 v73, v78, v79 offset1:33
	ds_write2_b32 v73, v80, v81 offset0:66 offset1:99
	s_waitcnt lgkmcnt(0)
	s_barrier
	ds_read2_b32 v[76:77], v74 offset1:1
	ds_read2_b32 v[78:79], v74 offset0:2 offset1:3
	s_and_b32 s39, s11, 64
	s_lshl_b64 s[4:5], s[4:5], 14
	s_add_u32 s4, s40, s4
	v_add_lshl_u32 v68, s39, v72, 7
	s_addc_u32 s5, s41, s5
	v_lshl_add_u64 v[80:81], s[4:5], 0, v[68:69]
	s_add_i32 s4, s10, s38
	v_lshl_add_u64 v[80:81], v[80:81], 0, v[66:67]
	s_cmp_ge_i32 s4, s7
	s_waitcnt lgkmcnt(0)
	global_store_dwordx4 v[80:81], v[76:79], off nt
	s_cbranch_scc1 .LBB0_119
	s_ashr_i32 s5, s4, 31
	s_lshr_b32 s5, s5, 22
	s_add_i32 s5, s4, s5
	s_ashr_i32 s40, s5, 10
	s_and_b32 s5, s5, 0xfffffc00
	s_sub_i32 s4, s4, s5
	s_ashr_i32 s5, s4, 31
	s_lshr_b32 s5, s5, 26
	s_add_i32 s4, s4, s5
	s_ashr_i32 s39, s4, 6
	s_ashr_i32 s41, s40, 31
	s_lshl_b64 s[4:5], s[40:41], 25
	v_lshl_add_u32 v6, s39, 7, v71
	s_add_u32 s4, s80, s4
	v_ashrrev_i32_e32 v7, 31, v6
	s_addc_u32 s5, s81, s5
	v_lshlrev_b64 v[6:7], 14, v[6:7]
	v_lshl_add_u64 v[6:7], s[4:5], 0, v[6:7]
	s_lshl_b32 s4, s39, 12
	s_lshl_b32 s5, s40, 16
	s_add_i32 s4, s4, s5
	s_add_i32 s5, s12, s11
	s_sub_i32 s4, s5, s4
	s_ashr_i32 s5, s4, 31
	v_lshl_add_u64 v[6:7], s[4:5], 2, v[6:7]
	v_lshlrev_b32_e32 v68, 2, v70
	v_lshl_add_u64 v[14:15], v[6:7], 0, v[68:69]
	v_add_co_u32_e32 v10, vcc, s35, v14
	s_nop 1
	v_addc_co_u32_e32 v11, vcc, 0, v15, vcc
	v_add_co_u32_e32 v16, vcc, s36, v14
	global_load_dwordx4 v[6:9], v[14:15], off nt
	s_nop 0
	global_load_dwordx4 v[10:13], v[10:11], off nt
	v_addc_co_u32_e32 v17, vcc, 0, v15, vcc
	v_add_co_u32_e32 v18, vcc, s37, v14
	s_nop 1
	v_addc_co_u32_e32 v19, vcc, 0, v15, vcc
	global_load_dwordx4 v[14:17], v[16:17], off nt
	s_nop 0
	global_load_dwordx4 v[18:21], v[18:19], off nt
	s_bitset1_b32 s98, 0
.LBB0_119:
	s_add_i32 s39, s38, s6
	s_cmp_ge_i32 s39, s7
	s_mov_b64 s[4:5], -1
	s_cbranch_scc1 .LBB0_116
	s_waitcnt vmcnt(12)
	s_cmp_eq_u32 s98, 15
	s_cbranch_scc1 .Lcvw_2
	s_waitcnt vmcnt(0)
.Lcvw_2:
	s_bitset0_b32 s98, 1
	s_ashr_i32 s4, s39, 31
	s_lshr_b32 s4, s4, 22
	v_mul_f32_e32 v68, 0x42800000, v2
	v_mul_f32_e32 v75, 0x42800000, v22
	v_mov_b32_e32 v78, v69
	s_add_i32 s5, s39, s4
	v_cvt_pk_fp8_f32 v78, v68, v75
	v_mul_f32_e32 v68, 0x42800000, v3
	v_mul_f32_e32 v75, 0x42800000, v23
	v_mov_b32_e32 v79, v69
	s_ashr_i32 s4, s5, 10
	s_and_b32 s5, s5, 0xfffffc00
	v_cvt_pk_fp8_f32 v79, v68, v75
	s_sub_i32 s5, s39, s5
	s_ashr_i32 s40, s5, 31
	s_lshr_b32 s40, s40, 26
	v_mul_f32_e32 v68, 0x42800000, v27
	v_mul_f32_e32 v75, 0x42800000, v31
	s_add_i32 s5, s5, s40
	v_cvt_pk_fp8_f32 v79, v68, v75 op_sel:[0,0,1]
	v_mul_f32_e32 v68, 0x42800000, v4
	v_mul_f32_e32 v75, 0x42800000, v24
	v_mov_b32_e32 v80, v69
	s_ashr_i32 s42, s5, 6
	s_ashr_i32 s5, s4, 31
	v_cvt_pk_fp8_f32 v80, v68, v75
	v_mul_f32_e32 v68, 0x42800000, v5
	v_mul_f32_e32 v75, 0x42800000, v25
	v_mov_b32_e32 v81, v69
	s_lshl_b64 s[40:41], s[4:5], 23
	v_cvt_pk_fp8_f32 v81, v68, v75
	s_add_u32 s40, s74, s40
	s_addc_u32 s41, s75, s41
	s_lshl_b32 s5, s42, 9
	s_lshl_b32 s4, s4, 13
	v_mul_f32_e32 v76, 0x42800000, v26
	v_mul_f32_e32 v77, 0x42800000, v30
	s_add_i32 s5, s5, s4
	s_add_i32 s4, s13, s16
	v_cvt_pk_fp8_f32 v78, v76, v77 op_sel:[0,0,1]
	v_mul_f32_e32 v76, 0x42800000, v28
	v_mul_f32_e32 v77, 0x42800000, v32
	v_mul_f32_e32 v68, 0x42800000, v29
	v_mul_f32_e32 v75, 0x42800000, v33
	s_sub_i32 s4, s4, s5
	v_cvt_pk_fp8_f32 v80, v76, v77 op_sel:[0,0,1]
	v_cvt_pk_fp8_f32 v81, v68, v75 op_sel:[0,0,1]
	s_and_b32 s4, s4, -16
	s_add_i32 s4, s4, s42
	v_add_u32_e32 v75, 0x2000, v73
	v_add_u32_e32 v76, 0x2200, v74
	s_ashr_i32 s5, s4, 31
	s_add_i32 s42, s18, s11
	ds_write2_b32 v75, v78, v79 offset0:128 offset1:161
	ds_write2_b32 v75, v80, v81 offset0:194 offset1:227
	s_waitcnt lgkmcnt(0)
	s_barrier
	v_add_u32_e32 v77, 0x2208, v74
	ds_read2_b32 v[78:79], v76 offset1:1
	ds_read2_b32 v[80:81], v77 offset1:1
	s_and_b32 s42, s42, 64
	s_lshl_b64 s[4:5], s[4:5], 14
	s_add_u32 s4, s40, s4
	v_add_lshl_u32 v68, s42, v72, 7
	s_addc_u32 s5, s41, s5
	v_lshl_add_u64 v[82:83], s[4:5], 0, v[68:69]
	s_add_i32 s4, s19, s38
	v_lshl_add_u64 v[82:83], v[82:83], 0, v[66:67]
	s_cmp_ge_i32 s4, s7
	s_waitcnt lgkmcnt(0)
	global_store_dwordx4 v[82:83], v[78:81], off nt
	s_cbranch_scc1 .LBB0_122
	s_ashr_i32 s5, s4, 31
	s_lshr_b32 s5, s5, 22
	s_add_i32 s5, s4, s5
	s_ashr_i32 s40, s5, 10
	s_and_b32 s5, s5, 0xfffffc00
	s_sub_i32 s4, s4, s5
	s_ashr_i32 s5, s4, 31
	s_lshr_b32 s5, s5, 26
	s_add_i32 s4, s4, s5
	s_ashr_i32 s42, s4, 6
	s_ashr_i32 s41, s40, 31
	s_lshl_b64 s[4:5], s[40:41], 25
	v_lshl_add_u32 v2, s42, 7, v71
	s_add_u32 s4, s80, s4
	v_ashrrev_i32_e32 v3, 31, v2
	s_addc_u32 s5, s81, s5
	v_lshlrev_b64 v[2:3], 14, v[2:3]
	v_lshl_add_u64 v[2:3], s[4:5], 0, v[2:3]
	s_lshl_b32 s4, s42, 12
	s_lshl_b32 s5, s40, 16
	s_add_i32 s4, s4, s5
	s_add_i32 s5, s20, s11
	s_sub_i32 s4, s5, s4
	s_ashr_i32 s5, s4, 31
	v_lshl_add_u64 v[2:3], s[4:5], 2, v[2:3]
	v_lshlrev_b32_e32 v68, 2, v70
	v_lshl_add_u64 v[26:27], v[2:3], 0, v[68:69]
	v_add_co_u32_e32 v22, vcc, s35, v26
	s_nop 1
	v_addc_co_u32_e32 v23, vcc, 0, v27, vcc
	v_add_co_u32_e32 v28, vcc, s36, v26
	global_load_dwordx4 v[2:5], v[26:27], off nt
	s_nop 0
	global_load_dwordx4 v[22:25], v[22:23], off nt
	v_addc_co_u32_e32 v29, vcc, 0, v27, vcc
	v_add_co_u32_e32 v30, vcc, s37, v26
	s_nop 1
	v_addc_co_u32_e32 v31, vcc, 0, v27, vcc
	global_load_dwordx4 v[26:29], v[28:29], off nt
	s_nop 0
	global_load_dwordx4 v[30:33], v[30:31], off nt
	s_bitset1_b32 s98, 1
.LBB0_122:
	s_add_i32 s40, s21, s38
	s_cmp_ge_i32 s40, s7
	s_mov_b64 s[4:5], -1
	s_cbranch_scc1 .LBB0_116
	s_waitcnt vmcnt(12)
	s_cmp_eq_u32 s98, 15
	s_cbranch_scc1 .Lcvw_3
	s_waitcnt vmcnt(0)
.Lcvw_3:
	s_bitset0_b32 s98, 2
	s_ashr_i32 s4, s40, 31
	s_lshr_b32 s4, s4, 22
	v_mul_f32_e32 v68, 0x42800000, v34
	v_mul_f32_e32 v78, 0x42800000, v38
	v_mov_b32_e32 v81, v69
	s_add_i32 s5, s40, s4
	v_cvt_pk_fp8_f32 v81, v68, v78
	v_mul_f32_e32 v68, 0x42800000, v35
	v_mul_f32_e32 v78, 0x42800000, v39
	v_mov_b32_e32 v82, v69
	s_ashr_i32 s4, s5, 10
	s_and_b32 s5, s5, 0xfffffc00
	v_cvt_pk_fp8_f32 v82, v68, v78
	s_sub_i32 s5, s40, s5
	s_ashr_i32 s40, s5, 31
	s_lshr_b32 s40, s40, 26
	v_mul_f32_e32 v68, 0x42800000, v43
	v_mul_f32_e32 v78, 0x42800000, v47
	s_add_i32 s5, s5, s40
	v_cvt_pk_fp8_f32 v82, v68, v78 op_sel:[0,0,1]
	v_mul_f32_e32 v68, 0x42800000, v36
	v_mul_f32_e32 v78, 0x42800000, v40
	v_mov_b32_e32 v83, v69
	s_ashr_i32 s42, s5, 6
	s_ashr_i32 s5, s4, 31
	v_cvt_pk_fp8_f32 v83, v68, v78
	v_mul_f32_e32 v68, 0x42800000, v37
	v_mul_f32_e32 v78, 0x42800000, v41
	v_mov_b32_e32 v84, v69
	s_lshl_b64 s[40:41], s[4:5], 23
	v_cvt_pk_fp8_f32 v84, v68, v78
	s_add_u32 s40, s74, s40
	s_addc_u32 s41, s75, s41
	s_lshl_b32 s5, s42, 9
	s_lshl_b32 s4, s4, 13
	v_mul_f32_e32 v79, 0x42800000, v42
	v_mul_f32_e32 v80, 0x42800000, v46
	s_add_i32 s5, s5, s4
	s_add_i32 s4, s24, s16
	v_cvt_pk_fp8_f32 v81, v79, v80 op_sel:[0,0,1]
	v_mul_f32_e32 v79, 0x42800000, v44
	v_mul_f32_e32 v80, 0x42800000, v48
	v_mul_f32_e32 v68, 0x42800000, v45
	v_mul_f32_e32 v78, 0x42800000, v49
	s_sub_i32 s4, s4, s5
	v_cvt_pk_fp8_f32 v83, v79, v80 op_sel:[0,0,1]
	v_cvt_pk_fp8_f32 v84, v68, v78 op_sel:[0,0,1]
	s_and_b32 s4, s4, -16
	s_add_i32 s4, s4, s42
	s_ashr_i32 s5, s4, 31
	s_add_i32 s42, s25, s11
	ds_write2_b32 v73, v81, v82 offset1:33
	ds_write2_b32 v73, v83, v84 offset0:66 offset1:99
	s_waitcnt lgkmcnt(0)
	s_barrier
	ds_read2_b32 v[78:79], v74 offset1:1
	ds_read2_b32 v[80:81], v74 offset0:2 offset1:3
	s_and_b32 s42, s42, 64
	s_lshl_b64 s[4:5], s[4:5], 14
	s_add_u32 s4, s40, s4
	v_add_lshl_u32 v68, s42, v72, 7
	s_addc_u32 s5, s41, s5
	v_lshl_add_u64 v[82:83], s[4:5], 0, v[68:69]
	s_add_i32 s4, s26, s38
	v_lshl_add_u64 v[82:83], v[82:83], 0, v[66:67]
	s_cmp_ge_i32 s4, s7
	s_waitcnt lgkmcnt(0)
	global_store_dwordx4 v[82:83], v[78:81], off nt
	s_cbranch_scc1 .LBB0_125
	s_ashr_i32 s5, s4, 31
	s_lshr_b32 s5, s5, 22
	s_add_i32 s5, s4, s5
	s_ashr_i32 s40, s5, 10
	s_and_b32 s5, s5, 0xfffffc00
	s_sub_i32 s4, s4, s5
	s_ashr_i32 s5, s4, 31
	s_lshr_b32 s5, s5, 26
	s_add_i32 s4, s4, s5
	s_ashr_i32 s42, s4, 6
	s_ashr_i32 s41, s40, 31
	s_lshl_b64 s[4:5], s[40:41], 25
	v_lshl_add_u32 v34, s42, 7, v71
	s_add_u32 s4, s80, s4
	v_ashrrev_i32_e32 v35, 31, v34
	s_addc_u32 s5, s81, s5
	v_lshlrev_b64 v[34:35], 14, v[34:35]
	v_lshl_add_u64 v[34:35], s[4:5], 0, v[34:35]
	s_lshl_b32 s4, s42, 12
	s_lshl_b32 s5, s40, 16
	s_add_i32 s4, s4, s5
	s_add_i32 s5, s27, s11
	s_sub_i32 s4, s5, s4
	s_ashr_i32 s5, s4, 31
	v_lshl_add_u64 v[34:35], s[4:5], 2, v[34:35]
	v_lshlrev_b32_e32 v68, 2, v70
	v_lshl_add_u64 v[42:43], v[34:35], 0, v[68:69]
	v_add_co_u32_e32 v38, vcc, 0x4000, v42
	s_nop 1
	v_addc_co_u32_e32 v39, vcc, 0, v43, vcc
	v_add_co_u32_e32 v44, vcc, 0x8000, v42
	global_load_dwordx4 v[34:37], v[42:43], off nt
	s_nop 0
	global_load_dwordx4 v[38:41], v[38:39], off nt
	v_addc_co_u32_e32 v45, vcc, 0, v43, vcc
	v_add_co_u32_e32 v46, vcc, 0xc000, v42
	s_nop 1
	v_addc_co_u32_e32 v47, vcc, 0, v43, vcc
	global_load_dwordx4 v[42:45], v[44:45], off nt
	s_nop 0
	global_load_dwordx4 v[46:49], v[46:47], off nt
	s_bitset1_b32 s98, 2
.LBB0_125:
	s_add_i32 s40, s28, s38
	s_cmp_ge_i32 s40, s7
	s_mov_b64 s[4:5], -1
	s_cbranch_scc1 .LBB0_116
	s_waitcnt vmcnt(12)
	s_cmp_eq_u32 s98, 15
	s_cbranch_scc1 .Lcvw_4
	s_waitcnt vmcnt(0)
.Lcvw_4:
	s_bitset0_b32 s98, 3
	s_ashr_i32 s4, s40, 31
	s_lshr_b32 s4, s4, 22
	v_mul_f32_e32 v68, 0x42800000, v50
	v_mul_f32_e32 v78, 0x42800000, v54
	v_mov_b32_e32 v81, v69
	s_add_i32 s5, s40, s4
	v_cvt_pk_fp8_f32 v81, v68, v78
	v_mul_f32_e32 v68, 0x42800000, v51
	v_mul_f32_e32 v78, 0x42800000, v55
	v_mov_b32_e32 v82, v69
	s_ashr_i32 s4, s5, 10
	s_and_b32 s5, s5, 0xfffffc00
	v_cvt_pk_fp8_f32 v82, v68, v78
	s_sub_i32 s5, s40, s5
	s_ashr_i32 s40, s5, 31
	s_lshr_b32 s40, s40, 26
	v_mul_f32_e32 v68, 0x42800000, v59
	v_mul_f32_e32 v78, 0x42800000, v63
	s_add_i32 s5, s5, s40
	v_cvt_pk_fp8_f32 v82, v68, v78 op_sel:[0,0,1]
	v_mul_f32_e32 v68, 0x42800000, v52
	v_mul_f32_e32 v78, 0x42800000, v56
	v_mov_b32_e32 v83, v69
	s_ashr_i32 s42, s5, 6
	s_ashr_i32 s5, s4, 31
	v_cvt_pk_fp8_f32 v83, v68, v78
	v_mul_f32_e32 v68, 0x42800000, v53
	v_mul_f32_e32 v78, 0x42800000, v57
	v_mov_b32_e32 v84, v69
	s_lshl_b64 s[40:41], s[4:5], 23
	v_cvt_pk_fp8_f32 v84, v68, v78
	s_add_u32 s40, s74, s40
	s_addc_u32 s41, s75, s41
	s_lshl_b32 s5, s42, 9
	s_lshl_b32 s4, s4, 13
	v_mul_f32_e32 v79, 0x42800000, v58
	v_mul_f32_e32 v80, 0x42800000, v62
	s_add_i32 s5, s5, s4
	s_add_i32 s4, s29, s16
	v_cvt_pk_fp8_f32 v81, v79, v80 op_sel:[0,0,1]
	v_mul_f32_e32 v79, 0x42800000, v60
	v_mul_f32_e32 v80, 0x42800000, v64
	v_mul_f32_e32 v68, 0x42800000, v61
	v_mul_f32_e32 v78, 0x42800000, v65
	s_sub_i32 s4, s4, s5
	v_cvt_pk_fp8_f32 v83, v79, v80 op_sel:[0,0,1]
	v_cvt_pk_fp8_f32 v84, v68, v78 op_sel:[0,0,1]
	s_and_b32 s4, s4, -16
	s_add_i32 s4, s4, s42
	s_ashr_i32 s5, s4, 31
	s_add_i32 s42, s30, s11
	ds_write2_b32 v75, v81, v82 offset0:128 offset1:161
	ds_write2_b32 v75, v83, v84 offset0:194 offset1:227
	s_waitcnt lgkmcnt(0)
	s_barrier
	ds_read2_b32 v[78:79], v76 offset1:1
	ds_read2_b32 v[80:81], v77 offset1:1
	s_and_b32 s42, s42, 64
	s_lshl_b64 s[4:5], s[4:5], 14
	s_add_u32 s4, s40, s4
	v_add_lshl_u32 v68, s42, v72, 7
	s_addc_u32 s5, s41, s5
	v_lshl_add_u64 v[76:77], s[4:5], 0, v[68:69]
	s_add_i32 s4, s31, s38
	v_lshl_add_u64 v[76:77], v[76:77], 0, v[66:67]
	s_cmp_ge_i32 s4, s7
	s_waitcnt lgkmcnt(0)
	global_store_dwordx4 v[76:77], v[78:81], off nt
	s_cbranch_scc1 .LBB0_115
	s_ashr_i32 s5, s4, 31
	s_lshr_b32 s5, s5, 22
	s_add_i32 s5, s4, s5
	s_ashr_i32 s40, s5, 10
	s_and_b32 s5, s5, 0xfffffc00
	s_sub_i32 s4, s4, s5
	s_ashr_i32 s5, s4, 31
	s_lshr_b32 s5, s5, 26
	s_add_i32 s4, s4, s5
	s_ashr_i32 s38, s4, 6
	s_ashr_i32 s41, s40, 31
	s_lshl_b64 s[4:5], s[40:41], 25
	v_lshl_add_u32 v50, s38, 7, v71
	s_add_u32 s4, s80, s4
	v_ashrrev_i32_e32 v51, 31, v50
	s_addc_u32 s5, s81, s5
	v_lshlrev_b64 v[50:51], 14, v[50:51]
	v_lshl_add_u64 v[50:51], s[4:5], 0, v[50:51]
	s_lshl_b32 s4, s38, 12
	s_lshl_b32 s5, s40, 16
	s_add_i32 s4, s4, s5
	s_add_i32 s5, s34, s11
	s_sub_i32 s4, s5, s4
	s_ashr_i32 s5, s4, 31
	v_lshl_add_u64 v[50:51], s[4:5], 2, v[50:51]
	v_lshlrev_b32_e32 v68, 2, v70
	v_lshl_add_u64 v[58:59], v[50:51], 0, v[68:69]
	v_add_co_u32_e32 v54, vcc, 0x4000, v58
	s_nop 1
	v_addc_co_u32_e32 v55, vcc, 0, v59, vcc
	v_add_co_u32_e32 v60, vcc, 0x8000, v58
	global_load_dwordx4 v[50:53], v[58:59], off nt
	s_nop 0
	global_load_dwordx4 v[54:57], v[54:55], off nt
	v_addc_co_u32_e32 v61, vcc, 0, v59, vcc
	v_add_co_u32_e32 v62, vcc, 0xc000, v58
	s_nop 1
	v_addc_co_u32_e32 v63, vcc, 0, v59, vcc
	global_load_dwordx4 v[58:61], v[60:61], off nt
	s_nop 0
	global_load_dwordx4 v[62:65], v[62:63], off nt
	s_bitset1_b32 s98, 3
	s_branch .LBB0_115

.LBB0_230:
	s_cmp_lt_i32 s29, s19
	s_cselect_b32 s10, 4, 2
	s_and_b64 s[2:3], s[2:3], exec
	s_cselect_b32 s2, 8, s10
	s_ashr_i32 s3, s12, 31
	s_lshr_b32 s3, s3, 22
	s_add_i32 s3, s12, s3
	s_ashr_i32 s10, s3, 10
	s_and_b32 s3, s3, 0xfffffc00
	s_sub_i32 s3, s12, s3
	s_ashr_i32 s11, s3, 31
	s_lshr_b32 s11, s11, 26
	s_add_i32 s11, s3, s11
	s_ashr_i32 s29, s11, 6
	s_ashr_i32 s11, s10, 31
	s_lshl_b64 s[10:11], s[10:11], 25
	v_lshl_add_u32 v2, s29, 7, v73
	s_add_u32 s10, s80, s10
	v_ashrrev_i32_e32 v3, 31, v2
	s_addc_u32 s11, s81, s11
	v_lshlrev_b64 v[2:3], 14, v[2:3]
	v_lshl_add_u64 v[2:3], s[10:11], 0, v[2:3]
	s_lshl_b32 s10, s29, 12
	s_lshl_b32 s3, s3, 6
	s_sub_i32 s10, s3, s10
	s_ashr_i32 s11, s10, 31
	v_lshl_add_u64 v[2:3], s[10:11], 2, v[2:3]
	v_mov_b32_e32 v71, v67
	s_waitcnt vmcnt(1)
	v_lshl_add_u64 v[10:11], v[2:3], 0, v[70:71]
	v_add_co_u32_e32 v6, vcc, s26, v10
	s_nop 1
	v_addc_co_u32_e32 v7, vcc, 0, v11, vcc
	v_add_co_u32_e32 v12, vcc, 0x8000, v10
	s_mov_b32 s98, 0
	s_barrier
	s_nop 0
	v_addc_co_u32_e32 v13, vcc, 0, v11, vcc
	s_waitcnt vmcnt(0)
	v_add_co_u32_e32 v14, vcc, 0xc000, v10
	s_nop 1
	v_addc_co_u32_e32 v15, vcc, 0, v11, vcc
	global_load_dwordx4 v[2:5], v[10:11], off nt
	s_nop 0
	global_load_dwordx4 v[6:9], v[6:7], off nt
	s_nop 0
	global_load_dwordx4 v[10:13], v[12:13], off nt
	s_nop 0
	global_load_dwordx4 v[14:17], v[14:15], off nt
	s_bitset1_b32 s98, 0
	s_add_i32 s3, s12, 1
	v_mov_b32_e32 v18, 0
	s_cmp_le_i32 s97, s3
	v_mov_b32_e32 v19, v18
	v_mov_b32_e32 v20, v18
	v_mov_b32_e32 v21, v18
	v_mov_b32_e32 v22, v18
	v_mov_b32_e32 v23, v18
	v_mov_b32_e32 v24, v18
	v_mov_b32_e32 v25, v18
	v_mov_b32_e32 v26, v18
	v_mov_b32_e32 v27, v18
	v_mov_b32_e32 v28, v18
	v_mov_b32_e32 v29, v18
	v_mov_b32_e32 v30, v18
	v_mov_b32_e32 v31, v18
	v_mov_b32_e32 v32, v18
	v_mov_b32_e32 v33, v18
	s_cbranch_scc1 .LBB0_232
	s_ashr_i32 s10, s3, 31
	s_lshr_b32 s10, s10, 22
	s_add_i32 s11, s3, s10
	s_ashr_i32 s10, s11, 10
	s_and_b32 s11, s11, 0xfffffc00
	s_sub_i32 s3, s3, s11
	s_ashr_i32 s11, s3, 31
	s_lshr_b32 s11, s11, 26
	s_add_i32 s11, s3, s11
	s_ashr_i32 s29, s11, 6
	s_ashr_i32 s11, s10, 31
	s_lshl_b64 s[10:11], s[10:11], 25
	v_lshl_add_u32 v18, s29, 7, v73
	s_add_u32 s10, s80, s10
	v_ashrrev_i32_e32 v19, 31, v18
	s_addc_u32 s11, s81, s11
	v_lshlrev_b64 v[18:19], 14, v[18:19]
	v_lshl_add_u64 v[18:19], s[10:11], 0, v[18:19]
	s_lshl_b32 s10, s29, 12
	s_lshl_b32 s3, s3, 6
	s_sub_i32 s10, s3, s10
	s_ashr_i32 s11, s10, 31
	v_lshl_add_u64 v[18:19], s[10:11], 2, v[18:19]
	v_lshl_add_u64 v[26:27], v[18:19], 0, v[70:71]
	v_add_co_u32_e32 v22, vcc, s26, v26
	s_nop 1
	v_addc_co_u32_e32 v23, vcc, 0, v27, vcc
	v_add_co_u32_e32 v28, vcc, s27, v26
	global_load_dwordx4 v[18:21], v[26:27], off nt
	s_nop 0
	global_load_dwordx4 v[22:25], v[22:23], off nt
	v_addc_co_u32_e32 v29, vcc, 0, v27, vcc
	v_add_co_u32_e32 v30, vcc, s28, v26
	s_nop 1
	v_addc_co_u32_e32 v31, vcc, 0, v27, vcc
	global_load_dwordx4 v[26:29], v[28:29], off nt
	s_nop 0
	global_load_dwordx4 v[30:33], v[30:31], off nt
	s_bitset1_b32 s98, 1
.LBB0_232:
	s_add_i32 s2, s12, s2
	s_min_i32 s10, s2, s97
	s_add_i32 s2, s12, 2
	s_cmp_ge_i32 s2, s10
	s_cbranch_scc1 .LBB0_234
	s_ashr_i32 s3, s2, 31
	s_lshr_b32 s3, s3, 22
	s_add_i32 s3, s2, s3
	s_ashr_i32 s30, s3, 10
	s_and_b32 s3, s3, 0xfffffc00
	s_sub_i32 s11, s2, s3
	s_ashr_i32 s2, s11, 31
	s_lshr_b32 s2, s2, 26
	s_add_i32 s2, s11, s2
	s_ashr_i32 s29, s2, 6
	s_ashr_i32 s31, s30, 31
	s_lshl_b64 s[2:3], s[30:31], 25
	v_lshl_add_u32 v34, s29, 7, v73
	s_add_u32 s2, s80, s2
	v_ashrrev_i32_e32 v35, 31, v34
	s_addc_u32 s3, s81, s3
	v_lshlrev_b64 v[34:35], 14, v[34:35]
	v_lshl_add_u64 v[34:35], s[2:3], 0, v[34:35]
	s_lshl_b32 s2, s29, 12
	s_lshl_b32 s3, s11, 6
	s_sub_i32 s2, s3, s2
	s_ashr_i32 s3, s2, 31
	v_lshl_add_u64 v[34:35], s[2:3], 2, v[34:35]
	v_mov_b32_e32 v71, v67
	v_lshl_add_u64 v[42:43], v[34:35], 0, v[70:71]
	v_add_co_u32_e32 v38, vcc, 0x4000, v42
	s_nop 1
	v_addc_co_u32_e32 v39, vcc, 0, v43, vcc
	v_add_co_u32_e32 v44, vcc, 0x8000, v42
	global_load_dwordx4 v[34:37], v[42:43], off nt
	s_nop 0
	global_load_dwordx4 v[38:41], v[38:39], off nt
	v_addc_co_u32_e32 v45, vcc, 0, v43, vcc
	v_add_co_u32_e32 v46, vcc, 0xc000, v42
	s_nop 1
	v_addc_co_u32_e32 v47, vcc, 0, v43, vcc
	global_load_dwordx4 v[42:45], v[44:45], off nt
	s_nop 0
	global_load_dwordx4 v[46:49], v[46:47], off nt
	s_bitset1_b32 s98, 2
.LBB0_234:
	s_add_i32 s2, s12, 3
	s_cmp_ge_i32 s2, s10
	s_cbranch_scc1 .LBB0_236
	s_ashr_i32 s3, s2, 31
	s_lshr_b32 s3, s3, 22
	s_add_i32 s3, s2, s3
	s_ashr_i32 s30, s3, 10
	s_and_b32 s3, s3, 0xfffffc00
	s_sub_i32 s11, s2, s3
	s_ashr_i32 s2, s11, 31
	s_lshr_b32 s2, s2, 26
	s_add_i32 s2, s11, s2
	s_ashr_i32 s12, s2, 6
	s_ashr_i32 s31, s30, 31
	s_lshl_b64 s[2:3], s[30:31], 25
	v_lshl_add_u32 v50, s12, 7, v73
	s_add_u32 s2, s80, s2
	v_ashrrev_i32_e32 v51, 31, v50
	s_addc_u32 s3, s81, s3
	v_lshlrev_b64 v[50:51], 14, v[50:51]
	v_lshl_add_u64 v[50:51], s[2:3], 0, v[50:51]
	s_lshl_b32 s2, s12, 12
	s_lshl_b32 s3, s11, 6
	s_sub_i32 s2, s3, s2
	s_ashr_i32 s3, s2, 31
	v_lshl_add_u64 v[50:51], s[2:3], 2, v[50:51]
	v_mov_b32_e32 v71, v67
	v_lshl_add_u64 v[58:59], v[50:51], 0, v[70:71]
	v_add_co_u32_e32 v54, vcc, 0x4000, v58
	s_nop 1
	v_addc_co_u32_e32 v55, vcc, 0, v59, vcc
	v_add_co_u32_e32 v60, vcc, 0x8000, v58
	global_load_dwordx4 v[50:53], v[58:59], off nt
	s_nop 0
	global_load_dwordx4 v[54:57], v[54:55], off nt
	v_addc_co_u32_e32 v61, vcc, 0, v59, vcc
	v_add_co_u32_e32 v62, vcc, 0xc000, v58
	s_nop 1
	v_addc_co_u32_e32 v63, vcc, 0, v59, vcc
	global_load_dwordx4 v[58:61], v[60:61], off nt
	s_nop 0
	global_load_dwordx4 v[62:65], v[62:63], off nt
	s_bitset1_b32 s98, 3

.Lcvw_5:
	s_bitset0_b32 s98, 0
	s_add_i32 s2, s12, -7
	s_ashr_i32 s3, s2, 31
	s_lshr_b32 s3, s3, 22
	s_add_i32 s3, s2, s3
	v_mul_f32_e32 v66, 0x42800000, v2
	v_mul_f32_e32 v71, 0x42800000, v6
	v_mov_b32_e32 v79, v67
	s_ashr_i32 s2, s3, 10
	s_and_b32 s3, s3, 0xfffffc00
	v_cvt_pk_fp8_f32 v79, v66, v71
	v_mul_f32_e32 v66, 0x42800000, v3
	v_mul_f32_e32 v71, 0x42800000, v7
	v_mov_b32_e32 v80, v67
	s_sub_i32 s3, s12, s3
	v_cvt_pk_fp8_f32 v80, v66, v71
	s_add_i32 s3, s3, -7
	s_ashr_i32 s29, s3, 31
	s_lshr_b32 s29, s29, 26
	v_mul_f32_e32 v66, 0x42800000, v11
	v_mul_f32_e32 v71, 0x42800000, v15
	s_add_i32 s3, s3, s29
	v_cvt_pk_fp8_f32 v80, v66, v71 op_sel:[0,0,1]
	v_mul_f32_e32 v66, 0x42800000, v4
	v_mul_f32_e32 v71, 0x42800000, v8
	v_mov_b32_e32 v81, v67
	s_ashr_i32 s29, s3, 6
	s_ashr_i32 s3, s2, 31
	v_cvt_pk_fp8_f32 v81, v66, v71
	v_mul_f32_e32 v66, 0x42800000, v5
	v_mul_f32_e32 v71, 0x42800000, v9
	v_mov_b32_e32 v82, v67
	s_lshl_b64 s[30:31], s[2:3], 23
	v_cvt_pk_fp8_f32 v82, v66, v71
	s_add_u32 s30, s74, s30
	s_addc_u32 s31, s75, s31
	s_lshl_b32 s3, s29, 9
	s_lshl_b32 s2, s2, 13
	v_mul_f32_e32 v77, 0x42800000, v10
	v_mul_f32_e32 v78, 0x42800000, v14
	s_add_i32 s3, s3, s2
	v_cvt_pk_fp8_f32 v79, v77, v78 op_sel:[0,0,1]
	v_mul_f32_e32 v77, 0x42800000, v12
	v_mul_f32_e32 v78, 0x42800000, v16
	v_mul_f32_e32 v66, 0x42800000, v13
	v_mul_f32_e32 v71, 0x42800000, v17
	s_sub_i32 s2, s13, s3
	v_cvt_pk_fp8_f32 v81, v77, v78 op_sel:[0,0,1]
	v_cvt_pk_fp8_f32 v82, v66, v71 op_sel:[0,0,1]
	s_and_b32 s2, s2, -16
	s_add_i32 s2, s2, s29
	v_add_u32_e32 v77, v75, v68
	s_ashr_i32 s3, s2, 31
	ds_write2_b32 v76, v79, v80 offset1:33
	ds_write2_b32 v76, v81, v82 offset0:66 offset1:99
	s_waitcnt lgkmcnt(0)
	s_barrier
	ds_read2_b32 v[78:79], v77 offset1:1
	ds_read2_b32 v[80:81], v77 offset0:2 offset1:3
	s_and_b32 s29, s11, 64
	s_lshl_b64 s[2:3], s[2:3], 14
	s_add_u32 s2, s30, s2
	v_add_lshl_u32 v66, s29, v72, 7
	s_addc_u32 s3, s31, s3
	v_lshl_add_u64 v[82:83], s[2:3], 0, v[66:67]
	s_add_i32 s29, s12, -3
	v_lshl_add_u64 v[82:83], v[82:83], 0, v[68:69]
	s_cmp_ge_i32 s29, s10
	s_waitcnt lgkmcnt(0)
	global_store_dwordx4 v[82:83], v[78:81], off nt
	s_cbranch_scc1 .LBB0_241
	s_ashr_i32 s2, s29, 31
	s_lshr_b32 s2, s2, 22
	s_add_i32 s3, s29, s2
	s_ashr_i32 s2, s3, 10
	s_and_b32 s3, s3, 0xfffffc00
	s_sub_i32 s3, s12, s3
	s_add_i32 s3, s3, -3
	s_ashr_i32 s30, s3, 31
	s_lshr_b32 s30, s30, 26
	s_add_i32 s3, s3, s30
	s_ashr_i32 s34, s3, 6
	s_ashr_i32 s3, s2, 31
	s_lshl_b64 s[30:31], s[2:3], 25
	s_add_u32 s30, s80, s30
	s_addc_u32 s31, s81, s31
	s_lshl_b32 s3, s34, 12
	s_lshl_b32 s2, s2, 16
	v_lshl_add_u32 v2, s34, 7, v73
	s_add_i32 s3, s3, s2
	v_ashrrev_i32_e32 v3, 31, v2
	s_sub_i32 s2, s11, s3
	v_lshlrev_b64 v[2:3], 14, v[2:3]
	s_addk_i32 s2, 0x100
	v_lshl_add_u64 v[2:3], s[30:31], 0, v[2:3]
	s_ashr_i32 s3, s2, 31
	v_lshl_add_u64 v[2:3], s[2:3], 2, v[2:3]
	v_mov_b32_e32 v71, v67
	v_lshl_add_u64 v[10:11], v[2:3], 0, v[70:71]
	v_add_co_u32_e32 v6, vcc, s26, v10
	s_nop 1
	v_addc_co_u32_e32 v7, vcc, 0, v11, vcc
	v_add_co_u32_e32 v12, vcc, s27, v10
	global_load_dwordx4 v[2:5], v[10:11], off nt
	s_nop 0
	global_load_dwordx4 v[6:9], v[6:7], off nt
	v_addc_co_u32_e32 v13, vcc, 0, v11, vcc
	v_add_co_u32_e32 v14, vcc, s28, v10
	s_nop 1
	v_addc_co_u32_e32 v15, vcc, 0, v11, vcc
	global_load_dwordx4 v[10:13], v[12:13], off nt
	s_nop 0
	global_load_dwordx4 v[14:17], v[14:15], off nt
	s_bitset1_b32 s98, 0
.LBB0_241:
	s_add_i32 s30, s12, -6
	s_cmp_ge_i32 s30, s10
	s_mov_b64 s[2:3], -1
	s_cbranch_scc1 .LBB0_238
	s_waitcnt vmcnt(12)
	s_cmp_eq_u32 s98, 15
	s_cbranch_scc1 .Lcvw_6
	s_waitcnt vmcnt(0)
.Lcvw_6:
	s_bitset0_b32 s98, 1
	s_ashr_i32 s2, s30, 31
	s_lshr_b32 s2, s2, 22
	s_add_i32 s30, s30, s2
	s_and_b32 s3, s30, 0xfffffc00
	v_mul_f32_e32 v71, 0x42800000, v18
	v_mul_f32_e32 v78, 0x42800000, v22
	v_mov_b32_e32 v81, v67
	s_sub_i32 s3, s12, s3
	v_cvt_pk_fp8_f32 v81, v71, v78
	v_mul_f32_e32 v71, 0x42800000, v19
	v_mul_f32_e32 v78, 0x42800000, v23
	v_mov_b32_e32 v82, v67
	s_add_i32 s3, s3, -6
	v_cvt_pk_fp8_f32 v82, v71, v78
	s_ashr_i32 s2, s30, 10
	s_ashr_i32 s30, s3, 31
	s_lshr_b32 s30, s30, 26
	s_add_i32 s3, s3, s30
	v_mul_f32_e32 v71, 0x42800000, v27
	v_mul_f32_e32 v78, 0x42800000, v31
	s_ashr_i32 s34, s3, 6
	s_ashr_i32 s3, s2, 31
	v_cvt_pk_fp8_f32 v82, v71, v78 op_sel:[0,0,1]
	v_mul_f32_e32 v71, 0x42800000, v20
	v_mul_f32_e32 v78, 0x42800000, v24
	v_mov_b32_e32 v83, v67
	s_lshl_b64 s[30:31], s[2:3], 23
	v_cvt_pk_fp8_f32 v83, v71, v78
	v_mul_f32_e32 v71, 0x42800000, v21
	v_mul_f32_e32 v78, 0x42800000, v25
	v_mov_b32_e32 v84, v67
	s_add_u32 s30, s74, s30
	v_cvt_pk_fp8_f32 v84, v71, v78
	s_addc_u32 s31, s75, s31
	s_lshl_b32 s3, s34, 9
	s_lshl_b32 s2, s2, 13
	s_add_i32 s3, s3, s2
	v_mul_f32_e32 v79, 0x42800000, v26
	v_mul_f32_e32 v80, 0x42800000, v30
	s_sub_i32 s2, s13, s3
	v_cvt_pk_fp8_f32 v81, v79, v80 op_sel:[0,0,1]
	v_mul_f32_e32 v79, 0x42800000, v28
	v_mul_f32_e32 v80, 0x42800000, v32
	v_mul_f32_e32 v71, 0x42800000, v29
	v_mul_f32_e32 v78, 0x42800000, v33
	s_add_i32 s2, s2, 8
	v_cvt_pk_fp8_f32 v83, v79, v80 op_sel:[0,0,1]
	v_cvt_pk_fp8_f32 v84, v71, v78 op_sel:[0,0,1]
	s_and_b32 s2, s2, -16
	s_add_i32 s2, s2, s34
	v_add_u32_e32 v78, 0x2000, v76
	v_add_u32_e32 v79, 0x2200, v77
	s_ashr_i32 s3, s2, 31
	s_add_i32 s34, s11, 64
	ds_write2_b32 v78, v81, v82 offset0:128 offset1:161
	ds_write2_b32 v78, v83, v84 offset0:194 offset1:227
	s_waitcnt lgkmcnt(0)
	s_barrier
	v_add_u32_e32 v80, 0x2208, v77
	ds_read2_b32 v[82:83], v79 offset1:1
	ds_read2_b32 v[84:85], v80 offset1:1
	s_and_b32 s34, s34, 64
	s_lshl_b64 s[2:3], s[2:3], 14
	s_add_u32 s2, s30, s2
	v_add_lshl_u32 v86, s34, v72, 7
	v_mov_b32_e32 v87, v67
	s_addc_u32 s3, s31, s3
	v_lshl_add_u64 v[86:87], s[2:3], 0, v[86:87]
	s_add_i32 s2, s12, -2
	v_lshl_add_u64 v[86:87], v[86:87], 0, v[68:69]
	s_cmp_ge_i32 s2, s10
	s_waitcnt lgkmcnt(0)
	global_store_dwordx4 v[86:87], v[82:85], off nt
	s_cbranch_scc1 .LBB0_244
	s_ashr_i32 s3, s2, 31
	s_lshr_b32 s3, s3, 22
	s_add_i32 s3, s2, s3
	s_ashr_i32 s2, s3, 10
	s_and_b32 s3, s3, 0xfffffc00
	s_sub_i32 s3, s12, s3
	s_add_i32 s3, s3, -2
	s_ashr_i32 s30, s3, 31
	s_lshr_b32 s30, s30, 26
	s_add_i32 s3, s3, s30
	s_ashr_i32 s34, s3, 6
	s_ashr_i32 s3, s2, 31
	s_lshl_b64 s[30:31], s[2:3], 25
	s_add_u32 s30, s80, s30
	s_addc_u32 s31, s81, s31
	s_lshl_b32 s3, s34, 12
	s_lshl_b32 s2, s2, 16
	v_lshl_add_u32 v18, s34, 7, v73
	s_add_i32 s3, s3, s2
	v_ashrrev_i32_e32 v19, 31, v18
	s_sub_i32 s2, s11, s3
	v_lshlrev_b64 v[18:19], 14, v[18:19]
	s_addk_i32 s2, 0x140
	v_lshl_add_u64 v[18:19], s[30:31], 0, v[18:19]
	s_ashr_i32 s3, s2, 31
	v_lshl_add_u64 v[18:19], s[2:3], 2, v[18:19]
	v_mov_b32_e32 v71, v67
	v_lshl_add_u64 v[26:27], v[18:19], 0, v[70:71]
	v_add_co_u32_e32 v22, vcc, s26, v26
	s_nop 1
	v_addc_co_u32_e32 v23, vcc, 0, v27, vcc
	v_add_co_u32_e32 v28, vcc, s27, v26
	global_load_dwordx4 v[18:21], v[26:27], off nt
	s_nop 0
	global_load_dwordx4 v[22:25], v[22:23], off nt
	v_addc_co_u32_e32 v29, vcc, 0, v27, vcc
	v_add_co_u32_e32 v30, vcc, s28, v26
	s_nop 1
	v_addc_co_u32_e32 v31, vcc, 0, v27, vcc
	global_load_dwordx4 v[26:29], v[28:29], off nt
	s_nop 0
	global_load_dwordx4 v[30:33], v[30:31], off nt
	s_bitset1_b32 s98, 1
.LBB0_244:
	s_add_i32 s30, s12, -5
	s_cmp_ge_i32 s30, s10
	s_mov_b64 s[2:3], -1
	s_cbranch_scc1 .LBB0_238
	s_waitcnt vmcnt(12)
	s_cmp_eq_u32 s98, 15
	s_cbranch_scc1 .Lcvw_7
	s_waitcnt vmcnt(0)
.Lcvw_7:
	s_bitset0_b32 s98, 2
	s_ashr_i32 s2, s30, 31
	s_lshr_b32 s2, s2, 22
	s_add_i32 s30, s30, s2
	s_and_b32 s3, s30, 0xfffffc00
	v_mul_f32_e32 v71, 0x42800000, v34
	v_mul_f32_e32 v81, 0x42800000, v38
	v_mov_b32_e32 v84, v67
	s_sub_i32 s3, s12, s3
	v_cvt_pk_fp8_f32 v84, v71, v81
	v_mul_f32_e32 v71, 0x42800000, v35
	v_mul_f32_e32 v81, 0x42800000, v39
	v_mov_b32_e32 v85, v67
	s_add_i32 s3, s3, -5
	v_cvt_pk_fp8_f32 v85, v71, v81
	s_ashr_i32 s2, s30, 10
	s_ashr_i32 s30, s3, 31
	s_lshr_b32 s30, s30, 26
	s_add_i32 s3, s3, s30
	v_mul_f32_e32 v71, 0x42800000, v43
	v_mul_f32_e32 v81, 0x42800000, v47
	s_ashr_i32 s34, s3, 6
	s_ashr_i32 s3, s2, 31
	v_cvt_pk_fp8_f32 v85, v71, v81 op_sel:[0,0,1]
	v_mul_f32_e32 v71, 0x42800000, v36
	v_mul_f32_e32 v81, 0x42800000, v40
	v_mov_b32_e32 v86, v67
	s_lshl_b64 s[30:31], s[2:3], 23
	v_cvt_pk_fp8_f32 v86, v71, v81
	v_mul_f32_e32 v71, 0x42800000, v37
	v_mul_f32_e32 v81, 0x42800000, v41
	v_mov_b32_e32 v87, v67
	s_add_u32 s30, s74, s30
	v_cvt_pk_fp8_f32 v87, v71, v81
	s_addc_u32 s31, s75, s31
	s_lshl_b32 s3, s34, 9
	s_lshl_b32 s2, s2, 13
	s_add_i32 s3, s3, s2
	v_mul_f32_e32 v82, 0x42800000, v42
	v_mul_f32_e32 v83, 0x42800000, v46
	s_sub_i32 s2, s13, s3
	v_cvt_pk_fp8_f32 v84, v82, v83 op_sel:[0,0,1]
	v_mul_f32_e32 v82, 0x42800000, v44
	v_mul_f32_e32 v83, 0x42800000, v48
	v_mul_f32_e32 v71, 0x42800000, v45
	v_mul_f32_e32 v81, 0x42800000, v49
	s_add_i32 s2, s2, 16
	v_cvt_pk_fp8_f32 v86, v82, v83 op_sel:[0,0,1]
	v_cvt_pk_fp8_f32 v87, v71, v81 op_sel:[0,0,1]
	s_and_b32 s2, s2, -16
	s_add_i32 s2, s2, s34
	s_ashr_i32 s3, s2, 31
	ds_write2_b32 v76, v84, v85 offset1:33
	ds_write2_b32 v76, v86, v87 offset0:66 offset1:99
	s_waitcnt lgkmcnt(0)
	s_barrier
	ds_read2_b32 v[82:83], v77 offset1:1
	ds_read2_b32 v[84:85], v77 offset0:2 offset1:3
	s_lshl_b64 s[2:3], s[2:3], 14
	s_add_u32 s2, s30, s2
	s_addc_u32 s3, s31, s3
	v_lshl_add_u64 v[86:87], s[2:3], 0, v[66:67]
	s_add_i32 s2, s12, -1
	v_lshl_add_u64 v[86:87], v[86:87], 0, v[68:69]
	s_cmp_ge_i32 s2, s10
	s_waitcnt lgkmcnt(0)
	global_store_dwordx4 v[86:87], v[82:85], off nt
	s_cbranch_scc1 .LBB0_247
	s_ashr_i32 s3, s2, 31
	s_lshr_b32 s3, s3, 22
	s_add_i32 s3, s2, s3
	s_ashr_i32 s2, s3, 10
	s_orn2_b32 s3, 0x3ff, s3
	s_add_i32 s3, s3, s12
	s_ashr_i32 s30, s3, 31
	s_lshr_b32 s30, s30, 26
	s_add_i32 s3, s3, s30
	s_ashr_i32 s34, s3, 6
	s_ashr_i32 s3, s2, 31
	s_lshl_b64 s[30:31], s[2:3], 25
	s_add_u32 s30, s80, s30
	s_addc_u32 s31, s81, s31
	s_lshl_b32 s3, s34, 12
	s_lshl_b32 s2, s2, 16
	v_lshl_add_u32 v34, s34, 7, v73
	s_add_i32 s3, s3, s2
	v_ashrrev_i32_e32 v35, 31, v34
	s_sub_i32 s2, s11, s3
	v_lshlrev_b64 v[34:35], 14, v[34:35]
	s_addk_i32 s2, 0x180
	v_lshl_add_u64 v[34:35], s[30:31], 0, v[34:35]
	s_ashr_i32 s3, s2, 31
	v_lshl_add_u64 v[34:35], s[2:3], 2, v[34:35]
	v_mov_b32_e32 v71, v67
	v_lshl_add_u64 v[42:43], v[34:35], 0, v[70:71]
	v_add_co_u32_e32 v38, vcc, 0x4000, v42
	s_nop 1
	v_addc_co_u32_e32 v39, vcc, 0, v43, vcc
	v_add_co_u32_e32 v44, vcc, 0x8000, v42
	global_load_dwordx4 v[34:37], v[42:43], off nt
	s_nop 0
	global_load_dwordx4 v[38:41], v[38:39], off nt
	v_addc_co_u32_e32 v45, vcc, 0, v43, vcc
	v_add_co_u32_e32 v46, vcc, 0xc000, v42
	s_nop 1
	v_addc_co_u32_e32 v47, vcc, 0, v43, vcc
	global_load_dwordx4 v[42:45], v[44:45], off nt
	s_nop 0
	global_load_dwordx4 v[46:49], v[46:47], off nt
	s_bitset1_b32 s98, 2
.LBB0_247:
	s_add_i32 s30, s12, -4
	s_cmp_ge_i32 s30, s10
	s_mov_b64 s[2:3], -1
	s_cbranch_scc1 .LBB0_238
	s_waitcnt vmcnt(12)
	s_cmp_eq_u32 s98, 15
	s_cbranch_scc1 .Lcvw_8
	s_waitcnt vmcnt(0)
.Lcvw_8:
	s_bitset0_b32 s98, 3
	s_ashr_i32 s2, s30, 31
	s_lshr_b32 s2, s2, 22
	s_add_i32 s30, s30, s2
	s_and_b32 s3, s30, 0xfffffc00
	v_mul_f32_e32 v66, 0x42800000, v50
	v_mul_f32_e32 v71, 0x42800000, v54
	v_mov_b32_e32 v82, v67
	s_sub_i32 s3, s12, s3
	v_cvt_pk_fp8_f32 v82, v66, v71
	v_mul_f32_e32 v66, 0x42800000, v51
	v_mul_f32_e32 v71, 0x42800000, v55
	v_mov_b32_e32 v83, v67
	s_add_i32 s3, s3, -4
	v_cvt_pk_fp8_f32 v83, v66, v71
	s_ashr_i32 s2, s30, 10
	s_ashr_i32 s30, s3, 31
	s_lshr_b32 s30, s30, 26
	s_add_i32 s3, s3, s30
	v_mul_f32_e32 v66, 0x42800000, v59
	v_mul_f32_e32 v71, 0x42800000, v63
	s_ashr_i32 s34, s3, 6
	s_ashr_i32 s3, s2, 31
	v_cvt_pk_fp8_f32 v83, v66, v71 op_sel:[0,0,1]
	v_mul_f32_e32 v66, 0x42800000, v52
	v_mul_f32_e32 v71, 0x42800000, v56
	v_mov_b32_e32 v84, v67
	s_lshl_b64 s[30:31], s[2:3], 23
	v_cvt_pk_fp8_f32 v84, v66, v71
	v_mul_f32_e32 v66, 0x42800000, v53
	v_mul_f32_e32 v71, 0x42800000, v57
	v_mov_b32_e32 v85, v67
	s_add_u32 s30, s74, s30
	v_cvt_pk_fp8_f32 v85, v66, v71
	s_addc_u32 s31, s75, s31
	s_lshl_b32 s3, s34, 9
	s_lshl_b32 s2, s2, 13
	s_add_i32 s3, s3, s2
	v_mul_f32_e32 v77, 0x42800000, v58
	v_mul_f32_e32 v81, 0x42800000, v62
	s_sub_i32 s2, s13, s3
	v_cvt_pk_fp8_f32 v82, v77, v81 op_sel:[0,0,1]
	v_mul_f32_e32 v77, 0x42800000, v60
	v_mul_f32_e32 v81, 0x42800000, v64
	v_mul_f32_e32 v66, 0x42800000, v61
	v_mul_f32_e32 v71, 0x42800000, v65
	s_add_i32 s2, s2, 24
	v_cvt_pk_fp8_f32 v84, v77, v81 op_sel:[0,0,1]
	v_cvt_pk_fp8_f32 v85, v66, v71 op_sel:[0,0,1]
	s_and_b32 s2, s2, -16
	s_add_i32 s2, s2, s34
	s_ashr_i32 s3, s2, 31
	s_add_i32 s34, s11, 0xc0
	ds_write2_b32 v78, v82, v83 offset0:128 offset1:161
	ds_write2_b32 v78, v84, v85 offset0:194 offset1:227
	s_waitcnt lgkmcnt(0)
	s_barrier
	ds_read2_b32 v[78:79], v79 offset1:1
	ds_read2_b32 v[80:81], v80 offset1:1
	s_and_b32 s34, s34, 64
	s_lshl_b64 s[2:3], s[2:3], 14
	s_add_u32 s2, s30, s2
	v_add_lshl_u32 v66, s34, v72, 7
	s_addc_u32 s3, s31, s3
	v_lshl_add_u64 v[82:83], s[2:3], 0, v[66:67]
	v_lshl_add_u64 v[82:83], v[82:83], 0, v[68:69]
	s_cmp_ge_i32 s12, s10
	s_waitcnt lgkmcnt(0)
	global_store_dwordx4 v[82:83], v[78:81], off nt
	s_cbranch_scc1 .LBB0_237
	s_ashr_i32 s2, s12, 31
	s_lshr_b32 s2, s2, 22
	s_add_i32 s3, s12, s2
	s_ashr_i32 s2, s3, 10
	s_and_b32 s3, s3, 0xfffffc00
	s_sub_i32 s3, s12, s3
	s_ashr_i32 s30, s3, 31
	s_lshr_b32 s30, s30, 26
	s_add_i32 s3, s3, s30
	s_ashr_i32 s34, s3, 6
	s_ashr_i32 s3, s2, 31
	s_lshl_b64 s[30:31], s[2:3], 25
	s_add_u32 s30, s80, s30
	s_addc_u32 s31, s81, s31
	s_lshl_b32 s3, s34, 12
	s_lshl_b32 s2, s2, 16
	v_lshl_add_u32 v50, s34, 7, v73
	s_add_i32 s3, s3, s2
	v_ashrrev_i32_e32 v51, 31, v50
	s_sub_i32 s2, s11, s3
	v_lshlrev_b64 v[50:51], 14, v[50:51]
	s_addk_i32 s2, 0x1c0
	v_lshl_add_u64 v[50:51], s[30:31], 0, v[50:51]
	s_ashr_i32 s3, s2, 31
	v_lshl_add_u64 v[50:51], s[2:3], 2, v[50:51]
	v_mov_b32_e32 v71, v67
	v_lshl_add_u64 v[58:59], v[50:51], 0, v[70:71]
	v_add_co_u32_e32 v54, vcc, 0x4000, v58
	s_nop 1
	v_addc_co_u32_e32 v55, vcc, 0, v59, vcc
	v_add_co_u32_e32 v60, vcc, 0x8000, v58
	global_load_dwordx4 v[50:53], v[58:59], off nt
	s_nop 0
	global_load_dwordx4 v[54:57], v[54:55], off nt
	v_addc_co_u32_e32 v61, vcc, 0, v59, vcc
	v_add_co_u32_e32 v62, vcc, 0xc000, v58
	s_nop 1
	v_addc_co_u32_e32 v63, vcc, 0, v59, vcc
	global_load_dwordx4 v[58:61], v[60:61], off nt
	s_nop 0
	global_load_dwordx4 v[62:65], v[62:63], off nt
	s_bitset1_b32 s98, 3
	s_branch .LBB0_237
.LBB0_250:
	s_cmp_lt_i32 s94, 4
	s_cselect_b64 s[0:1], -1, 0
	s_and_b64 s[10:11], s[0:1], s[6:7]
	s_and_b64 s[0:1], s[72:73], s[10:11]
	s_andn2_b64 vcc, exec, s[0:1]
	s_cbranch_vccnz .LBB0_259
	s_lshr_b32 s0, s96, 31
	s_add_i32 s0, s96, s0
	s_ashr_i32 s2, s0, 1
	s_add_i32 s3, s97, s76
	s_mul_i32 s6, s2, 31
	s_waitcnt vmcnt(0)
	v_lshrrev_b32_e32 v3, 4, v178
	v_and_b32_e32 v68, 15, v178
	s_cmp_lt_i32 s76, s6
	s_waitcnt lgkmcnt(0)
	v_mov_b32_e32 v2, 0
	s_cselect_b64 s[0:1], -1, 0
	s_cmp_ge_i32 s76, s6
	v_lshlrev_b32_e32 v71, 2, v3
	v_lshlrev_b32_e32 v66, 4, v68
	v_mov_b32_e32 v6, 0
	v_mov_b32_e32 v7, 0
	v_mov_b32_e32 v8, 0
	v_mov_b32_e32 v9, 0
	v_mov_b32_e32 v10, 0
	v_mov_b32_e32 v11, 0
	v_mov_b32_e32 v12, 0
	v_mov_b32_e32 v13, 0
	v_mov_b32_e32 v14, 0
	v_mov_b32_e32 v15, 0
	v_mov_b32_e32 v16, 0
	v_mov_b32_e32 v17, 0
	v_mov_b32_e32 v18, 0
	v_mov_b32_e32 v19, 0
	v_mov_b32_e32 v20, 0
	v_mov_b32_e32 v21, 0
	s_mov_b32 s98, 0
	s_barrier
	s_cbranch_scc1 .LBB0_253
	s_ashr_i32 s7, s3, 31
	s_lshr_b32 s7, s7, 22
	s_add_i32 s7, s3, s7
	s_ashr_i32 s12, s7, 10
	s_and_b32 s7, s7, 0xfffffc00
	s_sub_i32 s7, s3, s7
	s_ashr_i32 s13, s7, 31
	s_lshr_b32 s13, s13, 26
	s_add_i32 s13, s7, s13
	s_ashr_i32 s16, s13, 6
	s_ashr_i32 s13, s12, 31
	s_lshl_b64 s[12:13], s[12:13], 25
	v_lshl_add_u32 v4, s16, 7, v71
	s_add_u32 s12, s80, s12
	v_ashrrev_i32_e32 v5, 31, v4
	s_addc_u32 s13, s81, s13
	v_lshlrev_b64 v[4:5], 14, v[4:5]
	v_lshl_add_u64 v[4:5], s[12:13], 0, v[4:5]
	s_lshl_b32 s12, s16, 12
	s_lshl_b32 s7, s7, 6
	s_sub_i32 s12, s7, s12
	s_ashr_i32 s13, s12, 31
	v_lshl_add_u64 v[4:5], s[12:13], 2, v[4:5]
	v_mov_b32_e32 v67, 0
	v_lshl_add_u64 v[4:5], v[4:5], 0, v[66:67]
	s_movk_i32 s7, 0x4000
	v_add_co_u32_e32 v10, vcc, s7, v4
	s_mov_b32 s7, 0x8000
	s_nop 0
	v_addc_co_u32_e32 v11, vcc, 0, v5, vcc
	v_add_co_u32_e32 v14, vcc, s7, v4
	s_mov_b32 s7, 0xc000
	s_nop 0
	v_addc_co_u32_e32 v15, vcc, 0, v5, vcc
	global_load_dwordx4 v[6:9], v[4:5], off nt
	s_nop 0
	global_load_dwordx4 v[10:13], v[10:11], off nt
	v_add_co_u32_e32 v4, vcc, s7, v4
	s_nop 1
	v_addc_co_u32_e32 v5, vcc, 0, v5, vcc
	global_load_dwordx4 v[14:17], v[14:15], off nt
	s_nop 0
	global_load_dwordx4 v[18:21], v[4:5], off nt
	s_bitset1_b32 s98, 0
.LBB0_253:
	s_add_i32 s6, s6, s97
	s_add_i32 s7, s3, s2
	s_cmp_ge_i32 s7, s6
	v_mov_b32_e32 v3, 0
	v_mov_b32_e32 v4, 0
	v_mov_b32_e32 v5, 0
	v_mov_b32_e32 v22, 0
	v_mov_b32_e32 v23, 0
	v_mov_b32_e32 v24, 0
	v_mov_b32_e32 v25, 0
	v_mov_b32_e32 v26, 0
	v_mov_b32_e32 v27, 0
	v_mov_b32_e32 v28, 0
	v_mov_b32_e32 v29, 0
	v_mov_b32_e32 v30, 0
	v_mov_b32_e32 v31, 0
	v_mov_b32_e32 v32, 0
	v_mov_b32_e32 v33, 0
	s_cbranch_scc1 .LBB0_255
	s_ashr_i32 s12, s7, 31
	s_lshr_b32 s12, s12, 22
	s_add_i32 s13, s7, s12
	s_ashr_i32 s12, s13, 10
	s_and_b32 s13, s13, 0xfffffc00
	s_sub_i32 s16, s7, s13
	s_ashr_i32 s13, s16, 31
	s_lshr_b32 s13, s13, 26
	s_add_i32 s13, s16, s13
	s_ashr_i32 s17, s13, 6
	s_ashr_i32 s13, s12, 31
	s_lshl_b64 s[12:13], s[12:13], 25
	v_lshl_add_u32 v2, s17, 7, v71
	s_add_u32 s12, s80, s12
	v_ashrrev_i32_e32 v3, 31, v2
	s_addc_u32 s13, s81, s13
	v_lshlrev_b64 v[2:3], 14, v[2:3]
	v_lshl_add_u64 v[2:3], s[12:13], 0, v[2:3]
	s_lshl_b32 s12, s17, 12
	s_lshl_b32 s13, s16, 6
	s_sub_i32 s12, s13, s12
	s_ashr_i32 s13, s12, 31
	v_lshl_add_u64 v[2:3], s[12:13], 2, v[2:3]
	v_mov_b32_e32 v67, 0
	v_lshl_add_u64 v[26:27], v[2:3], 0, v[66:67]
	s_movk_i32 s12, 0x4000
	v_add_co_u32_e32 v22, vcc, s12, v26
	s_mov_b32 s12, 0x8000
	s_nop 0
	v_addc_co_u32_e32 v23, vcc, 0, v27, vcc
	v_add_co_u32_e32 v28, vcc, s12, v26
	s_mov_b32 s12, 0xc000
	s_nop 0
	v_addc_co_u32_e32 v29, vcc, 0, v27, vcc
	v_add_co_u32_e32 v30, vcc, s12, v26
	global_load_dwordx4 v[2:5], v[26:27], off nt
	s_nop 0
	global_load_dwordx4 v[22:25], v[22:23], off nt
	v_addc_co_u32_e32 v31, vcc, 0, v27, vcc
	global_load_dwordx4 v[26:29], v[28:29], off nt
	s_nop 0
	global_load_dwordx4 v[30:33], v[30:31], off nt
	s_bitset1_b32 s98, 1
.LBB0_255:
	s_add_i32 s7, s7, s2
	s_cmp_ge_i32 s7, s6
	s_cbranch_scc1 .LBB0_257
	s_ashr_i32 s12, s7, 31
	s_lshr_b32 s12, s12, 22
	s_add_i32 s13, s7, s12
	s_ashr_i32 s12, s13, 10
	s_and_b32 s13, s13, 0xfffffc00
	s_sub_i32 s16, s7, s13
	s_ashr_i32 s13, s16, 31
	s_lshr_b32 s13, s13, 26
	s_add_i32 s13, s16, s13
	s_ashr_i32 s17, s13, 6
	s_ashr_i32 s13, s12, 31
	s_lshl_b64 s[12:13], s[12:13], 25
	v_lshl_add_u32 v34, s17, 7, v71
	s_add_u32 s12, s80, s12
	v_ashrrev_i32_e32 v35, 31, v34
	s_addc_u32 s13, s81, s13
	v_lshlrev_b64 v[34:35], 14, v[34:35]
	v_lshl_add_u64 v[34:35], s[12:13], 0, v[34:35]
	s_lshl_b32 s12, s17, 12
	s_lshl_b32 s13, s16, 6
	s_sub_i32 s12, s13, s12
	s_ashr_i32 s13, s12, 31
	v_lshl_add_u64 v[34:35], s[12:13], 2, v[34:35]
	v_mov_b32_e32 v67, 0
	v_lshl_add_u64 v[42:43], v[34:35], 0, v[66:67]
	s_movk_i32 s12, 0x4000
	v_add_co_u32_e32 v38, vcc, s12, v42
	s_nop 1
	v_addc_co_u32_e32 v39, vcc, 0, v43, vcc
	v_add_co_u32_e32 v44, vcc, 0x8000, v42
	global_load_dwordx4 v[34:37], v[42:43], off nt
	s_nop 0
	global_load_dwordx4 v[38:41], v[38:39], off nt
	v_addc_co_u32_e32 v45, vcc, 0, v43, vcc
	v_add_co_u32_e32 v46, vcc, 0xc000, v42
	s_nop 1
	v_addc_co_u32_e32 v47, vcc, 0, v43, vcc
	global_load_dwordx4 v[42:45], v[44:45], off nt
	s_nop 0
	global_load_dwordx4 v[46:49], v[46:47], off nt
	s_bitset1_b32 s98, 2
.LBB0_257:
	s_add_i32 s7, s7, s2
	s_cmp_ge_i32 s7, s6
	s_cbranch_scc1 .LBB0_270
	s_ashr_i32 s12, s7, 31
	s_lshr_b32 s12, s12, 22
	s_add_i32 s13, s7, s12
	s_ashr_i32 s12, s13, 10
	s_and_b32 s13, s13, 0xfffffc00
	s_sub_i32 s7, s7, s13
	s_ashr_i32 s13, s7, 31
	s_lshr_b32 s13, s13, 26
	s_add_i32 s13, s7, s13
	s_ashr_i32 s16, s13, 6
	s_ashr_i32 s13, s12, 31
	s_lshl_b64 s[12:13], s[12:13], 25
	v_lshl_add_u32 v50, s16, 7, v71
	s_add_u32 s12, s80, s12
	v_ashrrev_i32_e32 v51, 31, v50
	s_addc_u32 s13, s81, s13
	v_lshlrev_b64 v[50:51], 14, v[50:51]
	v_lshl_add_u64 v[50:51], s[12:13], 0, v[50:51]
	s_lshl_b32 s12, s16, 12
	s_lshl_b32 s7, s7, 6
	s_sub_i32 s12, s7, s12
	s_ashr_i32 s13, s12, 31
	v_lshl_add_u64 v[50:51], s[12:13], 2, v[50:51]
	v_mov_b32_e32 v67, 0
	v_lshl_add_u64 v[58:59], v[50:51], 0, v[66:67]
	s_movk_i32 s7, 0x4000
	v_add_co_u32_e32 v54, vcc, s7, v58
	s_nop 1
	v_addc_co_u32_e32 v55, vcc, 0, v59, vcc
	v_add_co_u32_e32 v60, vcc, 0x8000, v58
	global_load_dwordx4 v[50:53], v[58:59], off nt
	s_nop 0
	global_load_dwordx4 v[54:57], v[54:55], off nt
	v_addc_co_u32_e32 v61, vcc, 0, v59, vcc
	v_add_co_u32_e32 v62, vcc, 0xc000, v58
	s_nop 1
	v_addc_co_u32_e32 v63, vcc, 0, v59, vcc
	global_load_dwordx4 v[58:61], v[60:61], off nt
	s_nop 0
	global_load_dwordx4 v[62:65], v[62:63], off nt
	s_bitset1_b32 s98, 3
	s_andn2_b64 vcc, exec, s[0:1]
	s_cbranch_vccnz .LBB0_285
	s_branch .LBB0_271

.Lcvw_9:
	s_bitset0_b32 s98, 0
	s_ashr_i32 s0, s3, 31
	s_lshr_b32 s0, s0, 22
	v_mul_f32_e32 v68, 0x42800000, v6
	v_mul_f32_e32 v75, 0x42800000, v10
	v_mov_b32_e32 v78, 0
	s_add_i32 s1, s3, s0
	v_cvt_pk_fp8_f32 v78, v68, v75
	v_mul_f32_e32 v68, 0x42800000, v7
	v_mul_f32_e32 v75, 0x42800000, v11
	v_mov_b32_e32 v79, 0
	s_ashr_i32 s0, s1, 10
	s_and_b32 s1, s1, 0xfffffc00
	v_cvt_pk_fp8_f32 v79, v68, v75
	s_sub_i32 s1, s3, s1
	s_ashr_i32 s42, s1, 31
	s_lshr_b32 s42, s42, 26
	v_mul_f32_e32 v68, 0x42800000, v15
	v_mul_f32_e32 v75, 0x42800000, v19
	s_add_i32 s1, s1, s42
	v_cvt_pk_fp8_f32 v79, v68, v75 op_sel:[0,0,1]
	v_mul_f32_e32 v68, 0x42800000, v8
	v_mul_f32_e32 v75, 0x42800000, v12
	v_mov_b32_e32 v80, 0
	s_ashr_i32 s44, s1, 6
	s_ashr_i32 s1, s0, 31
	v_cvt_pk_fp8_f32 v80, v68, v75
	v_mul_f32_e32 v68, 0x42800000, v9
	v_mul_f32_e32 v75, 0x42800000, v13
	v_mov_b32_e32 v81, 0
	s_lshl_b64 s[42:43], s[0:1], 23
	v_cvt_pk_fp8_f32 v81, v68, v75
	s_add_u32 s42, s74, s42
	s_addc_u32 s43, s75, s43
	s_lshl_b32 s1, s44, 9
	s_lshl_b32 s0, s0, 13
	v_mul_f32_e32 v76, 0x42800000, v14
	v_mul_f32_e32 v77, 0x42800000, v18
	s_add_i32 s1, s1, s0
	s_add_i32 s0, s17, s19
	v_cvt_pk_fp8_f32 v78, v76, v77 op_sel:[0,0,1]
	v_mul_f32_e32 v76, 0x42800000, v16
	v_mul_f32_e32 v77, 0x42800000, v20
	v_mul_f32_e32 v68, 0x42800000, v17
	v_mul_f32_e32 v75, 0x42800000, v21
	s_sub_i32 s0, s0, s1
	v_cvt_pk_fp8_f32 v80, v76, v77 op_sel:[0,0,1]
	v_cvt_pk_fp8_f32 v81, v68, v75 op_sel:[0,0,1]
	s_and_b32 s0, s0, -16
	s_add_i32 s0, s0, s44
	s_ashr_i32 s1, s0, 31
	s_add_i32 s44, s12, s13
	ds_write2_b32 v73, v78, v79 offset1:33
	ds_write2_b32 v73, v80, v81 offset0:66 offset1:99
	s_waitcnt lgkmcnt(0)
	s_barrier
	ds_read2_b32 v[76:77], v74 offset1:1
	ds_read2_b32 v[78:79], v74 offset0:2 offset1:3
	s_and_b32 s44, s44, 64
	s_lshl_b64 s[0:1], s[0:1], 14
	s_add_u32 s0, s42, s0
	v_add_lshl_u32 v68, s44, v72, 7
	s_addc_u32 s1, s43, s1
	v_lshl_add_u64 v[80:81], s[0:1], 0, v[68:69]
	s_add_i32 s0, s7, s3
	v_lshl_add_u64 v[80:81], v[80:81], 0, v[66:67]
	s_cmp_ge_i32 s0, s6
	s_waitcnt lgkmcnt(0)
	global_store_dwordx4 v[80:81], v[76:79], off nt
	s_cbranch_scc1 .LBB0_276
	s_ashr_i32 s1, s0, 31
	s_lshr_b32 s1, s1, 22
	s_add_i32 s1, s0, s1
	s_ashr_i32 s42, s1, 10
	s_and_b32 s1, s1, 0xfffffc00
	s_sub_i32 s0, s0, s1
	s_ashr_i32 s1, s0, 31
	s_lshr_b32 s1, s1, 26
	s_add_i32 s0, s0, s1
	s_ashr_i32 s44, s0, 6
	s_ashr_i32 s43, s42, 31
	s_lshl_b64 s[0:1], s[42:43], 25
	v_lshl_add_u32 v6, s44, 7, v71
	s_add_u32 s0, s80, s0
	v_ashrrev_i32_e32 v7, 31, v6
	s_addc_u32 s1, s81, s1
	v_lshlrev_b64 v[6:7], 14, v[6:7]
	v_lshl_add_u64 v[6:7], s[0:1], 0, v[6:7]
	s_lshl_b32 s0, s44, 12
	s_lshl_b32 s1, s42, 16
	s_add_i32 s0, s0, s1
	s_add_i32 s1, s38, s13
	s_sub_i32 s0, s1, s0
	s_ashr_i32 s1, s0, 31
	v_lshl_add_u64 v[6:7], s[0:1], 2, v[6:7]
	v_lshlrev_b32_e32 v68, 2, v70
	v_lshl_add_u64 v[14:15], v[6:7], 0, v[68:69]
	v_add_co_u32_e32 v10, vcc, s39, v14
	s_nop 1
	v_addc_co_u32_e32 v11, vcc, 0, v15, vcc
	v_add_co_u32_e32 v16, vcc, s40, v14
	global_load_dwordx4 v[6:9], v[14:15], off nt
	s_nop 0
	global_load_dwordx4 v[10:13], v[10:11], off nt
	v_addc_co_u32_e32 v17, vcc, 0, v15, vcc
	v_add_co_u32_e32 v18, vcc, s41, v14
	s_nop 1
	v_addc_co_u32_e32 v19, vcc, 0, v15, vcc
	global_load_dwordx4 v[14:17], v[16:17], off nt
	s_nop 0
	global_load_dwordx4 v[18:21], v[18:19], off nt
	s_bitset1_b32 s98, 0
.LBB0_276:
	s_add_i32 s42, s3, s2
	s_cmp_ge_i32 s42, s6
	s_mov_b64 s[0:1], -1
	s_cbranch_scc1 .LBB0_273
	s_waitcnt vmcnt(12)
	s_cmp_eq_u32 s98, 15
	s_cbranch_scc1 .Lcvw_10
	s_waitcnt vmcnt(0)
.Lcvw_10:
	s_bitset0_b32 s98, 1
	s_ashr_i32 s0, s42, 31
	s_lshr_b32 s0, s0, 22
	v_mul_f32_e32 v68, 0x42800000, v2
	v_mul_f32_e32 v75, 0x42800000, v22
	v_mov_b32_e32 v78, v69
	s_add_i32 s1, s42, s0
	v_cvt_pk_fp8_f32 v78, v68, v75
	v_mul_f32_e32 v68, 0x42800000, v3
	v_mul_f32_e32 v75, 0x42800000, v23
	v_mov_b32_e32 v79, v69
	s_ashr_i32 s0, s1, 10
	s_and_b32 s1, s1, 0xfffffc00
	v_cvt_pk_fp8_f32 v79, v68, v75
	s_sub_i32 s1, s42, s1
	s_ashr_i32 s43, s1, 31
	s_lshr_b32 s43, s43, 26
	v_mul_f32_e32 v68, 0x42800000, v27
	v_mul_f32_e32 v75, 0x42800000, v31
	s_add_i32 s1, s1, s43
	v_cvt_pk_fp8_f32 v79, v68, v75 op_sel:[0,0,1]
	v_mul_f32_e32 v68, 0x42800000, v4
	v_mul_f32_e32 v75, 0x42800000, v24
	v_mov_b32_e32 v80, v69
	s_ashr_i32 s43, s1, 6
	s_ashr_i32 s1, s0, 31
	v_cvt_pk_fp8_f32 v80, v68, v75
	v_mul_f32_e32 v68, 0x42800000, v5
	v_mul_f32_e32 v75, 0x42800000, v25
	v_mov_b32_e32 v81, v69
	s_lshl_b64 s[44:45], s[0:1], 23
	v_cvt_pk_fp8_f32 v81, v68, v75
	s_add_u32 s44, s74, s44
	s_addc_u32 s45, s75, s45
	s_lshl_b32 s1, s43, 9
	s_lshl_b32 s0, s0, 13
	v_mul_f32_e32 v76, 0x42800000, v26
	v_mul_f32_e32 v77, 0x42800000, v30
	s_add_i32 s1, s1, s0
	s_add_i32 s0, s18, s19
	v_cvt_pk_fp8_f32 v78, v76, v77 op_sel:[0,0,1]
	v_mul_f32_e32 v76, 0x42800000, v28
	v_mul_f32_e32 v77, 0x42800000, v32
	v_mul_f32_e32 v68, 0x42800000, v29
	v_mul_f32_e32 v75, 0x42800000, v33
	s_sub_i32 s0, s0, s1
	v_cvt_pk_fp8_f32 v80, v76, v77 op_sel:[0,0,1]
	v_cvt_pk_fp8_f32 v81, v68, v75 op_sel:[0,0,1]
	s_and_b32 s0, s0, -16
	s_add_i32 s0, s0, s43
	v_add_u32_e32 v75, 0x2000, v73
	v_add_u32_e32 v76, 0x2200, v74
	s_ashr_i32 s1, s0, 31
	s_add_i32 s43, s21, s13
	ds_write2_b32 v75, v78, v79 offset0:128 offset1:161
	ds_write2_b32 v75, v80, v81 offset0:194 offset1:227
	s_waitcnt lgkmcnt(0)
	s_barrier
	v_add_u32_e32 v77, 0x2208, v74
	ds_read2_b32 v[78:79], v76 offset1:1
	ds_read2_b32 v[80:81], v77 offset1:1
	s_and_b32 s43, s43, 64
	s_lshl_b64 s[0:1], s[0:1], 14
	s_add_u32 s0, s44, s0
	v_add_lshl_u32 v68, s43, v72, 7
	s_addc_u32 s1, s45, s1
	v_lshl_add_u64 v[82:83], s[0:1], 0, v[68:69]
	s_add_i32 s0, s24, s3
	v_lshl_add_u64 v[82:83], v[82:83], 0, v[66:67]
	s_cmp_ge_i32 s0, s6
	s_waitcnt lgkmcnt(0)
	global_store_dwordx4 v[82:83], v[78:81], off nt
	s_cbranch_scc1 .LBB0_279
	s_ashr_i32 s1, s0, 31
	s_lshr_b32 s1, s1, 22
	s_add_i32 s1, s0, s1
	s_ashr_i32 s44, s1, 10
	s_and_b32 s1, s1, 0xfffffc00
	s_sub_i32 s0, s0, s1
	s_ashr_i32 s1, s0, 31
	s_lshr_b32 s1, s1, 26
	s_add_i32 s0, s0, s1
	s_ashr_i32 s43, s0, 6
	s_ashr_i32 s45, s44, 31
	s_lshl_b64 s[0:1], s[44:45], 25
	v_lshl_add_u32 v2, s43, 7, v71
	s_add_u32 s0, s80, s0
	v_ashrrev_i32_e32 v3, 31, v2
	s_addc_u32 s1, s81, s1
	v_lshlrev_b64 v[2:3], 14, v[2:3]
	v_lshl_add_u64 v[2:3], s[0:1], 0, v[2:3]
	s_lshl_b32 s0, s43, 12
	s_lshl_b32 s1, s44, 16
	s_add_i32 s0, s0, s1
	s_add_i32 s1, s25, s13
	s_sub_i32 s0, s1, s0
	s_ashr_i32 s1, s0, 31
	v_lshl_add_u64 v[2:3], s[0:1], 2, v[2:3]
	v_lshlrev_b32_e32 v68, 2, v70
	v_lshl_add_u64 v[26:27], v[2:3], 0, v[68:69]
	v_add_co_u32_e32 v22, vcc, s39, v26
	s_nop 1
	v_addc_co_u32_e32 v23, vcc, 0, v27, vcc
	v_add_co_u32_e32 v28, vcc, s40, v26
	global_load_dwordx4 v[2:5], v[26:27], off nt
	s_nop 0
	global_load_dwordx4 v[22:25], v[22:23], off nt
	v_addc_co_u32_e32 v29, vcc, 0, v27, vcc
	v_add_co_u32_e32 v30, vcc, s41, v26
	s_nop 1
	v_addc_co_u32_e32 v31, vcc, 0, v27, vcc
	global_load_dwordx4 v[26:29], v[28:29], off nt
	s_nop 0
	global_load_dwordx4 v[30:33], v[30:31], off nt
	s_bitset1_b32 s98, 1
.LBB0_279:
	s_add_i32 s43, s26, s3
	s_cmp_ge_i32 s43, s6
	s_mov_b64 s[0:1], -1
	s_cbranch_scc1 .LBB0_273
	s_waitcnt vmcnt(12)
	s_cmp_eq_u32 s98, 15
	s_cbranch_scc1 .Lcvw_11
	s_waitcnt vmcnt(0)
.Lcvw_11:
	s_bitset0_b32 s98, 2
	s_ashr_i32 s0, s43, 31
	s_lshr_b32 s0, s0, 22
	v_mul_f32_e32 v68, 0x42800000, v34
	v_mul_f32_e32 v78, 0x42800000, v38
	v_mov_b32_e32 v81, v69
	s_add_i32 s1, s43, s0
	v_cvt_pk_fp8_f32 v81, v68, v78
	v_mul_f32_e32 v68, 0x42800000, v35
	v_mul_f32_e32 v78, 0x42800000, v39
	v_mov_b32_e32 v82, v69
	s_ashr_i32 s0, s1, 10
	s_and_b32 s1, s1, 0xfffffc00
	v_cvt_pk_fp8_f32 v82, v68, v78
	s_sub_i32 s1, s43, s1
	s_ashr_i32 s43, s1, 31
	s_lshr_b32 s43, s43, 26
	v_mul_f32_e32 v68, 0x42800000, v43
	v_mul_f32_e32 v78, 0x42800000, v47
	s_add_i32 s1, s1, s43
	v_cvt_pk_fp8_f32 v82, v68, v78 op_sel:[0,0,1]
	v_mul_f32_e32 v68, 0x42800000, v36
	v_mul_f32_e32 v78, 0x42800000, v40
	v_mov_b32_e32 v83, v69
	s_ashr_i32 s43, s1, 6
	s_ashr_i32 s1, s0, 31
	v_cvt_pk_fp8_f32 v83, v68, v78
	v_mul_f32_e32 v68, 0x42800000, v37
	v_mul_f32_e32 v78, 0x42800000, v41
	v_mov_b32_e32 v84, v69
	s_lshl_b64 s[44:45], s[0:1], 23
	v_cvt_pk_fp8_f32 v84, v68, v78
	s_add_u32 s44, s74, s44
	s_addc_u32 s45, s75, s45
	s_lshl_b32 s1, s43, 9
	s_lshl_b32 s0, s0, 13
	v_mul_f32_e32 v79, 0x42800000, v42
	v_mul_f32_e32 v80, 0x42800000, v46
	s_add_i32 s1, s1, s0
	s_add_i32 s0, s27, s19
	v_cvt_pk_fp8_f32 v81, v79, v80 op_sel:[0,0,1]
	v_mul_f32_e32 v79, 0x42800000, v44
	v_mul_f32_e32 v80, 0x42800000, v48
	v_mul_f32_e32 v68, 0x42800000, v45
	v_mul_f32_e32 v78, 0x42800000, v49
	s_sub_i32 s0, s0, s1
	v_cvt_pk_fp8_f32 v83, v79, v80 op_sel:[0,0,1]
	v_cvt_pk_fp8_f32 v84, v68, v78 op_sel:[0,0,1]
	s_and_b32 s0, s0, -16
	s_add_i32 s0, s0, s43
	s_ashr_i32 s1, s0, 31
	s_add_i32 s43, s28, s13
	ds_write2_b32 v73, v81, v82 offset1:33
	ds_write2_b32 v73, v83, v84 offset0:66 offset1:99
	s_waitcnt lgkmcnt(0)
	s_barrier
	ds_read2_b32 v[78:79], v74 offset1:1
	ds_read2_b32 v[80:81], v74 offset0:2 offset1:3
	s_and_b32 s43, s43, 64
	s_lshl_b64 s[0:1], s[0:1], 14
	s_add_u32 s0, s44, s0
	v_add_lshl_u32 v68, s43, v72, 7
	s_addc_u32 s1, s45, s1
	v_lshl_add_u64 v[82:83], s[0:1], 0, v[68:69]
	s_add_i32 s0, s29, s3
	v_lshl_add_u64 v[82:83], v[82:83], 0, v[66:67]
	s_cmp_ge_i32 s0, s6
	s_waitcnt lgkmcnt(0)
	global_store_dwordx4 v[82:83], v[78:81], off nt
	s_cbranch_scc1 .LBB0_282
	s_ashr_i32 s1, s0, 31
	s_lshr_b32 s1, s1, 22
	s_add_i32 s1, s0, s1
	s_ashr_i32 s44, s1, 10
	s_and_b32 s1, s1, 0xfffffc00
	s_sub_i32 s0, s0, s1
	s_ashr_i32 s1, s0, 31
	s_lshr_b32 s1, s1, 26
	s_add_i32 s0, s0, s1
	s_ashr_i32 s43, s0, 6
	s_ashr_i32 s45, s44, 31
	s_lshl_b64 s[0:1], s[44:45], 25
	v_lshl_add_u32 v34, s43, 7, v71
	s_add_u32 s0, s80, s0
	v_ashrrev_i32_e32 v35, 31, v34
	s_addc_u32 s1, s81, s1
	v_lshlrev_b64 v[34:35], 14, v[34:35]
	v_lshl_add_u64 v[34:35], s[0:1], 0, v[34:35]
	s_lshl_b32 s0, s43, 12
	s_lshl_b32 s1, s44, 16
	s_add_i32 s0, s0, s1
	s_add_i32 s1, s30, s13
	s_sub_i32 s0, s1, s0
	s_ashr_i32 s1, s0, 31
	v_lshl_add_u64 v[34:35], s[0:1], 2, v[34:35]
	v_lshlrev_b32_e32 v68, 2, v70
	v_lshl_add_u64 v[42:43], v[34:35], 0, v[68:69]
	v_add_co_u32_e32 v38, vcc, 0x4000, v42
	s_nop 1
	v_addc_co_u32_e32 v39, vcc, 0, v43, vcc
	v_add_co_u32_e32 v44, vcc, 0x8000, v42
	global_load_dwordx4 v[34:37], v[42:43], off nt
	s_nop 0
	global_load_dwordx4 v[38:41], v[38:39], off nt
	v_addc_co_u32_e32 v45, vcc, 0, v43, vcc
	v_add_co_u32_e32 v46, vcc, 0xc000, v42
	s_nop 1
	v_addc_co_u32_e32 v47, vcc, 0, v43, vcc
	global_load_dwordx4 v[42:45], v[44:45], off nt
	s_nop 0
	global_load_dwordx4 v[46:49], v[46:47], off nt
	s_bitset1_b32 s98, 2
.LBB0_282:
	s_add_i32 s43, s31, s3
	s_cmp_ge_i32 s43, s6
	s_mov_b64 s[0:1], -1
	s_cbranch_scc1 .LBB0_273
	s_waitcnt vmcnt(12)
	s_cmp_eq_u32 s98, 15
	s_cbranch_scc1 .Lcvw_12
	s_waitcnt vmcnt(0)
.Lcvw_12:
	s_bitset0_b32 s98, 3
	s_ashr_i32 s0, s43, 31
	s_lshr_b32 s0, s0, 22
	v_mul_f32_e32 v68, 0x42800000, v50
	v_mul_f32_e32 v78, 0x42800000, v54
	v_mov_b32_e32 v81, v69
	s_add_i32 s1, s43, s0
	v_cvt_pk_fp8_f32 v81, v68, v78
	v_mul_f32_e32 v68, 0x42800000, v51
	v_mul_f32_e32 v78, 0x42800000, v55
	v_mov_b32_e32 v82, v69
	s_ashr_i32 s0, s1, 10
	s_and_b32 s1, s1, 0xfffffc00
	v_cvt_pk_fp8_f32 v82, v68, v78
	s_sub_i32 s1, s43, s1
	s_ashr_i32 s43, s1, 31
	s_lshr_b32 s43, s43, 26
	v_mul_f32_e32 v68, 0x42800000, v59
	v_mul_f32_e32 v78, 0x42800000, v63
	s_add_i32 s1, s1, s43
	v_cvt_pk_fp8_f32 v82, v68, v78 op_sel:[0,0,1]
	v_mul_f32_e32 v68, 0x42800000, v52
	v_mul_f32_e32 v78, 0x42800000, v56
	v_mov_b32_e32 v83, v69
	s_ashr_i32 s43, s1, 6
	s_ashr_i32 s1, s0, 31
	v_cvt_pk_fp8_f32 v83, v68, v78
	v_mul_f32_e32 v68, 0x42800000, v53
	v_mul_f32_e32 v78, 0x42800000, v57
	v_mov_b32_e32 v84, v69
	s_lshl_b64 s[44:45], s[0:1], 23
	v_cvt_pk_fp8_f32 v84, v68, v78
	s_add_u32 s44, s74, s44
	s_addc_u32 s45, s75, s45
	s_lshl_b32 s1, s43, 9
	s_lshl_b32 s0, s0, 13
	v_mul_f32_e32 v79, 0x42800000, v58
	v_mul_f32_e32 v80, 0x42800000, v62
	s_add_i32 s1, s1, s0
	s_add_i32 s0, s34, s19
	v_cvt_pk_fp8_f32 v81, v79, v80 op_sel:[0,0,1]
	v_mul_f32_e32 v79, 0x42800000, v60
	v_mul_f32_e32 v80, 0x42800000, v64
	v_mul_f32_e32 v68, 0x42800000, v61
	v_mul_f32_e32 v78, 0x42800000, v65
	s_sub_i32 s0, s0, s1
	v_cvt_pk_fp8_f32 v83, v79, v80 op_sel:[0,0,1]
	v_cvt_pk_fp8_f32 v84, v68, v78 op_sel:[0,0,1]
	s_and_b32 s0, s0, -16
	s_add_i32 s0, s0, s43
	s_ashr_i32 s1, s0, 31
	s_add_i32 s43, s35, s13
	ds_write2_b32 v75, v81, v82 offset0:128 offset1:161
	ds_write2_b32 v75, v83, v84 offset0:194 offset1:227
	s_waitcnt lgkmcnt(0)
	s_barrier
	ds_read2_b32 v[78:79], v76 offset1:1
	ds_read2_b32 v[80:81], v77 offset1:1
	s_and_b32 s43, s43, 64
	s_lshl_b64 s[0:1], s[0:1], 14
	s_add_u32 s0, s44, s0
	v_add_lshl_u32 v68, s43, v72, 7
	s_addc_u32 s1, s45, s1
	v_lshl_add_u64 v[76:77], s[0:1], 0, v[68:69]
	s_add_i32 s0, s36, s3
	v_lshl_add_u64 v[76:77], v[76:77], 0, v[66:67]
	s_cmp_ge_i32 s0, s6
	s_waitcnt lgkmcnt(0)
	global_store_dwordx4 v[76:77], v[78:81], off nt
	s_cbranch_scc1 .LBB0_272
	s_ashr_i32 s1, s0, 31
	s_lshr_b32 s1, s1, 22
	s_add_i32 s1, s0, s1
	s_ashr_i32 s44, s1, 10
	s_and_b32 s1, s1, 0xfffffc00
	s_sub_i32 s0, s0, s1
	s_ashr_i32 s1, s0, 31
	s_lshr_b32 s1, s1, 26
	s_add_i32 s0, s0, s1
	s_ashr_i32 s3, s0, 6
	s_ashr_i32 s45, s44, 31
	s_lshl_b64 s[0:1], s[44:45], 25
	v_lshl_add_u32 v50, s3, 7, v71
	s_add_u32 s0, s80, s0
	v_ashrrev_i32_e32 v51, 31, v50
	s_addc_u32 s1, s81, s1
	v_lshlrev_b64 v[50:51], 14, v[50:51]
	v_lshl_add_u64 v[50:51], s[0:1], 0, v[50:51]
	s_lshl_b32 s0, s3, 12
	s_lshl_b32 s1, s44, 16
	s_add_i32 s0, s0, s1
	s_add_i32 s1, s37, s13
	s_sub_i32 s0, s1, s0
	s_ashr_i32 s1, s0, 31
	v_lshl_add_u64 v[50:51], s[0:1], 2, v[50:51]
	v_lshlrev_b32_e32 v68, 2, v70
	v_lshl_add_u64 v[58:59], v[50:51], 0, v[68:69]
	v_add_co_u32_e32 v54, vcc, 0x4000, v58
	s_nop 1
	v_addc_co_u32_e32 v55, vcc, 0, v59, vcc
	v_add_co_u32_e32 v60, vcc, 0x8000, v58
	global_load_dwordx4 v[50:53], v[58:59], off nt
	s_nop 0
	global_load_dwordx4 v[54:57], v[54:55], off nt
	v_addc_co_u32_e32 v61, vcc, 0, v59, vcc
	v_add_co_u32_e32 v62, vcc, 0xc000, v58
	s_nop 1
	v_addc_co_u32_e32 v63, vcc, 0, v59, vcc
	global_load_dwordx4 v[58:61], v[60:61], off nt
	s_nop 0
	global_load_dwordx4 v[62:65], v[62:63], off nt
	s_bitset1_b32 s98, 3
	s_branch .LBB0_272

.LBB0_420:
	s_cmp_lt_i32 s26, s17
	s_cselect_b32 s6, 4, 2
	s_and_b64 s[2:3], s[2:3], exec
	s_cselect_b32 s2, 8, s6
	s_ashr_i32 s3, s10, 31
	s_lshr_b32 s3, s3, 22
	s_add_i32 s3, s10, s3
	s_ashr_i32 s6, s3, 10
	s_and_b32 s3, s3, 0xfffffc00
	s_sub_i32 s3, s10, s3
	s_ashr_i32 s7, s3, 31
	s_lshr_b32 s7, s7, 26
	s_add_i32 s7, s3, s7
	s_ashr_i32 s26, s7, 6
	s_ashr_i32 s7, s6, 31
	s_lshl_b64 s[6:7], s[6:7], 25
	v_lshl_add_u32 v0, s26, 7, v72
	s_add_u32 s6, s80, s6
	v_ashrrev_i32_e32 v1, 31, v0
	s_addc_u32 s7, s81, s7
	v_lshlrev_b64 v[0:1], 14, v[0:1]
	v_lshl_add_u64 v[0:1], s[6:7], 0, v[0:1]
	s_lshl_b32 s6, s26, 12
	s_lshl_b32 s3, s3, 6
	s_sub_i32 s6, s3, s6
	s_ashr_i32 s7, s6, 31
	v_lshl_add_u64 v[0:1], s[6:7], 2, v[0:1]
	v_mov_b32_e32 v69, v65
	s_waitcnt vmcnt(1)
	v_lshl_add_u64 v[8:9], v[0:1], 0, v[68:69]
	v_add_co_u32_e32 v4, vcc, s23, v8
	s_nop 1
	v_addc_co_u32_e32 v5, vcc, 0, v9, vcc
	v_add_co_u32_e32 v10, vcc, 0x8000, v8
	s_mov_b32 s98, 0
	s_barrier
	s_nop 0
	v_addc_co_u32_e32 v11, vcc, 0, v9, vcc
	s_waitcnt vmcnt(0)
	v_add_co_u32_e32 v12, vcc, 0xc000, v8
	s_nop 1
	v_addc_co_u32_e32 v13, vcc, 0, v9, vcc
	global_load_dwordx4 v[0:3], v[8:9], off nt
	s_nop 0
	global_load_dwordx4 v[4:7], v[4:5], off nt
	s_nop 0
	global_load_dwordx4 v[8:11], v[10:11], off nt
	s_nop 0
	global_load_dwordx4 v[12:15], v[12:13], off nt
	s_bitset1_b32 s98, 0
	s_add_i32 s3, s10, 1
	v_mov_b32_e32 v16, 0
	s_cmp_le_i32 s36, s3
	v_mov_b32_e32 v17, v16
	v_mov_b32_e32 v18, v16
	v_mov_b32_e32 v19, v16
	v_mov_b32_e32 v20, v16
	v_mov_b32_e32 v21, v16
	v_mov_b32_e32 v22, v16
	v_mov_b32_e32 v23, v16
	v_mov_b32_e32 v24, v16
	v_mov_b32_e32 v25, v16
	v_mov_b32_e32 v26, v16
	v_mov_b32_e32 v27, v16
	v_mov_b32_e32 v28, v16
	v_mov_b32_e32 v29, v16
	v_mov_b32_e32 v30, v16
	v_mov_b32_e32 v31, v16
	s_cbranch_scc1 .LBB0_422
	s_ashr_i32 s6, s3, 31
	s_lshr_b32 s6, s6, 22
	s_add_i32 s7, s3, s6
	s_ashr_i32 s6, s7, 10
	s_and_b32 s7, s7, 0xfffffc00
	s_sub_i32 s3, s3, s7
	s_ashr_i32 s7, s3, 31
	s_lshr_b32 s7, s7, 26
	s_add_i32 s7, s3, s7
	s_ashr_i32 s26, s7, 6
	s_ashr_i32 s7, s6, 31
	s_lshl_b64 s[6:7], s[6:7], 25
	v_lshl_add_u32 v16, s26, 7, v72
	s_add_u32 s6, s80, s6
	v_ashrrev_i32_e32 v17, 31, v16
	s_addc_u32 s7, s81, s7
	v_lshlrev_b64 v[16:17], 14, v[16:17]
	v_lshl_add_u64 v[16:17], s[6:7], 0, v[16:17]
	s_lshl_b32 s6, s26, 12
	s_lshl_b32 s3, s3, 6
	s_sub_i32 s6, s3, s6
	s_ashr_i32 s7, s6, 31
	v_lshl_add_u64 v[16:17], s[6:7], 2, v[16:17]
	v_lshl_add_u64 v[24:25], v[16:17], 0, v[68:69]
	v_add_co_u32_e32 v20, vcc, s23, v24
	s_nop 1
	v_addc_co_u32_e32 v21, vcc, 0, v25, vcc
	v_add_co_u32_e32 v26, vcc, s24, v24
	global_load_dwordx4 v[16:19], v[24:25], off nt
	s_nop 0
	global_load_dwordx4 v[20:23], v[20:21], off nt
	v_addc_co_u32_e32 v27, vcc, 0, v25, vcc
	v_add_co_u32_e32 v28, vcc, s25, v24
	s_nop 1
	v_addc_co_u32_e32 v29, vcc, 0, v25, vcc
	global_load_dwordx4 v[24:27], v[26:27], off nt
	s_nop 0
	global_load_dwordx4 v[28:31], v[28:29], off nt
	s_bitset1_b32 s98, 1
.LBB0_422:
	s_add_i32 s2, s10, s2
	s_min_i32 s6, s2, s36
	s_add_i32 s2, s10, 2
	s_cmp_ge_i32 s2, s6
	s_cbranch_scc1 .LBB0_424
	s_ashr_i32 s3, s2, 31
	s_lshr_b32 s3, s3, 22
	s_add_i32 s3, s2, s3
	s_ashr_i32 s26, s3, 10
	s_and_b32 s3, s3, 0xfffffc00
	s_sub_i32 s7, s2, s3
	s_ashr_i32 s2, s7, 31
	s_lshr_b32 s2, s2, 26
	s_add_i32 s2, s7, s2
	s_ashr_i32 s28, s2, 6
	s_ashr_i32 s27, s26, 31
	s_lshl_b64 s[2:3], s[26:27], 25
	v_lshl_add_u32 v32, s28, 7, v72
	s_add_u32 s2, s80, s2
	v_ashrrev_i32_e32 v33, 31, v32
	s_addc_u32 s3, s81, s3
	v_lshlrev_b64 v[32:33], 14, v[32:33]
	v_lshl_add_u64 v[32:33], s[2:3], 0, v[32:33]
	s_lshl_b32 s2, s28, 12
	s_lshl_b32 s3, s7, 6
	s_sub_i32 s2, s3, s2
	s_ashr_i32 s3, s2, 31
	v_lshl_add_u64 v[32:33], s[2:3], 2, v[32:33]
	v_mov_b32_e32 v69, v65
	v_lshl_add_u64 v[40:41], v[32:33], 0, v[68:69]
	v_add_co_u32_e32 v36, vcc, 0x4000, v40
	s_nop 1
	v_addc_co_u32_e32 v37, vcc, 0, v41, vcc
	v_add_co_u32_e32 v42, vcc, 0x8000, v40
	global_load_dwordx4 v[32:35], v[40:41], off nt
	s_nop 0
	global_load_dwordx4 v[36:39], v[36:37], off nt
	v_addc_co_u32_e32 v43, vcc, 0, v41, vcc
	v_add_co_u32_e32 v44, vcc, 0xc000, v40
	s_nop 1
	v_addc_co_u32_e32 v45, vcc, 0, v41, vcc
	global_load_dwordx4 v[40:43], v[42:43], off nt
	s_nop 0
	global_load_dwordx4 v[44:47], v[44:45], off nt
	s_bitset1_b32 s98, 2
.LBB0_424:
	s_add_i32 s2, s10, 3
	s_cmp_ge_i32 s2, s6
	s_cbranch_scc1 .LBB0_426
	s_ashr_i32 s3, s2, 31
	s_lshr_b32 s3, s3, 22
	s_add_i32 s3, s2, s3
	s_ashr_i32 s26, s3, 10
	s_and_b32 s3, s3, 0xfffffc00
	s_sub_i32 s7, s2, s3
	s_ashr_i32 s2, s7, 31
	s_lshr_b32 s2, s2, 26
	s_add_i32 s2, s7, s2
	s_ashr_i32 s10, s2, 6
	s_ashr_i32 s27, s26, 31
	s_lshl_b64 s[2:3], s[26:27], 25
	v_lshl_add_u32 v48, s10, 7, v72
	s_add_u32 s2, s80, s2
	v_ashrrev_i32_e32 v49, 31, v48
	s_addc_u32 s3, s81, s3
	v_lshlrev_b64 v[48:49], 14, v[48:49]
	v_lshl_add_u64 v[48:49], s[2:3], 0, v[48:49]
	s_lshl_b32 s2, s10, 12
	s_lshl_b32 s3, s7, 6
	s_sub_i32 s2, s3, s2
	s_ashr_i32 s3, s2, 31
	v_lshl_add_u64 v[48:49], s[2:3], 2, v[48:49]
	v_mov_b32_e32 v69, v65
	v_lshl_add_u64 v[56:57], v[48:49], 0, v[68:69]
	v_add_co_u32_e32 v52, vcc, 0x4000, v56
	s_nop 1
	v_addc_co_u32_e32 v53, vcc, 0, v57, vcc
	v_add_co_u32_e32 v58, vcc, 0x8000, v56
	global_load_dwordx4 v[48:51], v[56:57], off nt
	s_nop 0
	global_load_dwordx4 v[52:55], v[52:53], off nt
	v_addc_co_u32_e32 v59, vcc, 0, v57, vcc
	v_add_co_u32_e32 v60, vcc, 0xc000, v56
	s_nop 1
	v_addc_co_u32_e32 v61, vcc, 0, v57, vcc
	global_load_dwordx4 v[56:59], v[58:59], off nt
	s_nop 0
	global_load_dwordx4 v[60:63], v[60:61], off nt
	s_bitset1_b32 s98, 3

.Lcvw_13:
	s_bitset0_b32 s98, 0
	s_add_i32 s2, s10, -7
	s_ashr_i32 s3, s2, 31
	s_lshr_b32 s3, s3, 22
	s_add_i32 s3, s2, s3
	v_mul_f32_e32 v64, 0x42800000, v0
	v_mul_f32_e32 v69, 0x42800000, v4
	v_mov_b32_e32 v78, v65
	s_ashr_i32 s2, s3, 10
	s_and_b32 s3, s3, 0xfffffc00
	v_cvt_pk_fp8_f32 v78, v64, v69
	v_mul_f32_e32 v64, 0x42800000, v1
	v_mul_f32_e32 v69, 0x42800000, v5
	v_mov_b32_e32 v79, v65
	s_sub_i32 s3, s10, s3
	v_cvt_pk_fp8_f32 v79, v64, v69
	s_add_i32 s3, s3, -7
	s_ashr_i32 s27, s3, 31
	s_lshr_b32 s27, s27, 26
	v_mul_f32_e32 v64, 0x42800000, v9
	v_mul_f32_e32 v69, 0x42800000, v13
	s_add_i32 s3, s3, s27
	v_cvt_pk_fp8_f32 v79, v64, v69 op_sel:[0,0,1]
	v_mul_f32_e32 v64, 0x42800000, v2
	v_mul_f32_e32 v69, 0x42800000, v6
	v_mov_b32_e32 v80, v65
	s_ashr_i32 s27, s3, 6
	s_ashr_i32 s3, s2, 31
	v_cvt_pk_fp8_f32 v80, v64, v69
	v_mul_f32_e32 v64, 0x42800000, v3
	v_mul_f32_e32 v69, 0x42800000, v7
	v_mov_b32_e32 v81, v65
	s_lshl_b64 s[28:29], s[2:3], 23
	v_cvt_pk_fp8_f32 v81, v64, v69
	s_add_u32 s30, s74, s28
	s_addc_u32 s31, s75, s29
	s_lshl_b32 s3, s27, 9
	s_lshl_b32 s2, s2, 13
	v_mul_f32_e32 v76, 0x42800000, v8
	v_mul_f32_e32 v77, 0x42800000, v12
	s_add_i32 s3, s3, s2
	s_add_i32 s29, s11, s26
	v_cvt_pk_fp8_f32 v78, v76, v77 op_sel:[0,0,1]
	v_mul_f32_e32 v76, 0x42800000, v10
	v_mul_f32_e32 v77, 0x42800000, v14
	v_mul_f32_e32 v64, 0x42800000, v11
	v_mul_f32_e32 v69, 0x42800000, v15
	s_sub_i32 s2, s29, s3
	v_cvt_pk_fp8_f32 v80, v76, v77 op_sel:[0,0,1]
	v_cvt_pk_fp8_f32 v81, v64, v69 op_sel:[0,0,1]
	s_and_b32 s2, s2, -16
	s_add_i32 s2, s2, s27
	v_add_u32_e32 v76, v74, v66
	s_ashr_i32 s3, s2, 31
	s_add_i32 s28, s19, s7
	ds_write2_b32 v75, v78, v79 offset1:33
	ds_write2_b32 v75, v80, v81 offset0:66 offset1:99
	s_waitcnt lgkmcnt(0)
	s_barrier
	ds_read2_b32 v[78:79], v76 offset1:1
	ds_read2_b32 v[80:81], v76 offset0:2 offset1:3
	s_and_b32 s27, s28, 64
	s_lshl_b64 s[2:3], s[2:3], 14
	s_add_u32 s2, s30, s2
	v_add_lshl_u32 v64, s27, v71, 7
	s_addc_u32 s3, s31, s3
	v_lshl_add_u64 v[82:83], s[2:3], 0, v[64:65]
	s_add_i32 s27, s10, -3
	v_lshl_add_u64 v[82:83], v[82:83], 0, v[66:67]
	s_cmp_ge_i32 s27, s6
	s_waitcnt lgkmcnt(0)
	global_store_dwordx4 v[82:83], v[78:81], off nt
	s_cbranch_scc1 .LBB0_431
	s_ashr_i32 s2, s27, 31
	s_lshr_b32 s2, s2, 22
	s_add_i32 s3, s27, s2
	s_ashr_i32 s2, s3, 10
	s_and_b32 s3, s3, 0xfffffc00
	s_sub_i32 s3, s10, s3
	s_add_i32 s3, s3, -3
	s_ashr_i32 s30, s3, 31
	s_lshr_b32 s30, s30, 26
	s_add_i32 s3, s3, s30
	s_ashr_i32 s34, s3, 6
	s_ashr_i32 s3, s2, 31
	s_lshl_b64 s[30:31], s[2:3], 25
	s_add_u32 s30, s80, s30
	s_addc_u32 s31, s81, s31
	s_lshl_b32 s3, s34, 12
	s_lshl_b32 s2, s2, 16
	v_lshl_add_u32 v0, s34, 7, v72
	s_add_i32 s3, s3, s2
	v_ashrrev_i32_e32 v1, 31, v0
	s_sub_i32 s2, s28, s3
	v_lshlrev_b64 v[0:1], 14, v[0:1]
	s_addk_i32 s2, 0x100
	v_lshl_add_u64 v[0:1], s[30:31], 0, v[0:1]
	s_ashr_i32 s3, s2, 31
	v_lshl_add_u64 v[0:1], s[2:3], 2, v[0:1]
	v_mov_b32_e32 v69, v65
	v_lshl_add_u64 v[8:9], v[0:1], 0, v[68:69]
	v_add_co_u32_e32 v4, vcc, s23, v8
	s_nop 1
	v_addc_co_u32_e32 v5, vcc, 0, v9, vcc
	v_add_co_u32_e32 v10, vcc, s24, v8
	global_load_dwordx4 v[0:3], v[8:9], off nt
	s_nop 0
	global_load_dwordx4 v[4:7], v[4:5], off nt
	v_addc_co_u32_e32 v11, vcc, 0, v9, vcc
	v_add_co_u32_e32 v12, vcc, s25, v8
	s_nop 1
	v_addc_co_u32_e32 v13, vcc, 0, v9, vcc
	global_load_dwordx4 v[8:11], v[10:11], off nt
	s_nop 0
	global_load_dwordx4 v[12:15], v[12:13], off nt
	s_bitset1_b32 s98, 0
.LBB0_431:
	s_add_i32 s30, s10, -6
	s_cmp_ge_i32 s30, s6
	s_mov_b64 s[2:3], -1
	s_cbranch_scc1 .LBB0_428
	s_waitcnt vmcnt(12)
	s_cmp_eq_u32 s98, 15
	s_cbranch_scc1 .Lcvw_14
	s_waitcnt vmcnt(0)
.Lcvw_14:
	s_bitset0_b32 s98, 1
	s_ashr_i32 s2, s30, 31
	s_lshr_b32 s2, s2, 22
	s_add_i32 s30, s30, s2
	s_and_b32 s3, s30, 0xfffffc00
	v_mul_f32_e32 v69, 0x42800000, v16
	v_mul_f32_e32 v77, 0x42800000, v20
	v_mov_b32_e32 v80, v65
	s_sub_i32 s3, s10, s3
	v_cvt_pk_fp8_f32 v80, v69, v77
	v_mul_f32_e32 v69, 0x42800000, v17
	v_mul_f32_e32 v77, 0x42800000, v21
	v_mov_b32_e32 v81, v65
	s_add_i32 s3, s3, -6
	v_cvt_pk_fp8_f32 v81, v69, v77
	s_ashr_i32 s2, s30, 10
	s_ashr_i32 s30, s3, 31
	s_lshr_b32 s30, s30, 26
	s_add_i32 s3, s3, s30
	v_mul_f32_e32 v69, 0x42800000, v25
	v_mul_f32_e32 v77, 0x42800000, v29
	s_ashr_i32 s34, s3, 6
	s_ashr_i32 s3, s2, 31
	v_cvt_pk_fp8_f32 v81, v69, v77 op_sel:[0,0,1]
	v_mul_f32_e32 v69, 0x42800000, v18
	v_mul_f32_e32 v77, 0x42800000, v22
	v_mov_b32_e32 v82, v65
	s_lshl_b64 s[30:31], s[2:3], 23
	v_cvt_pk_fp8_f32 v82, v69, v77
	v_mul_f32_e32 v69, 0x42800000, v19
	v_mul_f32_e32 v77, 0x42800000, v23
	v_mov_b32_e32 v83, v65
	s_add_u32 s30, s74, s30
	v_cvt_pk_fp8_f32 v83, v69, v77
	s_addc_u32 s31, s75, s31
	s_lshl_b32 s3, s34, 9
	s_lshl_b32 s2, s2, 13
	s_add_i32 s3, s3, s2
	v_mul_f32_e32 v78, 0x42800000, v24
	v_mul_f32_e32 v79, 0x42800000, v28
	s_sub_i32 s2, s29, s3
	v_cvt_pk_fp8_f32 v80, v78, v79 op_sel:[0,0,1]
	v_mul_f32_e32 v78, 0x42800000, v26
	v_mul_f32_e32 v79, 0x42800000, v30
	v_mul_f32_e32 v69, 0x42800000, v27
	v_mul_f32_e32 v77, 0x42800000, v31
	s_add_i32 s2, s2, 8
	v_cvt_pk_fp8_f32 v82, v78, v79 op_sel:[0,0,1]
	v_cvt_pk_fp8_f32 v83, v69, v77 op_sel:[0,0,1]
	s_and_b32 s2, s2, -16
	s_add_i32 s2, s2, s34
	v_add_u32_e32 v77, 0x2000, v75
	v_add_u32_e32 v78, 0x2200, v76
	s_ashr_i32 s3, s2, 31
	s_add_i32 s34, s28, 64
	ds_write2_b32 v77, v80, v81 offset0:128 offset1:161
	ds_write2_b32 v77, v82, v83 offset0:194 offset1:227
	s_waitcnt lgkmcnt(0)
	s_barrier
	v_add_u32_e32 v79, 0x2208, v76
	ds_read2_b32 v[80:81], v78 offset1:1
	ds_read2_b32 v[82:83], v79 offset1:1
	s_and_b32 s34, s34, 64
	s_lshl_b64 s[2:3], s[2:3], 14
	s_add_u32 s2, s30, s2
	v_add_lshl_u32 v84, s34, v71, 7
	v_mov_b32_e32 v85, v65
	s_addc_u32 s3, s31, s3
	v_lshl_add_u64 v[84:85], s[2:3], 0, v[84:85]
	s_add_i32 s2, s10, -2
	v_lshl_add_u64 v[84:85], v[84:85], 0, v[66:67]
	s_cmp_ge_i32 s2, s6
	s_waitcnt lgkmcnt(0)
	global_store_dwordx4 v[84:85], v[80:83], off nt
	s_cbranch_scc1 .LBB0_434
	s_ashr_i32 s3, s2, 31
	s_lshr_b32 s3, s3, 22
	s_add_i32 s3, s2, s3
	s_ashr_i32 s2, s3, 10
	s_and_b32 s3, s3, 0xfffffc00
	s_sub_i32 s3, s10, s3
	s_add_i32 s3, s3, -2
	s_ashr_i32 s30, s3, 31
	s_lshr_b32 s30, s30, 26
	s_add_i32 s3, s3, s30
	s_ashr_i32 s34, s3, 6
	s_ashr_i32 s3, s2, 31
	s_lshl_b64 s[30:31], s[2:3], 25
	s_add_u32 s30, s80, s30
	s_addc_u32 s31, s81, s31
	s_lshl_b32 s3, s34, 12
	s_lshl_b32 s2, s2, 16
	v_lshl_add_u32 v16, s34, 7, v72
	s_add_i32 s3, s3, s2
	v_ashrrev_i32_e32 v17, 31, v16
	s_sub_i32 s2, s28, s3
	v_lshlrev_b64 v[16:17], 14, v[16:17]
	s_addk_i32 s2, 0x140
	v_lshl_add_u64 v[16:17], s[30:31], 0, v[16:17]
	s_ashr_i32 s3, s2, 31
	v_lshl_add_u64 v[16:17], s[2:3], 2, v[16:17]
	v_mov_b32_e32 v69, v65
	v_lshl_add_u64 v[24:25], v[16:17], 0, v[68:69]
	v_add_co_u32_e32 v20, vcc, s23, v24
	s_nop 1
	v_addc_co_u32_e32 v21, vcc, 0, v25, vcc
	v_add_co_u32_e32 v26, vcc, s24, v24
	global_load_dwordx4 v[16:19], v[24:25], off nt
	s_nop 0
	global_load_dwordx4 v[20:23], v[20:21], off nt
	v_addc_co_u32_e32 v27, vcc, 0, v25, vcc
	v_add_co_u32_e32 v28, vcc, s25, v24
	s_nop 1
	v_addc_co_u32_e32 v29, vcc, 0, v25, vcc
	global_load_dwordx4 v[24:27], v[26:27], off nt
	s_nop 0
	global_load_dwordx4 v[28:31], v[28:29], off nt
	s_bitset1_b32 s98, 1
.LBB0_434:
	s_add_i32 s30, s10, -5
	s_cmp_ge_i32 s30, s6
	s_mov_b64 s[2:3], -1
	s_cbranch_scc1 .LBB0_428
	s_waitcnt vmcnt(12)
	s_cmp_eq_u32 s98, 15
	s_cbranch_scc1 .Lcvw_15
	s_waitcnt vmcnt(0)
.Lcvw_15:
	s_bitset0_b32 s98, 2
	s_ashr_i32 s2, s30, 31
	s_lshr_b32 s2, s2, 22
	s_add_i32 s30, s30, s2
	s_and_b32 s3, s30, 0xfffffc00
	v_mul_f32_e32 v69, 0x42800000, v32
	v_mul_f32_e32 v80, 0x42800000, v36
	v_mov_b32_e32 v83, v65
	s_sub_i32 s3, s10, s3
	v_cvt_pk_fp8_f32 v83, v69, v80
	v_mul_f32_e32 v69, 0x42800000, v33
	v_mul_f32_e32 v80, 0x42800000, v37
	v_mov_b32_e32 v84, v65
	s_add_i32 s3, s3, -5
	v_cvt_pk_fp8_f32 v84, v69, v80
	s_ashr_i32 s2, s30, 10
	s_ashr_i32 s30, s3, 31
	s_lshr_b32 s30, s30, 26
	s_add_i32 s3, s3, s30
	v_mul_f32_e32 v69, 0x42800000, v41
	v_mul_f32_e32 v80, 0x42800000, v45
	s_ashr_i32 s34, s3, 6
	s_ashr_i32 s3, s2, 31
	v_cvt_pk_fp8_f32 v84, v69, v80 op_sel:[0,0,1]
	v_mul_f32_e32 v69, 0x42800000, v34
	v_mul_f32_e32 v80, 0x42800000, v38
	v_mov_b32_e32 v85, v65
	s_lshl_b64 s[30:31], s[2:3], 23
	v_cvt_pk_fp8_f32 v85, v69, v80
	v_mul_f32_e32 v69, 0x42800000, v35
	v_mul_f32_e32 v80, 0x42800000, v39
	v_mov_b32_e32 v86, v65
	s_add_u32 s30, s74, s30
	v_cvt_pk_fp8_f32 v86, v69, v80
	s_addc_u32 s31, s75, s31
	s_lshl_b32 s3, s34, 9
	s_lshl_b32 s2, s2, 13
	s_add_i32 s3, s3, s2
	v_mul_f32_e32 v81, 0x42800000, v40
	v_mul_f32_e32 v82, 0x42800000, v44
	s_sub_i32 s2, s29, s3
	v_cvt_pk_fp8_f32 v83, v81, v82 op_sel:[0,0,1]
	v_mul_f32_e32 v81, 0x42800000, v42
	v_mul_f32_e32 v82, 0x42800000, v46
	v_mul_f32_e32 v69, 0x42800000, v43
	v_mul_f32_e32 v80, 0x42800000, v47
	s_add_i32 s2, s2, 16
	v_cvt_pk_fp8_f32 v85, v81, v82 op_sel:[0,0,1]
	v_cvt_pk_fp8_f32 v86, v69, v80 op_sel:[0,0,1]
	s_and_b32 s2, s2, -16
	s_add_i32 s2, s2, s34
	s_ashr_i32 s3, s2, 31
	ds_write2_b32 v75, v83, v84 offset1:33
	ds_write2_b32 v75, v85, v86 offset0:66 offset1:99
	s_waitcnt lgkmcnt(0)
	s_barrier
	ds_read2_b32 v[80:81], v76 offset1:1
	ds_read2_b32 v[82:83], v76 offset0:2 offset1:3
	s_lshl_b64 s[2:3], s[2:3], 14
	s_add_u32 s2, s30, s2
	s_addc_u32 s3, s31, s3
	v_lshl_add_u64 v[84:85], s[2:3], 0, v[64:65]
	s_add_i32 s2, s10, -1
	v_lshl_add_u64 v[84:85], v[84:85], 0, v[66:67]
	s_cmp_ge_i32 s2, s6
	s_waitcnt lgkmcnt(0)
	global_store_dwordx4 v[84:85], v[80:83], off nt
	s_cbranch_scc1 .LBB0_437
	s_ashr_i32 s3, s2, 31
	s_lshr_b32 s3, s3, 22
	s_add_i32 s3, s2, s3
	s_ashr_i32 s2, s3, 10
	s_orn2_b32 s3, 0x3ff, s3
	s_add_i32 s3, s3, s10
	s_ashr_i32 s30, s3, 31
	s_lshr_b32 s30, s30, 26
	s_add_i32 s3, s3, s30
	s_ashr_i32 s34, s3, 6
	s_ashr_i32 s3, s2, 31
	s_lshl_b64 s[30:31], s[2:3], 25
	s_add_u32 s30, s80, s30
	s_addc_u32 s31, s81, s31
	s_lshl_b32 s3, s34, 12
	s_lshl_b32 s2, s2, 16
	v_lshl_add_u32 v32, s34, 7, v72
	s_add_i32 s3, s3, s2
	v_ashrrev_i32_e32 v33, 31, v32
	s_sub_i32 s2, s28, s3
	v_lshlrev_b64 v[32:33], 14, v[32:33]
	s_addk_i32 s2, 0x180
	v_lshl_add_u64 v[32:33], s[30:31], 0, v[32:33]
	s_ashr_i32 s3, s2, 31
	v_lshl_add_u64 v[32:33], s[2:3], 2, v[32:33]
	v_mov_b32_e32 v69, v65
	v_lshl_add_u64 v[40:41], v[32:33], 0, v[68:69]
	v_add_co_u32_e32 v36, vcc, 0x4000, v40
	s_nop 1
	v_addc_co_u32_e32 v37, vcc, 0, v41, vcc
	v_add_co_u32_e32 v42, vcc, 0x8000, v40
	global_load_dwordx4 v[32:35], v[40:41], off nt
	s_nop 0
	global_load_dwordx4 v[36:39], v[36:37], off nt
	v_addc_co_u32_e32 v43, vcc, 0, v41, vcc
	v_add_co_u32_e32 v44, vcc, 0xc000, v40
	s_nop 1
	v_addc_co_u32_e32 v45, vcc, 0, v41, vcc
	global_load_dwordx4 v[40:43], v[42:43], off nt
	s_nop 0
	global_load_dwordx4 v[44:47], v[44:45], off nt
	s_bitset1_b32 s98, 2
.LBB0_437:
	s_add_i32 s30, s10, -4
	s_cmp_ge_i32 s30, s6
	s_mov_b64 s[2:3], -1
	s_cbranch_scc1 .LBB0_428
	s_waitcnt vmcnt(12)
	s_cmp_eq_u32 s98, 15
	s_cbranch_scc1 .Lcvw_16
	s_waitcnt vmcnt(0)
.Lcvw_16:
	s_bitset0_b32 s98, 3
	s_ashr_i32 s2, s30, 31
	s_lshr_b32 s2, s2, 22
	s_add_i32 s30, s30, s2
	s_and_b32 s3, s30, 0xfffffc00
	v_mul_f32_e32 v64, 0x42800000, v48
	v_mul_f32_e32 v69, 0x42800000, v52
	v_mov_b32_e32 v81, v65
	s_sub_i32 s3, s10, s3
	v_cvt_pk_fp8_f32 v81, v64, v69
	v_mul_f32_e32 v64, 0x42800000, v49
	v_mul_f32_e32 v69, 0x42800000, v53
	v_mov_b32_e32 v82, v65
	s_add_i32 s3, s3, -4
	v_cvt_pk_fp8_f32 v82, v64, v69
	s_ashr_i32 s2, s30, 10
	s_ashr_i32 s30, s3, 31
	s_lshr_b32 s30, s30, 26
	s_add_i32 s3, s3, s30
	v_mul_f32_e32 v64, 0x42800000, v57
	v_mul_f32_e32 v69, 0x42800000, v61
	s_ashr_i32 s34, s3, 6
	s_ashr_i32 s3, s2, 31
	v_cvt_pk_fp8_f32 v82, v64, v69 op_sel:[0,0,1]
	v_mul_f32_e32 v64, 0x42800000, v50
	v_mul_f32_e32 v69, 0x42800000, v54
	v_mov_b32_e32 v83, v65
	s_lshl_b64 s[30:31], s[2:3], 23
	v_cvt_pk_fp8_f32 v83, v64, v69
	v_mul_f32_e32 v64, 0x42800000, v51
	v_mul_f32_e32 v69, 0x42800000, v55
	v_mov_b32_e32 v84, v65
	s_add_u32 s30, s74, s30
	v_cvt_pk_fp8_f32 v84, v64, v69
	s_addc_u32 s31, s75, s31
	s_lshl_b32 s3, s34, 9
	s_lshl_b32 s2, s2, 13
	s_add_i32 s3, s3, s2
	v_mul_f32_e32 v76, 0x42800000, v56
	v_mul_f32_e32 v80, 0x42800000, v60
	s_sub_i32 s2, s29, s3
	v_cvt_pk_fp8_f32 v81, v76, v80 op_sel:[0,0,1]
	v_mul_f32_e32 v76, 0x42800000, v58
	v_mul_f32_e32 v80, 0x42800000, v62
	v_mul_f32_e32 v64, 0x42800000, v59
	v_mul_f32_e32 v69, 0x42800000, v63
	s_add_i32 s2, s2, 24
	v_cvt_pk_fp8_f32 v83, v76, v80 op_sel:[0,0,1]
	v_cvt_pk_fp8_f32 v84, v64, v69 op_sel:[0,0,1]
	s_and_b32 s2, s2, -16
	s_add_i32 s2, s2, s34
	s_ashr_i32 s3, s2, 31
	s_add_i32 s29, s28, 0xc0
	ds_write2_b32 v77, v81, v82 offset0:128 offset1:161
	ds_write2_b32 v77, v83, v84 offset0:194 offset1:227
	s_waitcnt lgkmcnt(0)
	s_barrier
	ds_read2_b32 v[76:77], v78 offset1:1
	ds_read2_b32 v[78:79], v79 offset1:1
	s_and_b32 s29, s29, 64
	s_lshl_b64 s[2:3], s[2:3], 14
	s_add_u32 s2, s30, s2
	v_add_lshl_u32 v64, s29, v71, 7
	s_addc_u32 s3, s31, s3
	v_lshl_add_u64 v[80:81], s[2:3], 0, v[64:65]
	v_lshl_add_u64 v[80:81], v[80:81], 0, v[66:67]
	s_cmp_ge_i32 s10, s6
	s_waitcnt lgkmcnt(0)
	global_store_dwordx4 v[80:81], v[76:79], off nt
	s_cbranch_scc1 .LBB0_427
	s_ashr_i32 s2, s10, 31
	s_lshr_b32 s2, s2, 22
	s_add_i32 s3, s10, s2
	s_ashr_i32 s2, s3, 10
	s_and_b32 s3, s3, 0xfffffc00
	s_sub_i32 s3, s10, s3
	s_ashr_i32 s29, s3, 31
	s_lshr_b32 s29, s29, 26
	s_add_i32 s3, s3, s29
	s_ashr_i32 s29, s3, 6
	s_ashr_i32 s3, s2, 31
	s_lshl_b64 s[30:31], s[2:3], 25
	s_add_u32 s30, s80, s30
	s_addc_u32 s31, s81, s31
	s_lshl_b32 s3, s29, 12
	s_lshl_b32 s2, s2, 16
	v_lshl_add_u32 v48, s29, 7, v72
	s_add_i32 s3, s3, s2
	v_ashrrev_i32_e32 v49, 31, v48
	s_sub_i32 s2, s28, s3
	v_lshlrev_b64 v[48:49], 14, v[48:49]
	s_addk_i32 s2, 0x1c0
	v_lshl_add_u64 v[48:49], s[30:31], 0, v[48:49]
	s_ashr_i32 s3, s2, 31
	v_lshl_add_u64 v[48:49], s[2:3], 2, v[48:49]
	v_mov_b32_e32 v69, v65
	v_lshl_add_u64 v[56:57], v[48:49], 0, v[68:69]
	v_add_co_u32_e32 v52, vcc, 0x4000, v56
	s_nop 1
	v_addc_co_u32_e32 v53, vcc, 0, v57, vcc
	v_add_co_u32_e32 v58, vcc, 0x8000, v56
	global_load_dwordx4 v[48:51], v[56:57], off nt
	s_nop 0
	global_load_dwordx4 v[52:55], v[52:53], off nt
	v_addc_co_u32_e32 v59, vcc, 0, v57, vcc
	v_add_co_u32_e32 v60, vcc, 0xc000, v56
	s_nop 1
	v_addc_co_u32_e32 v61, vcc, 0, v57, vcc
	global_load_dwordx4 v[56:59], v[58:59], off nt
	s_nop 0
	global_load_dwordx4 v[60:63], v[60:61], off nt
	s_bitset1_b32 s98, 3
	s_branch .LBB0_427
.LBB0_440:
	s_cmp_lt_i32 s94, 6
	s_cselect_b64 s[0:1], -1, 0
	s_cmp_gt_i32 s95, 5
	s_cselect_b64 s[2:3], -1, 0
	s_and_b64 s[0:1], s[0:1], s[2:3]
	s_and_b64 s[2:3], s[72:73], s[0:1]
	s_andn2_b64 vcc, exec, s[2:3]
	s_cbranch_vccnz .LBB0_449
	s_lshr_b32 s2, s96, 31
	s_add_i32 s2, s96, s2
	s_ashr_i32 s6, s2, 1
	s_add_i32 s7, s36, s76
	s_mul_i32 s10, s6, 14
	s_waitcnt vmcnt(0)
	v_lshrrev_b32_e32 v1, 4, v178
	v_and_b32_e32 v66, 15, v178
	s_cmp_lt_i32 s76, s10
	s_waitcnt lgkmcnt(0)
	v_mov_b32_e32 v0, 0
	s_cselect_b64 s[2:3], -1, 0
	s_cmp_ge_i32 s76, s10
	v_lshlrev_b32_e32 v69, 2, v1
	v_lshlrev_b32_e32 v64, 4, v66
	v_mov_b32_e32 v4, 0
	v_mov_b32_e32 v5, 0
	v_mov_b32_e32 v6, 0
	v_mov_b32_e32 v7, 0
	v_mov_b32_e32 v8, 0
	v_mov_b32_e32 v9, 0
	v_mov_b32_e32 v10, 0
	v_mov_b32_e32 v11, 0
	v_mov_b32_e32 v12, 0
	v_mov_b32_e32 v13, 0
	v_mov_b32_e32 v14, 0
	v_mov_b32_e32 v15, 0
	v_mov_b32_e32 v16, 0
	v_mov_b32_e32 v17, 0
	v_mov_b32_e32 v18, 0
	v_mov_b32_e32 v19, 0
	s_mov_b32 s98, 0
	s_barrier
	s_cbranch_scc1 .LBB0_443
	s_ashr_i32 s11, s7, 31
	s_lshr_b32 s11, s11, 22
	s_add_i32 s11, s7, s11
	s_ashr_i32 s12, s11, 10
	s_and_b32 s11, s11, 0xfffffc00
	s_sub_i32 s11, s7, s11
	s_ashr_i32 s13, s11, 31
	s_lshr_b32 s13, s13, 26
	s_add_i32 s13, s11, s13
	s_ashr_i32 s16, s13, 6
	s_ashr_i32 s13, s12, 31
	s_lshl_b64 s[12:13], s[12:13], 25
	v_lshl_add_u32 v2, s16, 7, v69
	s_add_u32 s12, s80, s12
	v_ashrrev_i32_e32 v3, 31, v2
	s_addc_u32 s13, s81, s13
	v_lshlrev_b64 v[2:3], 14, v[2:3]
	v_lshl_add_u64 v[2:3], s[12:13], 0, v[2:3]
	s_lshl_b32 s12, s16, 12
	s_lshl_b32 s11, s11, 6
	s_sub_i32 s12, s11, s12
	s_ashr_i32 s13, s12, 31
	v_lshl_add_u64 v[2:3], s[12:13], 2, v[2:3]
	v_mov_b32_e32 v65, 0
	v_lshl_add_u64 v[2:3], v[2:3], 0, v[64:65]
	s_movk_i32 s11, 0x4000
	v_add_co_u32_e32 v12, vcc, s11, v2
	s_mov_b32 s11, 0x8000
	s_nop 0
	v_addc_co_u32_e32 v13, vcc, 0, v3, vcc
	global_load_dwordx4 v[4:7], v[2:3], off nt
	global_load_dwordx4 v[8:11], v[12:13], off nt
	v_add_co_u32_e32 v12, vcc, s11, v2
	s_mov_b32 s11, 0xc000
	s_nop 0
	v_addc_co_u32_e32 v13, vcc, 0, v3, vcc
	v_add_co_u32_e32 v2, vcc, s11, v2
	s_nop 1
	v_addc_co_u32_e32 v3, vcc, 0, v3, vcc
	global_load_dwordx4 v[12:15], v[12:13], off nt
	s_nop 0
	global_load_dwordx4 v[16:19], v[2:3], off nt
	s_bitset1_b32 s98, 0
.LBB0_443:
	s_add_i32 s10, s10, s36
	s_add_i32 s11, s7, s6
	s_cmp_ge_i32 s11, s10
	v_mov_b32_e32 v1, 0
	v_mov_b32_e32 v2, 0
	v_mov_b32_e32 v3, 0
	v_mov_b32_e32 v20, 0
	v_mov_b32_e32 v21, 0
	v_mov_b32_e32 v22, 0
	v_mov_b32_e32 v23, 0
	v_mov_b32_e32 v24, 0
	v_mov_b32_e32 v25, 0
	v_mov_b32_e32 v26, 0
	v_mov_b32_e32 v27, 0
	v_mov_b32_e32 v28, 0
	v_mov_b32_e32 v29, 0
	v_mov_b32_e32 v30, 0
	v_mov_b32_e32 v31, 0
	s_cbranch_scc1 .LBB0_445
	s_ashr_i32 s12, s11, 31
	s_lshr_b32 s12, s12, 22
	s_add_i32 s13, s11, s12
	s_ashr_i32 s12, s13, 10
	s_and_b32 s13, s13, 0xfffffc00
	s_sub_i32 s16, s11, s13
	s_ashr_i32 s13, s16, 31
	s_lshr_b32 s13, s13, 26
	s_add_i32 s13, s16, s13
	s_ashr_i32 s17, s13, 6
	s_ashr_i32 s13, s12, 31
	s_lshl_b64 s[12:13], s[12:13], 25
	v_lshl_add_u32 v0, s17, 7, v69
	s_add_u32 s12, s80, s12
	v_ashrrev_i32_e32 v1, 31, v0
	s_addc_u32 s13, s81, s13
	v_lshlrev_b64 v[0:1], 14, v[0:1]
	v_lshl_add_u64 v[0:1], s[12:13], 0, v[0:1]
	s_lshl_b32 s12, s17, 12
	s_lshl_b32 s13, s16, 6
	s_sub_i32 s12, s13, s12
	s_ashr_i32 s13, s12, 31
	v_lshl_add_u64 v[0:1], s[12:13], 2, v[0:1]
	v_mov_b32_e32 v65, 0
	v_lshl_add_u64 v[24:25], v[0:1], 0, v[64:65]
	s_movk_i32 s12, 0x4000
	v_add_co_u32_e32 v26, vcc, s12, v24
	s_mov_b32 s12, 0x8000
	s_nop 0
	v_addc_co_u32_e32 v27, vcc, 0, v25, vcc
	global_load_dwordx4 v[0:3], v[24:25], off nt
	global_load_dwordx4 v[20:23], v[26:27], off nt
	v_add_co_u32_e32 v26, vcc, s12, v24
	s_mov_b32 s12, 0xc000
	s_nop 0
	v_addc_co_u32_e32 v27, vcc, 0, v25, vcc
	v_add_co_u32_e32 v28, vcc, s12, v24
	s_nop 1
	v_addc_co_u32_e32 v29, vcc, 0, v25, vcc
	global_load_dwordx4 v[24:27], v[26:27], off nt
	s_nop 0
	global_load_dwordx4 v[28:31], v[28:29], off nt
	s_bitset1_b32 s98, 1
.LBB0_445:
	s_add_i32 s11, s11, s6
	s_cmp_ge_i32 s11, s10
	s_cbranch_scc1 .LBB0_447
	s_ashr_i32 s12, s11, 31
	s_lshr_b32 s12, s12, 22
	s_add_i32 s13, s11, s12
	s_ashr_i32 s12, s13, 10
	s_and_b32 s13, s13, 0xfffffc00
	s_sub_i32 s16, s11, s13
	s_ashr_i32 s13, s16, 31
	s_lshr_b32 s13, s13, 26
	s_add_i32 s13, s16, s13
	s_ashr_i32 s17, s13, 6
	s_ashr_i32 s13, s12, 31
	s_lshl_b64 s[12:13], s[12:13], 25
	v_lshl_add_u32 v32, s17, 7, v69
	s_add_u32 s12, s80, s12
	v_ashrrev_i32_e32 v33, 31, v32
	s_addc_u32 s13, s81, s13
	v_lshlrev_b64 v[32:33], 14, v[32:33]
	v_lshl_add_u64 v[32:33], s[12:13], 0, v[32:33]
	s_lshl_b32 s12, s17, 12
	s_lshl_b32 s13, s16, 6
	s_sub_i32 s12, s13, s12
	s_ashr_i32 s13, s12, 31
	v_lshl_add_u64 v[32:33], s[12:13], 2, v[32:33]
	v_mov_b32_e32 v65, 0
	v_lshl_add_u64 v[40:41], v[32:33], 0, v[64:65]
	s_movk_i32 s12, 0x4000
	v_add_co_u32_e32 v42, vcc, s12, v40
	s_nop 1
	v_addc_co_u32_e32 v43, vcc, 0, v41, vcc
	global_load_dwordx4 v[32:35], v[40:41], off nt
	global_load_dwordx4 v[36:39], v[42:43], off nt
	v_add_co_u32_e32 v42, vcc, 0x8000, v40
	s_nop 1
	v_addc_co_u32_e32 v43, vcc, 0, v41, vcc
	v_add_co_u32_e32 v44, vcc, 0xc000, v40
	s_nop 1
	v_addc_co_u32_e32 v45, vcc, 0, v41, vcc
	global_load_dwordx4 v[40:43], v[42:43], off nt
	s_nop 0
	global_load_dwordx4 v[44:47], v[44:45], off nt
	s_bitset1_b32 s98, 2
.LBB0_447:
	s_add_i32 s11, s11, s6
	s_cmp_ge_i32 s11, s10
	s_cbranch_scc1 .LBB0_460
	s_ashr_i32 s12, s11, 31
	s_lshr_b32 s12, s12, 22
	s_add_i32 s13, s11, s12
	s_ashr_i32 s12, s13, 10
	s_and_b32 s13, s13, 0xfffffc00
	s_sub_i32 s11, s11, s13
	s_ashr_i32 s13, s11, 31
	s_lshr_b32 s13, s13, 26
	s_add_i32 s13, s11, s13
	s_ashr_i32 s16, s13, 6
	s_ashr_i32 s13, s12, 31
	s_lshl_b64 s[12:13], s[12:13], 25
	v_lshl_add_u32 v48, s16, 7, v69
	s_add_u32 s12, s80, s12
	v_ashrrev_i32_e32 v49, 31, v48
	s_addc_u32 s13, s81, s13
	v_lshlrev_b64 v[48:49], 14, v[48:49]
	v_lshl_add_u64 v[48:49], s[12:13], 0, v[48:49]
	s_lshl_b32 s12, s16, 12
	s_lshl_b32 s11, s11, 6
	s_sub_i32 s12, s11, s12
	s_ashr_i32 s13, s12, 31
	v_lshl_add_u64 v[48:49], s[12:13], 2, v[48:49]
	v_mov_b32_e32 v65, 0
	v_lshl_add_u64 v[56:57], v[48:49], 0, v[64:65]
	s_movk_i32 s11, 0x4000
	v_add_co_u32_e32 v58, vcc, s11, v56
	s_nop 1
	v_addc_co_u32_e32 v59, vcc, 0, v57, vcc
	global_load_dwordx4 v[48:51], v[56:57], off nt
	global_load_dwordx4 v[52:55], v[58:59], off nt
	v_add_co_u32_e32 v58, vcc, 0x8000, v56
	s_nop 1
	v_addc_co_u32_e32 v59, vcc, 0, v57, vcc
	v_add_co_u32_e32 v60, vcc, 0xc000, v56
	s_nop 1
	v_addc_co_u32_e32 v61, vcc, 0, v57, vcc
	global_load_dwordx4 v[56:59], v[58:59], off nt
	s_nop 0
	global_load_dwordx4 v[60:63], v[60:61], off nt
	s_bitset1_b32 s98, 3
	s_andn2_b64 vcc, exec, s[2:3]
	s_cbranch_vccnz .LBB0_475
	s_branch .LBB0_461

.Lcvw_17:
	s_bitset0_b32 s98, 0
	s_ashr_i32 s2, s7, 31
	s_lshr_b32 s2, s2, 22
	v_mul_f32_e32 v66, 0x42800000, v4
	v_mul_f32_e32 v74, 0x42800000, v8
	v_mov_b32_e32 v77, 0
	s_add_i32 s3, s7, s2
	v_cvt_pk_fp8_f32 v77, v66, v74
	v_mul_f32_e32 v66, 0x42800000, v5
	v_mul_f32_e32 v74, 0x42800000, v9
	v_mov_b32_e32 v78, 0
	s_ashr_i32 s2, s3, 10
	s_and_b32 s3, s3, 0xfffffc00
	v_cvt_pk_fp8_f32 v78, v66, v74
	s_sub_i32 s3, s7, s3
	s_ashr_i32 s41, s3, 31
	s_lshr_b32 s41, s41, 26
	v_mul_f32_e32 v66, 0x42800000, v13
	v_mul_f32_e32 v74, 0x42800000, v17
	s_add_i32 s3, s3, s41
	v_cvt_pk_fp8_f32 v78, v66, v74 op_sel:[0,0,1]
	v_mul_f32_e32 v66, 0x42800000, v6
	v_mul_f32_e32 v74, 0x42800000, v10
	v_mov_b32_e32 v79, 0
	s_ashr_i32 s41, s3, 6
	s_ashr_i32 s3, s2, 31
	v_cvt_pk_fp8_f32 v79, v66, v74
	v_mul_f32_e32 v66, 0x42800000, v7
	v_mul_f32_e32 v74, 0x42800000, v11
	v_mov_b32_e32 v80, 0
	s_lshl_b64 s[42:43], s[2:3], 23
	v_cvt_pk_fp8_f32 v80, v66, v74
	s_add_u32 s42, s74, s42
	s_addc_u32 s43, s75, s43
	s_lshl_b32 s3, s41, 9
	s_lshl_b32 s2, s2, 13
	v_mul_f32_e32 v75, 0x42800000, v12
	v_mul_f32_e32 v76, 0x42800000, v16
	s_add_i32 s3, s3, s2
	s_add_i32 s2, s17, s19
	v_cvt_pk_fp8_f32 v77, v75, v76 op_sel:[0,0,1]
	v_mul_f32_e32 v75, 0x42800000, v14
	v_mul_f32_e32 v76, 0x42800000, v18
	v_mul_f32_e32 v66, 0x42800000, v15
	v_mul_f32_e32 v74, 0x42800000, v19
	s_sub_i32 s2, s2, s3
	v_cvt_pk_fp8_f32 v79, v75, v76 op_sel:[0,0,1]
	v_cvt_pk_fp8_f32 v80, v66, v74 op_sel:[0,0,1]
	s_and_b32 s2, s2, -16
	s_add_i32 s2, s2, s41
	s_ashr_i32 s3, s2, 31
	s_add_i32 s41, s12, s13
	ds_write2_b32 v72, v77, v78 offset1:33
	ds_write2_b32 v72, v79, v80 offset0:66 offset1:99
	s_waitcnt lgkmcnt(0)
	s_barrier
	ds_read2_b32 v[74:75], v73 offset1:1
	ds_read2_b32 v[76:77], v73 offset0:2 offset1:3
	s_and_b32 s41, s41, 64
	s_lshl_b64 s[2:3], s[2:3], 14
	s_add_u32 s2, s42, s2
	v_add_lshl_u32 v66, s41, v71, 7
	s_addc_u32 s3, s43, s3
	v_lshl_add_u64 v[78:79], s[2:3], 0, v[66:67]
	s_add_i32 s2, s11, s7
	v_lshl_add_u64 v[78:79], v[78:79], 0, v[64:65]
	s_cmp_ge_i32 s2, s10
	s_waitcnt lgkmcnt(0)
	global_store_dwordx4 v[78:79], v[74:77], off nt
	s_cbranch_scc1 .LBB0_466
	s_ashr_i32 s3, s2, 31
	s_lshr_b32 s3, s3, 22
	s_add_i32 s3, s2, s3
	s_ashr_i32 s42, s3, 10
	s_and_b32 s3, s3, 0xfffffc00
	s_sub_i32 s2, s2, s3
	s_ashr_i32 s3, s2, 31
	s_lshr_b32 s3, s3, 26
	s_add_i32 s2, s2, s3
	s_ashr_i32 s41, s2, 6
	s_ashr_i32 s43, s42, 31
	s_lshl_b64 s[2:3], s[42:43], 25
	v_lshl_add_u32 v4, s41, 7, v69
	s_add_u32 s2, s80, s2
	v_ashrrev_i32_e32 v5, 31, v4
	s_addc_u32 s3, s81, s3
	v_lshlrev_b64 v[4:5], 14, v[4:5]
	v_lshl_add_u64 v[4:5], s[2:3], 0, v[4:5]
	s_lshl_b32 s2, s41, 12
	s_lshl_b32 s3, s42, 16
	s_add_i32 s2, s2, s3
	s_add_i32 s3, s37, s13
	s_sub_i32 s2, s3, s2
	s_ashr_i32 s3, s2, 31
	v_lshl_add_u64 v[4:5], s[2:3], 2, v[4:5]
	v_lshlrev_b32_e32 v66, 2, v68
	v_lshl_add_u64 v[12:13], v[4:5], 0, v[66:67]
	v_add_co_u32_e32 v8, vcc, s38, v12
	s_nop 1
	v_addc_co_u32_e32 v9, vcc, 0, v13, vcc
	v_add_co_u32_e32 v14, vcc, s39, v12
	global_load_dwordx4 v[4:7], v[12:13], off nt
	s_nop 0
	global_load_dwordx4 v[8:11], v[8:9], off nt
	v_addc_co_u32_e32 v15, vcc, 0, v13, vcc
	v_add_co_u32_e32 v16, vcc, s40, v12
	s_nop 1
	v_addc_co_u32_e32 v17, vcc, 0, v13, vcc
	global_load_dwordx4 v[12:15], v[14:15], off nt
	s_nop 0
	global_load_dwordx4 v[16:19], v[16:17], off nt
	s_bitset1_b32 s98, 0
.LBB0_466:
	s_add_i32 s41, s7, s6
	s_cmp_ge_i32 s41, s10
	s_mov_b64 s[2:3], -1
	s_cbranch_scc1 .LBB0_463
	s_waitcnt vmcnt(12)
	s_cmp_eq_u32 s98, 15
	s_cbranch_scc1 .Lcvw_18
	s_waitcnt vmcnt(0)
.Lcvw_18:
	s_bitset0_b32 s98, 1
	s_ashr_i32 s2, s41, 31
	s_lshr_b32 s2, s2, 22
	v_mul_f32_e32 v66, 0x42800000, v0
	v_mul_f32_e32 v74, 0x42800000, v20
	v_mov_b32_e32 v77, v67
	s_add_i32 s3, s41, s2
	v_cvt_pk_fp8_f32 v77, v66, v74
	v_mul_f32_e32 v66, 0x42800000, v1
	v_mul_f32_e32 v74, 0x42800000, v21
	v_mov_b32_e32 v78, v67
	s_ashr_i32 s2, s3, 10
	s_and_b32 s3, s3, 0xfffffc00
	v_cvt_pk_fp8_f32 v78, v66, v74
	s_sub_i32 s3, s41, s3
	s_ashr_i32 s42, s3, 31
	s_lshr_b32 s42, s42, 26
	v_mul_f32_e32 v66, 0x42800000, v25
	v_mul_f32_e32 v74, 0x42800000, v29
	s_add_i32 s3, s3, s42
	v_cvt_pk_fp8_f32 v78, v66, v74 op_sel:[0,0,1]
	v_mul_f32_e32 v66, 0x42800000, v2
	v_mul_f32_e32 v74, 0x42800000, v22
	v_mov_b32_e32 v79, v67
	s_ashr_i32 s44, s3, 6
	s_ashr_i32 s3, s2, 31
	v_cvt_pk_fp8_f32 v79, v66, v74
	v_mul_f32_e32 v66, 0x42800000, v3
	v_mul_f32_e32 v74, 0x42800000, v23
	v_mov_b32_e32 v80, v67
	s_lshl_b64 s[42:43], s[2:3], 23
	v_cvt_pk_fp8_f32 v80, v66, v74
	s_add_u32 s42, s74, s42
	s_addc_u32 s43, s75, s43
	s_lshl_b32 s3, s44, 9
	s_lshl_b32 s2, s2, 13
	v_mul_f32_e32 v75, 0x42800000, v24
	v_mul_f32_e32 v76, 0x42800000, v28
	s_add_i32 s3, s3, s2
	s_add_i32 s2, s18, s19
	v_cvt_pk_fp8_f32 v77, v75, v76 op_sel:[0,0,1]
	v_mul_f32_e32 v75, 0x42800000, v26
	v_mul_f32_e32 v76, 0x42800000, v30
	v_mul_f32_e32 v66, 0x42800000, v27
	v_mul_f32_e32 v74, 0x42800000, v31
	s_sub_i32 s2, s2, s3
	v_cvt_pk_fp8_f32 v79, v75, v76 op_sel:[0,0,1]
	v_cvt_pk_fp8_f32 v80, v66, v74 op_sel:[0,0,1]
	s_and_b32 s2, s2, -16
	s_add_i32 s2, s2, s44
	v_add_u32_e32 v74, 0x2000, v72
	v_add_u32_e32 v75, 0x2200, v73
	s_ashr_i32 s3, s2, 31
	s_add_i32 s44, s21, s13
	ds_write2_b32 v74, v77, v78 offset0:128 offset1:161
	ds_write2_b32 v74, v79, v80 offset0:194 offset1:227
	s_waitcnt lgkmcnt(0)
	s_barrier
	v_add_u32_e32 v76, 0x2208, v73
	ds_read2_b32 v[78:79], v75 offset1:1
	ds_read2_b32 v[80:81], v76 offset1:1
	s_and_b32 s44, s44, 64
	s_lshl_b64 s[2:3], s[2:3], 14
	s_add_u32 s2, s42, s2
	v_add_lshl_u32 v66, s44, v71, 7
	s_addc_u32 s3, s43, s3
	v_lshl_add_u64 v[82:83], s[2:3], 0, v[66:67]
	s_add_i32 s2, s22, s7
	v_lshl_add_u64 v[82:83], v[82:83], 0, v[64:65]
	s_cmp_ge_i32 s2, s10
	s_waitcnt lgkmcnt(0)
	global_store_dwordx4 v[82:83], v[78:81], off nt
	s_cbranch_scc1 .LBB0_469
	s_ashr_i32 s3, s2, 31
	s_lshr_b32 s3, s3, 22
	s_add_i32 s3, s2, s3
	s_ashr_i32 s42, s3, 10
	s_and_b32 s3, s3, 0xfffffc00
	s_sub_i32 s2, s2, s3
	s_ashr_i32 s3, s2, 31
	s_lshr_b32 s3, s3, 26
	s_add_i32 s2, s2, s3
	s_ashr_i32 s44, s2, 6
	s_ashr_i32 s43, s42, 31
	s_lshl_b64 s[2:3], s[42:43], 25
	v_lshl_add_u32 v0, s44, 7, v69
	s_add_u32 s2, s80, s2
	v_ashrrev_i32_e32 v1, 31, v0
	s_addc_u32 s3, s81, s3
	v_lshlrev_b64 v[0:1], 14, v[0:1]
	v_lshl_add_u64 v[0:1], s[2:3], 0, v[0:1]
	s_lshl_b32 s2, s44, 12
	s_lshl_b32 s3, s42, 16
	s_add_i32 s2, s2, s3
	s_add_i32 s3, s23, s13
	s_sub_i32 s2, s3, s2
	s_ashr_i32 s3, s2, 31
	v_lshl_add_u64 v[0:1], s[2:3], 2, v[0:1]
	v_lshlrev_b32_e32 v66, 2, v68
	v_lshl_add_u64 v[24:25], v[0:1], 0, v[66:67]
	v_add_co_u32_e32 v20, vcc, s38, v24
	s_nop 1
	v_addc_co_u32_e32 v21, vcc, 0, v25, vcc
	v_add_co_u32_e32 v26, vcc, s39, v24
	global_load_dwordx4 v[0:3], v[24:25], off nt
	s_nop 0
	global_load_dwordx4 v[20:23], v[20:21], off nt
	v_addc_co_u32_e32 v27, vcc, 0, v25, vcc
	v_add_co_u32_e32 v28, vcc, s40, v24
	s_nop 1
	v_addc_co_u32_e32 v29, vcc, 0, v25, vcc
	global_load_dwordx4 v[24:27], v[26:27], off nt
	s_nop 0
	global_load_dwordx4 v[28:31], v[28:29], off nt
	s_bitset1_b32 s98, 1
.LBB0_469:
	s_add_i32 s42, s24, s7
	s_cmp_ge_i32 s42, s10
	s_mov_b64 s[2:3], -1
	s_cbranch_scc1 .LBB0_463
	s_waitcnt vmcnt(12)
	s_cmp_eq_u32 s98, 15
	s_cbranch_scc1 .Lcvw_19
	s_waitcnt vmcnt(0)
.Lcvw_19:
	s_bitset0_b32 s98, 2
	s_ashr_i32 s2, s42, 31
	s_lshr_b32 s2, s2, 22
	v_mul_f32_e32 v66, 0x42800000, v32
	v_mul_f32_e32 v77, 0x42800000, v36
	v_mov_b32_e32 v80, v67
	s_add_i32 s3, s42, s2
	v_cvt_pk_fp8_f32 v80, v66, v77
	v_mul_f32_e32 v66, 0x42800000, v33
	v_mul_f32_e32 v77, 0x42800000, v37
	v_mov_b32_e32 v81, v67
	s_ashr_i32 s2, s3, 10
	s_and_b32 s3, s3, 0xfffffc00
	v_cvt_pk_fp8_f32 v81, v66, v77
	s_sub_i32 s3, s42, s3
	s_ashr_i32 s42, s3, 31
	s_lshr_b32 s42, s42, 26
	v_mul_f32_e32 v66, 0x42800000, v41
	v_mul_f32_e32 v77, 0x42800000, v45
	s_add_i32 s3, s3, s42
	v_cvt_pk_fp8_f32 v81, v66, v77 op_sel:[0,0,1]
	v_mul_f32_e32 v66, 0x42800000, v34
	v_mul_f32_e32 v77, 0x42800000, v38
	v_mov_b32_e32 v82, v67
	s_ashr_i32 s44, s3, 6
	s_ashr_i32 s3, s2, 31
	v_cvt_pk_fp8_f32 v82, v66, v77
	v_mul_f32_e32 v66, 0x42800000, v35
	v_mul_f32_e32 v77, 0x42800000, v39
	v_mov_b32_e32 v83, v67
	s_lshl_b64 s[42:43], s[2:3], 23
	v_cvt_pk_fp8_f32 v83, v66, v77
	s_add_u32 s42, s74, s42
	s_addc_u32 s43, s75, s43
	s_lshl_b32 s3, s44, 9
	s_lshl_b32 s2, s2, 13
	v_mul_f32_e32 v78, 0x42800000, v40
	v_mul_f32_e32 v79, 0x42800000, v44
	s_add_i32 s3, s3, s2
	s_add_i32 s2, s25, s19
	v_cvt_pk_fp8_f32 v80, v78, v79 op_sel:[0,0,1]
	v_mul_f32_e32 v78, 0x42800000, v42
	v_mul_f32_e32 v79, 0x42800000, v46
	v_mul_f32_e32 v66, 0x42800000, v43
	v_mul_f32_e32 v77, 0x42800000, v47
	s_sub_i32 s2, s2, s3
	v_cvt_pk_fp8_f32 v82, v78, v79 op_sel:[0,0,1]
	v_cvt_pk_fp8_f32 v83, v66, v77 op_sel:[0,0,1]
	s_and_b32 s2, s2, -16
	s_add_i32 s2, s2, s44
	s_ashr_i32 s3, s2, 31
	s_add_i32 s44, s26, s13
	ds_write2_b32 v72, v80, v81 offset1:33
	ds_write2_b32 v72, v82, v83 offset0:66 offset1:99
	s_waitcnt lgkmcnt(0)
	s_barrier
	ds_read2_b32 v[78:79], v73 offset1:1
	ds_read2_b32 v[80:81], v73 offset0:2 offset1:3
	s_and_b32 s44, s44, 64
	s_lshl_b64 s[2:3], s[2:3], 14
	s_add_u32 s2, s42, s2
	v_add_lshl_u32 v66, s44, v71, 7
	s_addc_u32 s3, s43, s3
	v_lshl_add_u64 v[82:83], s[2:3], 0, v[66:67]
	s_add_i32 s2, s27, s7
	v_lshl_add_u64 v[82:83], v[82:83], 0, v[64:65]
	s_cmp_ge_i32 s2, s10
	s_waitcnt lgkmcnt(0)
	global_store_dwordx4 v[82:83], v[78:81], off nt
	s_cbranch_scc1 .LBB0_472
	s_ashr_i32 s3, s2, 31
	s_lshr_b32 s3, s3, 22
	s_add_i32 s3, s2, s3
	s_ashr_i32 s42, s3, 10
	s_and_b32 s3, s3, 0xfffffc00
	s_sub_i32 s2, s2, s3
	s_ashr_i32 s3, s2, 31
	s_lshr_b32 s3, s3, 26
	s_add_i32 s2, s2, s3
	s_ashr_i32 s44, s2, 6
	s_ashr_i32 s43, s42, 31
	s_lshl_b64 s[2:3], s[42:43], 25
	v_lshl_add_u32 v32, s44, 7, v69
	s_add_u32 s2, s80, s2
	v_ashrrev_i32_e32 v33, 31, v32
	s_addc_u32 s3, s81, s3
	v_lshlrev_b64 v[32:33], 14, v[32:33]
	v_lshl_add_u64 v[32:33], s[2:3], 0, v[32:33]
	s_lshl_b32 s2, s44, 12
	s_lshl_b32 s3, s42, 16
	s_add_i32 s2, s2, s3
	s_add_i32 s3, s28, s13
	s_sub_i32 s2, s3, s2
	s_ashr_i32 s3, s2, 31
	v_lshl_add_u64 v[32:33], s[2:3], 2, v[32:33]
	v_lshlrev_b32_e32 v66, 2, v68
	v_lshl_add_u64 v[40:41], v[32:33], 0, v[66:67]
	v_add_co_u32_e32 v36, vcc, 0x4000, v40
	s_nop 1
	v_addc_co_u32_e32 v37, vcc, 0, v41, vcc
	v_add_co_u32_e32 v42, vcc, 0x8000, v40
	global_load_dwordx4 v[32:35], v[40:41], off nt
	s_nop 0
	global_load_dwordx4 v[36:39], v[36:37], off nt
	v_addc_co_u32_e32 v43, vcc, 0, v41, vcc
	v_add_co_u32_e32 v44, vcc, 0xc000, v40
	s_nop 1
	v_addc_co_u32_e32 v45, vcc, 0, v41, vcc
	global_load_dwordx4 v[40:43], v[42:43], off nt
	s_nop 0
	global_load_dwordx4 v[44:47], v[44:45], off nt
	s_bitset1_b32 s98, 2
.LBB0_472:
	s_add_i32 s42, s29, s7
	s_cmp_ge_i32 s42, s10
	s_mov_b64 s[2:3], -1
	s_cbranch_scc1 .LBB0_463
	s_waitcnt vmcnt(12)
	s_cmp_eq_u32 s98, 15
	s_cbranch_scc1 .Lcvw_20
	s_waitcnt vmcnt(0)
.Lcvw_20:
	s_bitset0_b32 s98, 3
	s_ashr_i32 s2, s42, 31
	s_lshr_b32 s2, s2, 22
	v_mul_f32_e32 v66, 0x42800000, v48
	v_mul_f32_e32 v77, 0x42800000, v52
	v_mov_b32_e32 v80, v67
	s_add_i32 s3, s42, s2
	v_cvt_pk_fp8_f32 v80, v66, v77
	v_mul_f32_e32 v66, 0x42800000, v49
	v_mul_f32_e32 v77, 0x42800000, v53
	v_mov_b32_e32 v81, v67
	s_ashr_i32 s2, s3, 10
	s_and_b32 s3, s3, 0xfffffc00
	v_cvt_pk_fp8_f32 v81, v66, v77
	s_sub_i32 s3, s42, s3
	s_ashr_i32 s42, s3, 31
	s_lshr_b32 s42, s42, 26
	v_mul_f32_e32 v66, 0x42800000, v57
	v_mul_f32_e32 v77, 0x42800000, v61
	s_add_i32 s3, s3, s42
	v_cvt_pk_fp8_f32 v81, v66, v77 op_sel:[0,0,1]
	v_mul_f32_e32 v66, 0x42800000, v50
	v_mul_f32_e32 v77, 0x42800000, v54
	v_mov_b32_e32 v82, v67
	s_ashr_i32 s44, s3, 6
	s_ashr_i32 s3, s2, 31
	v_cvt_pk_fp8_f32 v82, v66, v77
	v_mul_f32_e32 v66, 0x42800000, v51
	v_mul_f32_e32 v77, 0x42800000, v55
	v_mov_b32_e32 v83, v67
	s_lshl_b64 s[42:43], s[2:3], 23
	v_cvt_pk_fp8_f32 v83, v66, v77
	s_add_u32 s42, s74, s42
	s_addc_u32 s43, s75, s43
	s_lshl_b32 s3, s44, 9
	s_lshl_b32 s2, s2, 13
	v_mul_f32_e32 v78, 0x42800000, v56
	v_mul_f32_e32 v79, 0x42800000, v60
	s_add_i32 s3, s3, s2
	s_add_i32 s2, s30, s19
	v_cvt_pk_fp8_f32 v80, v78, v79 op_sel:[0,0,1]
	v_mul_f32_e32 v78, 0x42800000, v58
	v_mul_f32_e32 v79, 0x42800000, v62
	v_mul_f32_e32 v66, 0x42800000, v59
	v_mul_f32_e32 v77, 0x42800000, v63
	s_sub_i32 s2, s2, s3
	v_cvt_pk_fp8_f32 v82, v78, v79 op_sel:[0,0,1]
	v_cvt_pk_fp8_f32 v83, v66, v77 op_sel:[0,0,1]
	s_and_b32 s2, s2, -16
	s_add_i32 s2, s2, s44
	s_ashr_i32 s3, s2, 31
	s_add_i32 s44, s31, s13
	ds_write2_b32 v74, v80, v81 offset0:128 offset1:161
	ds_write2_b32 v74, v82, v83 offset0:194 offset1:227
	s_waitcnt lgkmcnt(0)
	s_barrier
	ds_read2_b32 v[74:75], v75 offset1:1
	ds_read2_b32 v[76:77], v76 offset1:1
	s_and_b32 s44, s44, 64
	s_lshl_b64 s[2:3], s[2:3], 14
	s_add_u32 s2, s42, s2
	v_add_lshl_u32 v66, s44, v71, 7
	s_addc_u32 s3, s43, s3
	v_lshl_add_u64 v[78:79], s[2:3], 0, v[66:67]
	s_add_i32 s2, s34, s7
	v_lshl_add_u64 v[78:79], v[78:79], 0, v[64:65]
	s_cmp_ge_i32 s2, s10
	s_waitcnt lgkmcnt(0)
	global_store_dwordx4 v[78:79], v[74:77], off nt
	s_cbranch_scc1 .LBB0_462
	s_ashr_i32 s3, s2, 31
	s_lshr_b32 s3, s3, 22
	s_add_i32 s3, s2, s3
	s_ashr_i32 s42, s3, 10
	s_and_b32 s3, s3, 0xfffffc00
	s_sub_i32 s2, s2, s3
	s_ashr_i32 s3, s2, 31
	s_lshr_b32 s3, s3, 26
	s_add_i32 s2, s2, s3
	s_ashr_i32 s7, s2, 6
	s_ashr_i32 s43, s42, 31
	s_lshl_b64 s[2:3], s[42:43], 25
	v_lshl_add_u32 v48, s7, 7, v69
	s_add_u32 s2, s80, s2
	v_ashrrev_i32_e32 v49, 31, v48
	s_addc_u32 s3, s81, s3
	v_lshlrev_b64 v[48:49], 14, v[48:49]
	v_lshl_add_u64 v[48:49], s[2:3], 0, v[48:49]
	s_lshl_b32 s2, s7, 12
	s_lshl_b32 s3, s42, 16
	s_add_i32 s2, s2, s3
	s_add_i32 s3, s35, s13
	s_sub_i32 s2, s3, s2
	s_ashr_i32 s3, s2, 31
	v_lshl_add_u64 v[48:49], s[2:3], 2, v[48:49]
	v_lshlrev_b32_e32 v66, 2, v68
	v_lshl_add_u64 v[56:57], v[48:49], 0, v[66:67]
	v_add_co_u32_e32 v52, vcc, 0x4000, v56
	s_nop 1
	v_addc_co_u32_e32 v53, vcc, 0, v57, vcc
	v_add_co_u32_e32 v58, vcc, 0x8000, v56
	global_load_dwordx4 v[48:51], v[56:57], off nt
	s_nop 0
	global_load_dwordx4 v[52:55], v[52:53], off nt
	v_addc_co_u32_e32 v59, vcc, 0, v57, vcc
	v_add_co_u32_e32 v60, vcc, 0xc000, v56
	s_nop 1
	v_addc_co_u32_e32 v61, vcc, 0, v57, vcc
	global_load_dwordx4 v[56:59], v[58:59], off nt
	s_nop 0
	global_load_dwordx4 v[60:63], v[60:61], off nt
	s_bitset1_b32 s98, 3
	s_branch .LBB0_462

.LBB0_549:
	s_cmp_lt_i32 s26, s17
	s_cselect_b32 s8, 4, 2
	s_and_b64 s[4:5], s[4:5], exec
	s_cselect_b32 s4, 8, s8
	s_ashr_i32 s5, s10, 31
	s_lshr_b32 s5, s5, 22
	s_add_i32 s5, s10, s5
	s_ashr_i32 s8, s5, 10
	s_and_b32 s5, s5, 0xfffffc00
	s_sub_i32 s5, s10, s5
	s_ashr_i32 s9, s5, 31
	s_lshr_b32 s9, s9, 26
	s_add_i32 s9, s5, s9
	s_ashr_i32 s26, s9, 6
	s_ashr_i32 s9, s8, 31
	s_lshl_b64 s[8:9], s[8:9], 25
	v_lshl_add_u32 v0, s26, 7, v72
	s_add_u32 s8, s80, s8
	v_ashrrev_i32_e32 v1, 31, v0
	s_addc_u32 s9, s81, s9
	v_lshlrev_b64 v[0:1], 14, v[0:1]
	v_lshl_add_u64 v[0:1], s[8:9], 0, v[0:1]
	s_lshl_b32 s8, s26, 12
	s_lshl_b32 s5, s5, 6
	s_sub_i32 s8, s5, s8
	s_ashr_i32 s9, s8, 31
	v_lshl_add_u64 v[0:1], s[8:9], 2, v[0:1]
	v_mov_b32_e32 v69, v65
	s_waitcnt vmcnt(1)
	v_lshl_add_u64 v[8:9], v[0:1], 0, v[68:69]
	v_add_co_u32_e32 v4, vcc, s23, v8
	s_nop 1
	v_addc_co_u32_e32 v5, vcc, 0, v9, vcc
	v_add_co_u32_e32 v10, vcc, 0x8000, v8
	s_mov_b32 s98, 0
	s_barrier
	s_nop 0
	v_addc_co_u32_e32 v11, vcc, 0, v9, vcc
	s_waitcnt vmcnt(0)
	v_add_co_u32_e32 v12, vcc, 0xc000, v8
	s_nop 1
	v_addc_co_u32_e32 v13, vcc, 0, v9, vcc
	global_load_dwordx4 v[0:3], v[8:9], off nt
	s_nop 0
	global_load_dwordx4 v[4:7], v[4:5], off nt
	s_nop 0
	global_load_dwordx4 v[8:11], v[10:11], off nt
	s_nop 0
	global_load_dwordx4 v[12:15], v[12:13], off nt
	s_bitset1_b32 s98, 0
	s_add_i32 s5, s10, 1
	v_mov_b32_e32 v16, 0
	s_cmp_le_i32 s77, s5
	v_mov_b32_e32 v17, v16
	v_mov_b32_e32 v18, v16
	v_mov_b32_e32 v19, v16
	v_mov_b32_e32 v20, v16
	v_mov_b32_e32 v21, v16
	v_mov_b32_e32 v22, v16
	v_mov_b32_e32 v23, v16
	v_mov_b32_e32 v24, v16
	v_mov_b32_e32 v25, v16
	v_mov_b32_e32 v26, v16
	v_mov_b32_e32 v27, v16
	v_mov_b32_e32 v28, v16
	v_mov_b32_e32 v29, v16
	v_mov_b32_e32 v30, v16
	v_mov_b32_e32 v31, v16
	s_cbranch_scc1 .LBB0_551
	s_ashr_i32 s8, s5, 31
	s_lshr_b32 s8, s8, 22
	s_add_i32 s9, s5, s8
	s_ashr_i32 s8, s9, 10
	s_and_b32 s9, s9, 0xfffffc00
	s_sub_i32 s5, s5, s9
	s_ashr_i32 s9, s5, 31
	s_lshr_b32 s9, s9, 26
	s_add_i32 s9, s5, s9
	s_ashr_i32 s26, s9, 6
	s_ashr_i32 s9, s8, 31
	s_lshl_b64 s[8:9], s[8:9], 25
	v_lshl_add_u32 v16, s26, 7, v72
	s_add_u32 s8, s80, s8
	v_ashrrev_i32_e32 v17, 31, v16
	s_addc_u32 s9, s81, s9
	v_lshlrev_b64 v[16:17], 14, v[16:17]
	v_lshl_add_u64 v[16:17], s[8:9], 0, v[16:17]
	s_lshl_b32 s8, s26, 12
	s_lshl_b32 s5, s5, 6
	s_sub_i32 s8, s5, s8
	s_ashr_i32 s9, s8, 31
	v_lshl_add_u64 v[16:17], s[8:9], 2, v[16:17]
	v_lshl_add_u64 v[24:25], v[16:17], 0, v[68:69]
	v_add_co_u32_e32 v20, vcc, s23, v24
	s_nop 1
	v_addc_co_u32_e32 v21, vcc, 0, v25, vcc
	v_add_co_u32_e32 v26, vcc, s24, v24
	global_load_dwordx4 v[16:19], v[24:25], off nt
	s_nop 0
	global_load_dwordx4 v[20:23], v[20:21], off nt
	v_addc_co_u32_e32 v27, vcc, 0, v25, vcc
	v_add_co_u32_e32 v28, vcc, s25, v24
	s_nop 1
	v_addc_co_u32_e32 v29, vcc, 0, v25, vcc
	global_load_dwordx4 v[24:27], v[26:27], off nt
	s_nop 0
	global_load_dwordx4 v[28:31], v[28:29], off nt
	s_bitset1_b32 s98, 1
.LBB0_551:
	s_add_i32 s4, s10, s4
	s_min_i32 s8, s4, s77
	s_add_i32 s4, s10, 2
	s_cmp_ge_i32 s4, s8
	s_cbranch_scc1 .LBB0_553
	s_ashr_i32 s5, s4, 31
	s_lshr_b32 s5, s5, 22
	s_add_i32 s5, s4, s5
	s_ashr_i32 s26, s5, 10
	s_and_b32 s5, s5, 0xfffffc00
	s_sub_i32 s9, s4, s5
	s_ashr_i32 s4, s9, 31
	s_lshr_b32 s4, s4, 26
	s_add_i32 s4, s9, s4
	s_ashr_i32 s28, s4, 6
	s_ashr_i32 s27, s26, 31
	s_lshl_b64 s[4:5], s[26:27], 25
	v_lshl_add_u32 v32, s28, 7, v72
	s_add_u32 s4, s80, s4
	v_ashrrev_i32_e32 v33, 31, v32
	s_addc_u32 s5, s81, s5
	v_lshlrev_b64 v[32:33], 14, v[32:33]
	v_lshl_add_u64 v[32:33], s[4:5], 0, v[32:33]
	s_lshl_b32 s4, s28, 12
	s_lshl_b32 s5, s9, 6
	s_sub_i32 s4, s5, s4
	s_ashr_i32 s5, s4, 31
	v_lshl_add_u64 v[32:33], s[4:5], 2, v[32:33]
	v_mov_b32_e32 v69, v65
	v_lshl_add_u64 v[40:41], v[32:33], 0, v[68:69]
	v_add_co_u32_e32 v36, vcc, 0x4000, v40
	s_nop 1
	v_addc_co_u32_e32 v37, vcc, 0, v41, vcc
	v_add_co_u32_e32 v42, vcc, 0x8000, v40
	global_load_dwordx4 v[32:35], v[40:41], off nt
	s_nop 0
	global_load_dwordx4 v[36:39], v[36:37], off nt
	v_addc_co_u32_e32 v43, vcc, 0, v41, vcc
	v_add_co_u32_e32 v44, vcc, 0xc000, v40
	s_nop 1
	v_addc_co_u32_e32 v45, vcc, 0, v41, vcc
	global_load_dwordx4 v[40:43], v[42:43], off nt
	s_nop 0
	global_load_dwordx4 v[44:47], v[44:45], off nt
	s_bitset1_b32 s98, 2
.LBB0_553:
	s_add_i32 s4, s10, 3
	s_cmp_ge_i32 s4, s8
	s_cbranch_scc1 .LBB0_555
	s_ashr_i32 s5, s4, 31
	s_lshr_b32 s5, s5, 22
	s_add_i32 s5, s4, s5
	s_ashr_i32 s26, s5, 10
	s_and_b32 s5, s5, 0xfffffc00
	s_sub_i32 s9, s4, s5
	s_ashr_i32 s4, s9, 31
	s_lshr_b32 s4, s4, 26
	s_add_i32 s4, s9, s4
	s_ashr_i32 s10, s4, 6
	s_ashr_i32 s27, s26, 31
	s_lshl_b64 s[4:5], s[26:27], 25
	v_lshl_add_u32 v48, s10, 7, v72
	s_add_u32 s4, s80, s4
	v_ashrrev_i32_e32 v49, 31, v48
	s_addc_u32 s5, s81, s5
	v_lshlrev_b64 v[48:49], 14, v[48:49]
	v_lshl_add_u64 v[48:49], s[4:5], 0, v[48:49]
	s_lshl_b32 s4, s10, 12
	s_lshl_b32 s5, s9, 6
	s_sub_i32 s4, s5, s4
	s_ashr_i32 s5, s4, 31
	v_lshl_add_u64 v[48:49], s[4:5], 2, v[48:49]
	v_mov_b32_e32 v69, v65
	v_lshl_add_u64 v[56:57], v[48:49], 0, v[68:69]
	v_add_co_u32_e32 v52, vcc, 0x4000, v56
	s_nop 1
	v_addc_co_u32_e32 v53, vcc, 0, v57, vcc
	v_add_co_u32_e32 v58, vcc, 0x8000, v56
	global_load_dwordx4 v[48:51], v[56:57], off nt
	s_nop 0
	global_load_dwordx4 v[52:55], v[52:53], off nt
	v_addc_co_u32_e32 v59, vcc, 0, v57, vcc
	v_add_co_u32_e32 v60, vcc, 0xc000, v56
	s_nop 1
	v_addc_co_u32_e32 v61, vcc, 0, v57, vcc
	global_load_dwordx4 v[56:59], v[58:59], off nt
	s_nop 0
	global_load_dwordx4 v[60:63], v[60:61], off nt
	s_bitset1_b32 s98, 3

.Lcvw_21:
	s_bitset0_b32 s98, 0
	s_add_i32 s4, s10, -7
	s_ashr_i32 s5, s4, 31
	s_lshr_b32 s5, s5, 22
	s_add_i32 s5, s4, s5
	v_mul_f32_e32 v64, 0x42800000, v0
	v_mul_f32_e32 v69, 0x42800000, v4
	v_mov_b32_e32 v78, v65
	s_ashr_i32 s4, s5, 10
	s_and_b32 s5, s5, 0xfffffc00
	v_cvt_pk_fp8_f32 v78, v64, v69
	v_mul_f32_e32 v64, 0x42800000, v1
	v_mul_f32_e32 v69, 0x42800000, v5
	v_mov_b32_e32 v79, v65
	s_sub_i32 s5, s10, s5
	v_cvt_pk_fp8_f32 v79, v64, v69
	s_add_i32 s5, s5, -7
	s_ashr_i32 s27, s5, 31
	s_lshr_b32 s27, s27, 26
	v_mul_f32_e32 v64, 0x42800000, v9
	v_mul_f32_e32 v69, 0x42800000, v13
	s_add_i32 s5, s5, s27
	v_cvt_pk_fp8_f32 v79, v64, v69 op_sel:[0,0,1]
	v_mul_f32_e32 v64, 0x42800000, v2
	v_mul_f32_e32 v69, 0x42800000, v6
	v_mov_b32_e32 v80, v65
	s_ashr_i32 s27, s5, 6
	s_ashr_i32 s5, s4, 31
	v_cvt_pk_fp8_f32 v80, v64, v69
	v_mul_f32_e32 v64, 0x42800000, v3
	v_mul_f32_e32 v69, 0x42800000, v7
	v_mov_b32_e32 v81, v65
	s_lshl_b64 s[28:29], s[4:5], 23
	v_cvt_pk_fp8_f32 v81, v64, v69
	s_add_u32 s30, s74, s28
	s_addc_u32 s31, s75, s29
	s_lshl_b32 s5, s27, 9
	s_lshl_b32 s4, s4, 13
	v_mul_f32_e32 v76, 0x42800000, v8
	v_mul_f32_e32 v77, 0x42800000, v12
	s_add_i32 s5, s5, s4
	s_add_i32 s29, s11, s26
	v_cvt_pk_fp8_f32 v78, v76, v77 op_sel:[0,0,1]
	v_mul_f32_e32 v76, 0x42800000, v10
	v_mul_f32_e32 v77, 0x42800000, v14
	v_mul_f32_e32 v64, 0x42800000, v11
	v_mul_f32_e32 v69, 0x42800000, v15
	s_sub_i32 s4, s29, s5
	v_cvt_pk_fp8_f32 v80, v76, v77 op_sel:[0,0,1]
	v_cvt_pk_fp8_f32 v81, v64, v69 op_sel:[0,0,1]
	s_and_b32 s4, s4, -16
	s_add_i32 s4, s4, s27
	v_add_u32_e32 v76, v74, v66
	s_ashr_i32 s5, s4, 31
	s_add_i32 s28, s19, s9
	ds_write2_b32 v75, v78, v79 offset1:33
	ds_write2_b32 v75, v80, v81 offset0:66 offset1:99
	s_waitcnt lgkmcnt(0)
	s_barrier
	ds_read2_b32 v[78:79], v76 offset1:1
	ds_read2_b32 v[80:81], v76 offset0:2 offset1:3
	s_and_b32 s27, s28, 64
	s_lshl_b64 s[4:5], s[4:5], 14
	s_add_u32 s4, s30, s4
	v_add_lshl_u32 v64, s27, v71, 7
	s_addc_u32 s5, s31, s5
	v_lshl_add_u64 v[82:83], s[4:5], 0, v[64:65]
	s_add_i32 s27, s10, -3
	v_lshl_add_u64 v[82:83], v[82:83], 0, v[66:67]
	s_cmp_ge_i32 s27, s8
	s_waitcnt lgkmcnt(0)
	global_store_dwordx4 v[82:83], v[78:81], off nt
	s_cbranch_scc1 .LBB0_560
	s_ashr_i32 s4, s27, 31
	s_lshr_b32 s4, s4, 22
	s_add_i32 s5, s27, s4
	s_ashr_i32 s4, s5, 10
	s_and_b32 s5, s5, 0xfffffc00
	s_sub_i32 s5, s10, s5
	s_add_i32 s5, s5, -3
	s_ashr_i32 s30, s5, 31
	s_lshr_b32 s30, s30, 26
	s_add_i32 s5, s5, s30
	s_ashr_i32 s34, s5, 6
	s_ashr_i32 s5, s4, 31
	s_lshl_b64 s[30:31], s[4:5], 25
	s_add_u32 s30, s80, s30
	s_addc_u32 s31, s81, s31
	s_lshl_b32 s5, s34, 12
	s_lshl_b32 s4, s4, 16
	v_lshl_add_u32 v0, s34, 7, v72
	s_add_i32 s5, s5, s4
	v_ashrrev_i32_e32 v1, 31, v0
	s_sub_i32 s4, s28, s5
	v_lshlrev_b64 v[0:1], 14, v[0:1]
	s_addk_i32 s4, 0x100
	v_lshl_add_u64 v[0:1], s[30:31], 0, v[0:1]
	s_ashr_i32 s5, s4, 31
	v_lshl_add_u64 v[0:1], s[4:5], 2, v[0:1]
	v_mov_b32_e32 v69, v65
	v_lshl_add_u64 v[8:9], v[0:1], 0, v[68:69]
	v_add_co_u32_e32 v4, vcc, s23, v8
	s_nop 1
	v_addc_co_u32_e32 v5, vcc, 0, v9, vcc
	v_add_co_u32_e32 v10, vcc, s24, v8
	global_load_dwordx4 v[0:3], v[8:9], off nt
	s_nop 0
	global_load_dwordx4 v[4:7], v[4:5], off nt
	v_addc_co_u32_e32 v11, vcc, 0, v9, vcc
	v_add_co_u32_e32 v12, vcc, s25, v8
	s_nop 1
	v_addc_co_u32_e32 v13, vcc, 0, v9, vcc
	global_load_dwordx4 v[8:11], v[10:11], off nt
	s_nop 0
	global_load_dwordx4 v[12:15], v[12:13], off nt
	s_bitset1_b32 s98, 0
.LBB0_560:
	s_add_i32 s30, s10, -6
	s_cmp_ge_i32 s30, s8
	s_mov_b64 s[4:5], -1
	s_cbranch_scc1 .LBB0_557
	s_waitcnt vmcnt(12)
	s_cmp_eq_u32 s98, 15
	s_cbranch_scc1 .Lcvw_22
	s_waitcnt vmcnt(0)
.Lcvw_22:
	s_bitset0_b32 s98, 1
	s_ashr_i32 s4, s30, 31
	s_lshr_b32 s4, s4, 22
	s_add_i32 s30, s30, s4
	s_and_b32 s5, s30, 0xfffffc00
	v_mul_f32_e32 v69, 0x42800000, v16
	v_mul_f32_e32 v77, 0x42800000, v20
	v_mov_b32_e32 v80, v65
	s_sub_i32 s5, s10, s5
	v_cvt_pk_fp8_f32 v80, v69, v77
	v_mul_f32_e32 v69, 0x42800000, v17
	v_mul_f32_e32 v77, 0x42800000, v21
	v_mov_b32_e32 v81, v65
	s_add_i32 s5, s5, -6
	v_cvt_pk_fp8_f32 v81, v69, v77
	s_ashr_i32 s4, s30, 10
	s_ashr_i32 s30, s5, 31
	s_lshr_b32 s30, s30, 26
	s_add_i32 s5, s5, s30
	v_mul_f32_e32 v69, 0x42800000, v25
	v_mul_f32_e32 v77, 0x42800000, v29
	s_ashr_i32 s34, s5, 6
	s_ashr_i32 s5, s4, 31
	v_cvt_pk_fp8_f32 v81, v69, v77 op_sel:[0,0,1]
	v_mul_f32_e32 v69, 0x42800000, v18
	v_mul_f32_e32 v77, 0x42800000, v22
	v_mov_b32_e32 v82, v65
	s_lshl_b64 s[30:31], s[4:5], 23
	v_cvt_pk_fp8_f32 v82, v69, v77
	v_mul_f32_e32 v69, 0x42800000, v19
	v_mul_f32_e32 v77, 0x42800000, v23
	v_mov_b32_e32 v83, v65
	s_add_u32 s30, s74, s30
	v_cvt_pk_fp8_f32 v83, v69, v77
	s_addc_u32 s31, s75, s31
	s_lshl_b32 s5, s34, 9
	s_lshl_b32 s4, s4, 13
	s_add_i32 s5, s5, s4
	v_mul_f32_e32 v78, 0x42800000, v24
	v_mul_f32_e32 v79, 0x42800000, v28
	s_sub_i32 s4, s29, s5
	v_cvt_pk_fp8_f32 v80, v78, v79 op_sel:[0,0,1]
	v_mul_f32_e32 v78, 0x42800000, v26
	v_mul_f32_e32 v79, 0x42800000, v30
	v_mul_f32_e32 v69, 0x42800000, v27
	v_mul_f32_e32 v77, 0x42800000, v31
	s_add_i32 s4, s4, 8
	v_cvt_pk_fp8_f32 v82, v78, v79 op_sel:[0,0,1]
	v_cvt_pk_fp8_f32 v83, v69, v77 op_sel:[0,0,1]
	s_and_b32 s4, s4, -16
	s_add_i32 s4, s4, s34
	v_add_u32_e32 v77, 0x2000, v75
	v_add_u32_e32 v78, 0x2200, v76
	s_ashr_i32 s5, s4, 31
	s_add_i32 s34, s28, 64
	ds_write2_b32 v77, v80, v81 offset0:128 offset1:161
	ds_write2_b32 v77, v82, v83 offset0:194 offset1:227
	s_waitcnt lgkmcnt(0)
	s_barrier
	v_add_u32_e32 v79, 0x2208, v76
	ds_read2_b32 v[80:81], v78 offset1:1
	ds_read2_b32 v[82:83], v79 offset1:1
	s_and_b32 s34, s34, 64
	s_lshl_b64 s[4:5], s[4:5], 14
	s_add_u32 s4, s30, s4
	v_add_lshl_u32 v84, s34, v71, 7
	v_mov_b32_e32 v85, v65
	s_addc_u32 s5, s31, s5
	v_lshl_add_u64 v[84:85], s[4:5], 0, v[84:85]
	s_add_i32 s4, s10, -2
	v_lshl_add_u64 v[84:85], v[84:85], 0, v[66:67]
	s_cmp_ge_i32 s4, s8
	s_waitcnt lgkmcnt(0)
	global_store_dwordx4 v[84:85], v[80:83], off nt
	s_cbranch_scc1 .LBB0_563
	s_ashr_i32 s5, s4, 31
	s_lshr_b32 s5, s5, 22
	s_add_i32 s5, s4, s5
	s_ashr_i32 s4, s5, 10
	s_and_b32 s5, s5, 0xfffffc00
	s_sub_i32 s5, s10, s5
	s_add_i32 s5, s5, -2
	s_ashr_i32 s30, s5, 31
	s_lshr_b32 s30, s30, 26
	s_add_i32 s5, s5, s30
	s_ashr_i32 s34, s5, 6
	s_ashr_i32 s5, s4, 31
	s_lshl_b64 s[30:31], s[4:5], 25
	s_add_u32 s30, s80, s30
	s_addc_u32 s31, s81, s31
	s_lshl_b32 s5, s34, 12
	s_lshl_b32 s4, s4, 16
	v_lshl_add_u32 v16, s34, 7, v72
	s_add_i32 s5, s5, s4
	v_ashrrev_i32_e32 v17, 31, v16
	s_sub_i32 s4, s28, s5
	v_lshlrev_b64 v[16:17], 14, v[16:17]
	s_addk_i32 s4, 0x140
	v_lshl_add_u64 v[16:17], s[30:31], 0, v[16:17]
	s_ashr_i32 s5, s4, 31
	v_lshl_add_u64 v[16:17], s[4:5], 2, v[16:17]
	v_mov_b32_e32 v69, v65
	v_lshl_add_u64 v[24:25], v[16:17], 0, v[68:69]
	v_add_co_u32_e32 v20, vcc, s23, v24
	s_nop 1
	v_addc_co_u32_e32 v21, vcc, 0, v25, vcc
	v_add_co_u32_e32 v26, vcc, s24, v24
	global_load_dwordx4 v[16:19], v[24:25], off nt
	s_nop 0
	global_load_dwordx4 v[20:23], v[20:21], off nt
	v_addc_co_u32_e32 v27, vcc, 0, v25, vcc
	v_add_co_u32_e32 v28, vcc, s25, v24
	s_nop 1
	v_addc_co_u32_e32 v29, vcc, 0, v25, vcc
	global_load_dwordx4 v[24:27], v[26:27], off nt
	s_nop 0
	global_load_dwordx4 v[28:31], v[28:29], off nt
	s_bitset1_b32 s98, 1
.LBB0_563:
	s_add_i32 s30, s10, -5
	s_cmp_ge_i32 s30, s8
	s_mov_b64 s[4:5], -1
	s_cbranch_scc1 .LBB0_557
	s_waitcnt vmcnt(12)
	s_cmp_eq_u32 s98, 15
	s_cbranch_scc1 .Lcvw_23
	s_waitcnt vmcnt(0)
.Lcvw_23:
	s_bitset0_b32 s98, 2
	s_ashr_i32 s4, s30, 31
	s_lshr_b32 s4, s4, 22
	s_add_i32 s30, s30, s4
	s_and_b32 s5, s30, 0xfffffc00
	v_mul_f32_e32 v69, 0x42800000, v32
	v_mul_f32_e32 v80, 0x42800000, v36
	v_mov_b32_e32 v83, v65
	s_sub_i32 s5, s10, s5
	v_cvt_pk_fp8_f32 v83, v69, v80
	v_mul_f32_e32 v69, 0x42800000, v33
	v_mul_f32_e32 v80, 0x42800000, v37
	v_mov_b32_e32 v84, v65
	s_add_i32 s5, s5, -5
	v_cvt_pk_fp8_f32 v84, v69, v80
	s_ashr_i32 s4, s30, 10
	s_ashr_i32 s30, s5, 31
	s_lshr_b32 s30, s30, 26
	s_add_i32 s5, s5, s30
	v_mul_f32_e32 v69, 0x42800000, v41
	v_mul_f32_e32 v80, 0x42800000, v45
	s_ashr_i32 s34, s5, 6
	s_ashr_i32 s5, s4, 31
	v_cvt_pk_fp8_f32 v84, v69, v80 op_sel:[0,0,1]
	v_mul_f32_e32 v69, 0x42800000, v34
	v_mul_f32_e32 v80, 0x42800000, v38
	v_mov_b32_e32 v85, v65
	s_lshl_b64 s[30:31], s[4:5], 23
	v_cvt_pk_fp8_f32 v85, v69, v80
	v_mul_f32_e32 v69, 0x42800000, v35
	v_mul_f32_e32 v80, 0x42800000, v39
	v_mov_b32_e32 v86, v65
	s_add_u32 s30, s74, s30
	v_cvt_pk_fp8_f32 v86, v69, v80
	s_addc_u32 s31, s75, s31
	s_lshl_b32 s5, s34, 9
	s_lshl_b32 s4, s4, 13
	s_add_i32 s5, s5, s4
	v_mul_f32_e32 v81, 0x42800000, v40
	v_mul_f32_e32 v82, 0x42800000, v44
	s_sub_i32 s4, s29, s5
	v_cvt_pk_fp8_f32 v83, v81, v82 op_sel:[0,0,1]
	v_mul_f32_e32 v81, 0x42800000, v42
	v_mul_f32_e32 v82, 0x42800000, v46
	v_mul_f32_e32 v69, 0x42800000, v43
	v_mul_f32_e32 v80, 0x42800000, v47
	s_add_i32 s4, s4, 16
	v_cvt_pk_fp8_f32 v85, v81, v82 op_sel:[0,0,1]
	v_cvt_pk_fp8_f32 v86, v69, v80 op_sel:[0,0,1]
	s_and_b32 s4, s4, -16
	s_add_i32 s4, s4, s34
	s_ashr_i32 s5, s4, 31
	ds_write2_b32 v75, v83, v84 offset1:33
	ds_write2_b32 v75, v85, v86 offset0:66 offset1:99
	s_waitcnt lgkmcnt(0)
	s_barrier
	ds_read2_b32 v[80:81], v76 offset1:1
	ds_read2_b32 v[82:83], v76 offset0:2 offset1:3
	s_lshl_b64 s[4:5], s[4:5], 14
	s_add_u32 s4, s30, s4
	s_addc_u32 s5, s31, s5
	v_lshl_add_u64 v[84:85], s[4:5], 0, v[64:65]
	s_add_i32 s4, s10, -1
	v_lshl_add_u64 v[84:85], v[84:85], 0, v[66:67]
	s_cmp_ge_i32 s4, s8
	s_waitcnt lgkmcnt(0)
	global_store_dwordx4 v[84:85], v[80:83], off nt
	s_cbranch_scc1 .LBB0_566
	s_ashr_i32 s5, s4, 31
	s_lshr_b32 s5, s5, 22
	s_add_i32 s5, s4, s5
	s_ashr_i32 s4, s5, 10
	s_orn2_b32 s5, 0x3ff, s5
	s_add_i32 s5, s5, s10
	s_ashr_i32 s30, s5, 31
	s_lshr_b32 s30, s30, 26
	s_add_i32 s5, s5, s30
	s_ashr_i32 s34, s5, 6
	s_ashr_i32 s5, s4, 31
	s_lshl_b64 s[30:31], s[4:5], 25
	s_add_u32 s30, s80, s30
	s_addc_u32 s31, s81, s31
	s_lshl_b32 s5, s34, 12
	s_lshl_b32 s4, s4, 16
	v_lshl_add_u32 v32, s34, 7, v72
	s_add_i32 s5, s5, s4
	v_ashrrev_i32_e32 v33, 31, v32
	s_sub_i32 s4, s28, s5
	v_lshlrev_b64 v[32:33], 14, v[32:33]
	s_addk_i32 s4, 0x180
	v_lshl_add_u64 v[32:33], s[30:31], 0, v[32:33]
	s_ashr_i32 s5, s4, 31
	v_lshl_add_u64 v[32:33], s[4:5], 2, v[32:33]
	v_mov_b32_e32 v69, v65
	v_lshl_add_u64 v[40:41], v[32:33], 0, v[68:69]
	v_add_co_u32_e32 v36, vcc, 0x4000, v40
	s_nop 1
	v_addc_co_u32_e32 v37, vcc, 0, v41, vcc
	v_add_co_u32_e32 v42, vcc, 0x8000, v40
	global_load_dwordx4 v[32:35], v[40:41], off nt
	s_nop 0
	global_load_dwordx4 v[36:39], v[36:37], off nt
	v_addc_co_u32_e32 v43, vcc, 0, v41, vcc
	v_add_co_u32_e32 v44, vcc, 0xc000, v40
	s_nop 1
	v_addc_co_u32_e32 v45, vcc, 0, v41, vcc
	global_load_dwordx4 v[40:43], v[42:43], off nt
	s_nop 0
	global_load_dwordx4 v[44:47], v[44:45], off nt
	s_bitset1_b32 s98, 2
.LBB0_566:
	s_add_i32 s30, s10, -4
	s_cmp_ge_i32 s30, s8
	s_mov_b64 s[4:5], -1
	s_cbranch_scc1 .LBB0_557
	s_waitcnt vmcnt(12)
	s_cmp_eq_u32 s98, 15
	s_cbranch_scc1 .Lcvw_24
	s_waitcnt vmcnt(0)
.Lcvw_24:
	s_bitset0_b32 s98, 3
	s_ashr_i32 s4, s30, 31
	s_lshr_b32 s4, s4, 22
	s_add_i32 s30, s30, s4
	s_and_b32 s5, s30, 0xfffffc00
	v_mul_f32_e32 v64, 0x42800000, v48
	v_mul_f32_e32 v69, 0x42800000, v52
	v_mov_b32_e32 v81, v65
	s_sub_i32 s5, s10, s5
	v_cvt_pk_fp8_f32 v81, v64, v69
	v_mul_f32_e32 v64, 0x42800000, v49
	v_mul_f32_e32 v69, 0x42800000, v53
	v_mov_b32_e32 v82, v65
	s_add_i32 s5, s5, -4
	v_cvt_pk_fp8_f32 v82, v64, v69
	s_ashr_i32 s4, s30, 10
	s_ashr_i32 s30, s5, 31
	s_lshr_b32 s30, s30, 26
	s_add_i32 s5, s5, s30
	v_mul_f32_e32 v64, 0x42800000, v57
	v_mul_f32_e32 v69, 0x42800000, v61
	s_ashr_i32 s34, s5, 6
	s_ashr_i32 s5, s4, 31
	v_cvt_pk_fp8_f32 v82, v64, v69 op_sel:[0,0,1]
	v_mul_f32_e32 v64, 0x42800000, v50
	v_mul_f32_e32 v69, 0x42800000, v54
	v_mov_b32_e32 v83, v65
	s_lshl_b64 s[30:31], s[4:5], 23
	v_cvt_pk_fp8_f32 v83, v64, v69
	v_mul_f32_e32 v64, 0x42800000, v51
	v_mul_f32_e32 v69, 0x42800000, v55
	v_mov_b32_e32 v84, v65
	s_add_u32 s30, s74, s30
	v_cvt_pk_fp8_f32 v84, v64, v69
	s_addc_u32 s31, s75, s31
	s_lshl_b32 s5, s34, 9
	s_lshl_b32 s4, s4, 13
	s_add_i32 s5, s5, s4
	v_mul_f32_e32 v76, 0x42800000, v56
	v_mul_f32_e32 v80, 0x42800000, v60
	s_sub_i32 s4, s29, s5
	v_cvt_pk_fp8_f32 v81, v76, v80 op_sel:[0,0,1]
	v_mul_f32_e32 v76, 0x42800000, v58
	v_mul_f32_e32 v80, 0x42800000, v62
	v_mul_f32_e32 v64, 0x42800000, v59
	v_mul_f32_e32 v69, 0x42800000, v63
	s_add_i32 s4, s4, 24
	v_cvt_pk_fp8_f32 v83, v76, v80 op_sel:[0,0,1]
	v_cvt_pk_fp8_f32 v84, v64, v69 op_sel:[0,0,1]
	s_and_b32 s4, s4, -16
	s_add_i32 s4, s4, s34
	s_ashr_i32 s5, s4, 31
	s_add_i32 s29, s28, 0xc0
	ds_write2_b32 v77, v81, v82 offset0:128 offset1:161
	ds_write2_b32 v77, v83, v84 offset0:194 offset1:227
	s_waitcnt lgkmcnt(0)
	s_barrier
	ds_read2_b32 v[76:77], v78 offset1:1
	ds_read2_b32 v[78:79], v79 offset1:1
	s_and_b32 s29, s29, 64
	s_lshl_b64 s[4:5], s[4:5], 14
	s_add_u32 s4, s30, s4
	v_add_lshl_u32 v64, s29, v71, 7
	s_addc_u32 s5, s31, s5
	v_lshl_add_u64 v[80:81], s[4:5], 0, v[64:65]
	v_lshl_add_u64 v[80:81], v[80:81], 0, v[66:67]
	s_cmp_ge_i32 s10, s8
	s_waitcnt lgkmcnt(0)
	global_store_dwordx4 v[80:81], v[76:79], off nt
	s_cbranch_scc1 .LBB0_556
	s_ashr_i32 s4, s10, 31
	s_lshr_b32 s4, s4, 22
	s_add_i32 s5, s10, s4
	s_ashr_i32 s4, s5, 10
	s_and_b32 s5, s5, 0xfffffc00
	s_sub_i32 s5, s10, s5
	s_ashr_i32 s29, s5, 31
	s_lshr_b32 s29, s29, 26
	s_add_i32 s5, s5, s29
	s_ashr_i32 s29, s5, 6
	s_ashr_i32 s5, s4, 31
	s_lshl_b64 s[30:31], s[4:5], 25
	s_add_u32 s30, s80, s30
	s_addc_u32 s31, s81, s31
	s_lshl_b32 s5, s29, 12
	s_lshl_b32 s4, s4, 16
	v_lshl_add_u32 v48, s29, 7, v72
	s_add_i32 s5, s5, s4
	v_ashrrev_i32_e32 v49, 31, v48
	s_sub_i32 s4, s28, s5
	v_lshlrev_b64 v[48:49], 14, v[48:49]
	s_addk_i32 s4, 0x1c0
	v_lshl_add_u64 v[48:49], s[30:31], 0, v[48:49]
	s_ashr_i32 s5, s4, 31
	v_lshl_add_u64 v[48:49], s[4:5], 2, v[48:49]
	v_mov_b32_e32 v69, v65
	v_lshl_add_u64 v[56:57], v[48:49], 0, v[68:69]
	v_add_co_u32_e32 v52, vcc, 0x4000, v56
	s_nop 1
	v_addc_co_u32_e32 v53, vcc, 0, v57, vcc
	v_add_co_u32_e32 v58, vcc, 0x8000, v56
	global_load_dwordx4 v[48:51], v[56:57], off nt
	s_nop 0
	global_load_dwordx4 v[52:55], v[52:53], off nt
	v_addc_co_u32_e32 v59, vcc, 0, v57, vcc
	v_add_co_u32_e32 v60, vcc, 0xc000, v56
	s_nop 1
	v_addc_co_u32_e32 v61, vcc, 0, v57, vcc
	global_load_dwordx4 v[56:59], v[58:59], off nt
	s_nop 0
	global_load_dwordx4 v[60:63], v[60:61], off nt
	s_bitset1_b32 s98, 3
	s_branch .LBB0_556
.LBB0_569:
	s_cmp_lt_i32 s94, 7
	s_cselect_b64 s[0:1], -1, 0
	s_and_b64 s[72:73], s[0:1], s[6:7]
	s_and_b64 s[0:1], s[70:71], s[72:73]
	s_andn2_b64 vcc, exec, s[0:1]
	s_cbranch_vccnz .LBB0_578
	s_lshr_b32 s0, s96, 31
	s_add_i32 s0, s96, s0
	s_ashr_i32 s4, s0, 1
	s_add_i32 s5, s77, s76
	s_mul_i32 s6, s4, 10
	s_waitcnt vmcnt(0)
	v_lshrrev_b32_e32 v1, 4, v178
	v_and_b32_e32 v66, 15, v178
	s_cmp_lt_i32 s76, s6
	s_waitcnt lgkmcnt(0)
	v_mov_b32_e32 v0, 0
	s_cselect_b64 s[0:1], -1, 0
	s_cmp_ge_i32 s76, s6
	v_lshlrev_b32_e32 v69, 2, v1
	v_lshlrev_b32_e32 v64, 4, v66
	v_mov_b32_e32 v4, 0
	v_mov_b32_e32 v5, 0
	v_mov_b32_e32 v6, 0
	v_mov_b32_e32 v7, 0
	v_mov_b32_e32 v8, 0
	v_mov_b32_e32 v9, 0
	v_mov_b32_e32 v10, 0
	v_mov_b32_e32 v11, 0
	v_mov_b32_e32 v12, 0
	v_mov_b32_e32 v13, 0
	v_mov_b32_e32 v14, 0
	v_mov_b32_e32 v15, 0
	v_mov_b32_e32 v16, 0
	v_mov_b32_e32 v17, 0
	v_mov_b32_e32 v18, 0
	v_mov_b32_e32 v19, 0
	s_mov_b32 s98, 0
	s_barrier
	s_cbranch_scc1 .LBB0_572
	s_ashr_i32 s7, s5, 31
	s_lshr_b32 s7, s7, 22
	s_add_i32 s7, s5, s7
	s_ashr_i32 s8, s7, 10
	s_and_b32 s7, s7, 0xfffffc00
	s_sub_i32 s7, s5, s7
	s_ashr_i32 s9, s7, 31
	s_lshr_b32 s9, s9, 26
	s_add_i32 s9, s7, s9
	s_ashr_i32 s10, s9, 6
	s_ashr_i32 s9, s8, 31
	s_lshl_b64 s[8:9], s[8:9], 25
	v_lshl_add_u32 v2, s10, 7, v69
	s_add_u32 s8, s80, s8
	v_ashrrev_i32_e32 v3, 31, v2
	s_addc_u32 s9, s81, s9
	v_lshlrev_b64 v[2:3], 14, v[2:3]
	v_lshl_add_u64 v[2:3], s[8:9], 0, v[2:3]
	s_lshl_b32 s8, s10, 12
	s_lshl_b32 s7, s7, 6
	s_sub_i32 s8, s7, s8
	s_ashr_i32 s9, s8, 31
	v_lshl_add_u64 v[2:3], s[8:9], 2, v[2:3]
	v_mov_b32_e32 v65, 0
	v_lshl_add_u64 v[2:3], v[2:3], 0, v[64:65]
	s_movk_i32 s7, 0x4000
	v_add_co_u32_e32 v12, vcc, s7, v2
	s_mov_b32 s7, 0x8000
	s_nop 0
	v_addc_co_u32_e32 v13, vcc, 0, v3, vcc
	v_add_co_u32_e32 v20, vcc, s7, v2
	s_mov_b32 s7, 0xc000
	s_nop 0
	v_addc_co_u32_e32 v21, vcc, 0, v3, vcc
	global_load_dwordx4 v[4:7], v[2:3], off nt
	global_load_dwordx4 v[8:11], v[12:13], off nt
	v_add_co_u32_e32 v2, vcc, s7, v2
	s_nop 1
	v_addc_co_u32_e32 v3, vcc, 0, v3, vcc
	global_load_dwordx4 v[12:15], v[20:21], off nt
	global_load_dwordx4 v[16:19], v[2:3], off nt
	s_bitset1_b32 s98, 0
.LBB0_572:
	s_add_i32 s6, s6, s77
	s_add_i32 s7, s5, s4
	s_cmp_ge_i32 s7, s6
	v_mov_b32_e32 v1, 0
	v_mov_b32_e32 v2, 0
	v_mov_b32_e32 v3, 0
	v_mov_b32_e32 v20, 0
	v_mov_b32_e32 v21, 0
	v_mov_b32_e32 v22, 0
	v_mov_b32_e32 v23, 0
	v_mov_b32_e32 v24, 0
	v_mov_b32_e32 v25, 0
	v_mov_b32_e32 v26, 0
	v_mov_b32_e32 v27, 0
	v_mov_b32_e32 v28, 0
	v_mov_b32_e32 v29, 0
	v_mov_b32_e32 v30, 0
	v_mov_b32_e32 v31, 0
	s_cbranch_scc1 .LBB0_574
	s_ashr_i32 s8, s7, 31
	s_lshr_b32 s8, s8, 22
	s_add_i32 s9, s7, s8
	s_ashr_i32 s8, s9, 10
	s_and_b32 s9, s9, 0xfffffc00
	s_sub_i32 s10, s7, s9
	s_ashr_i32 s9, s10, 31
	s_lshr_b32 s9, s9, 26
	s_add_i32 s9, s10, s9
	s_ashr_i32 s11, s9, 6
	s_ashr_i32 s9, s8, 31
	s_lshl_b64 s[8:9], s[8:9], 25
	v_lshl_add_u32 v0, s11, 7, v69
	s_add_u32 s8, s80, s8
	v_ashrrev_i32_e32 v1, 31, v0
	s_addc_u32 s9, s81, s9
	v_lshlrev_b64 v[0:1], 14, v[0:1]
	v_lshl_add_u64 v[0:1], s[8:9], 0, v[0:1]
	s_lshl_b32 s8, s11, 12
	s_lshl_b32 s9, s10, 6
	s_sub_i32 s8, s9, s8
	s_ashr_i32 s9, s8, 31
	v_lshl_add_u64 v[0:1], s[8:9], 2, v[0:1]
	v_mov_b32_e32 v65, 0
	v_lshl_add_u64 v[24:25], v[0:1], 0, v[64:65]
	s_movk_i32 s8, 0x4000
	v_add_co_u32_e32 v26, vcc, s8, v24
	s_mov_b32 s8, 0x8000
	s_nop 0
	v_addc_co_u32_e32 v27, vcc, 0, v25, vcc
	global_load_dwordx4 v[0:3], v[24:25], off nt
	global_load_dwordx4 v[20:23], v[26:27], off nt
	v_add_co_u32_e32 v26, vcc, s8, v24
	s_mov_b32 s8, 0xc000
	s_nop 0
	v_addc_co_u32_e32 v27, vcc, 0, v25, vcc
	v_add_co_u32_e32 v28, vcc, s8, v24
	s_nop 1
	v_addc_co_u32_e32 v29, vcc, 0, v25, vcc
	global_load_dwordx4 v[24:27], v[26:27], off nt
	s_nop 0
	global_load_dwordx4 v[28:31], v[28:29], off nt
	s_bitset1_b32 s98, 1
.LBB0_574:
	s_add_i32 s7, s7, s4
	s_cmp_ge_i32 s7, s6
	s_cbranch_scc1 .LBB0_576
	s_ashr_i32 s8, s7, 31
	s_lshr_b32 s8, s8, 22
	s_add_i32 s9, s7, s8
	s_ashr_i32 s8, s9, 10
	s_and_b32 s9, s9, 0xfffffc00
	s_sub_i32 s10, s7, s9
	s_ashr_i32 s9, s10, 31
	s_lshr_b32 s9, s9, 26
	s_add_i32 s9, s10, s9
	s_ashr_i32 s11, s9, 6
	s_ashr_i32 s9, s8, 31
	s_lshl_b64 s[8:9], s[8:9], 25
	v_lshl_add_u32 v32, s11, 7, v69
	s_add_u32 s8, s80, s8
	v_ashrrev_i32_e32 v33, 31, v32
	s_addc_u32 s9, s81, s9
	v_lshlrev_b64 v[32:33], 14, v[32:33]
	v_lshl_add_u64 v[32:33], s[8:9], 0, v[32:33]
	s_lshl_b32 s8, s11, 12
	s_lshl_b32 s9, s10, 6
	s_sub_i32 s8, s9, s8
	s_ashr_i32 s9, s8, 31
	v_lshl_add_u64 v[32:33], s[8:9], 2, v[32:33]
	v_mov_b32_e32 v65, 0
	v_lshl_add_u64 v[40:41], v[32:33], 0, v[64:65]
	s_movk_i32 s8, 0x4000
	v_add_co_u32_e32 v42, vcc, s8, v40
	s_nop 1
	v_addc_co_u32_e32 v43, vcc, 0, v41, vcc
	global_load_dwordx4 v[32:35], v[40:41], off nt
	global_load_dwordx4 v[36:39], v[42:43], off nt
	v_add_co_u32_e32 v42, vcc, 0x8000, v40
	s_nop 1
	v_addc_co_u32_e32 v43, vcc, 0, v41, vcc
	v_add_co_u32_e32 v44, vcc, 0xc000, v40
	s_nop 1
	v_addc_co_u32_e32 v45, vcc, 0, v41, vcc
	global_load_dwordx4 v[40:43], v[42:43], off nt
	s_nop 0
	global_load_dwordx4 v[44:47], v[44:45], off nt
	s_bitset1_b32 s98, 2
.LBB0_576:
	s_add_i32 s7, s7, s4
	s_cmp_ge_i32 s7, s6
	s_cbranch_scc1 .LBB0_589
	s_ashr_i32 s8, s7, 31
	s_lshr_b32 s8, s8, 22
	s_add_i32 s9, s7, s8
	s_ashr_i32 s8, s9, 10
	s_and_b32 s9, s9, 0xfffffc00
	s_sub_i32 s7, s7, s9
	s_ashr_i32 s9, s7, 31
	s_lshr_b32 s9, s9, 26
	s_add_i32 s9, s7, s9
	s_ashr_i32 s10, s9, 6
	s_ashr_i32 s9, s8, 31
	s_lshl_b64 s[8:9], s[8:9], 25
	v_lshl_add_u32 v48, s10, 7, v69
	s_add_u32 s8, s80, s8
	v_ashrrev_i32_e32 v49, 31, v48
	s_addc_u32 s9, s81, s9
	v_lshlrev_b64 v[48:49], 14, v[48:49]
	v_lshl_add_u64 v[48:49], s[8:9], 0, v[48:49]
	s_lshl_b32 s8, s10, 12
	s_lshl_b32 s7, s7, 6
	s_sub_i32 s8, s7, s8
	s_ashr_i32 s9, s8, 31
	v_lshl_add_u64 v[48:49], s[8:9], 2, v[48:49]
	v_mov_b32_e32 v65, 0
	v_lshl_add_u64 v[56:57], v[48:49], 0, v[64:65]
	s_movk_i32 s7, 0x4000
	v_add_co_u32_e32 v58, vcc, s7, v56
	s_nop 1
	v_addc_co_u32_e32 v59, vcc, 0, v57, vcc
	v_add_co_u32_e32 v64, vcc, 0x8000, v56
	global_load_dwordx4 v[48:51], v[56:57], off nt
	global_load_dwordx4 v[52:55], v[58:59], off nt
	v_addc_co_u32_e32 v65, vcc, 0, v57, vcc
	v_add_co_u32_e32 v72, vcc, 0xc000, v56
	s_nop 1
	v_addc_co_u32_e32 v73, vcc, 0, v57, vcc
	global_load_dwordx4 v[56:59], v[64:65], off nt
	global_load_dwordx4 v[60:63], v[72:73], off nt
	s_bitset1_b32 s98, 3
	s_andn2_b64 vcc, exec, s[0:1]
	s_cbranch_vccnz .LBB0_604
	s_branch .LBB0_590

.Lcvw_25:
	s_bitset0_b32 s98, 0
	s_ashr_i32 s0, s5, 31
	s_lshr_b32 s0, s0, 22
	v_mul_f32_e32 v66, 0x42800000, v4
	v_mul_f32_e32 v74, 0x42800000, v8
	v_mov_b32_e32 v77, 0
	s_add_i32 s1, s5, s0
	v_cvt_pk_fp8_f32 v77, v66, v74
	v_mul_f32_e32 v66, 0x42800000, v5
	v_mul_f32_e32 v74, 0x42800000, v9
	v_mov_b32_e32 v78, 0
	s_ashr_i32 s0, s1, 10
	s_and_b32 s1, s1, 0xfffffc00
	v_cvt_pk_fp8_f32 v78, v66, v74
	s_sub_i32 s1, s5, s1
	s_ashr_i32 s36, s1, 31
	s_lshr_b32 s36, s36, 26
	v_mul_f32_e32 v66, 0x42800000, v13
	v_mul_f32_e32 v74, 0x42800000, v17
	s_add_i32 s1, s1, s36
	v_cvt_pk_fp8_f32 v78, v66, v74 op_sel:[0,0,1]
	v_mul_f32_e32 v66, 0x42800000, v6
	v_mul_f32_e32 v74, 0x42800000, v10
	v_mov_b32_e32 v79, 0
	s_ashr_i32 s38, s1, 6
	s_ashr_i32 s1, s0, 31
	v_cvt_pk_fp8_f32 v79, v66, v74
	v_mul_f32_e32 v66, 0x42800000, v7
	v_mul_f32_e32 v74, 0x42800000, v11
	v_mov_b32_e32 v80, 0
	s_lshl_b64 s[36:37], s[0:1], 23
	v_cvt_pk_fp8_f32 v80, v66, v74
	s_add_u32 s36, s74, s36
	s_addc_u32 s37, s75, s37
	s_lshl_b32 s1, s38, 9
	s_lshl_b32 s0, s0, 13
	v_mul_f32_e32 v75, 0x42800000, v12
	v_mul_f32_e32 v76, 0x42800000, v16
	s_add_i32 s1, s1, s0
	s_add_i32 s0, s11, s13
	v_cvt_pk_fp8_f32 v77, v75, v76 op_sel:[0,0,1]
	v_mul_f32_e32 v75, 0x42800000, v14
	v_mul_f32_e32 v76, 0x42800000, v18
	v_mul_f32_e32 v66, 0x42800000, v15
	v_mul_f32_e32 v74, 0x42800000, v19
	s_sub_i32 s0, s0, s1
	v_cvt_pk_fp8_f32 v79, v75, v76 op_sel:[0,0,1]
	v_cvt_pk_fp8_f32 v80, v66, v74 op_sel:[0,0,1]
	s_and_b32 s0, s0, -16
	s_add_i32 s0, s0, s38
	s_ashr_i32 s1, s0, 31
	s_add_i32 s38, s8, s9
	ds_write2_b32 v72, v77, v78 offset1:33
	ds_write2_b32 v72, v79, v80 offset0:66 offset1:99
	s_waitcnt lgkmcnt(0)
	s_barrier
	ds_read2_b32 v[74:75], v73 offset1:1
	ds_read2_b32 v[76:77], v73 offset0:2 offset1:3
	s_and_b32 s38, s38, 64
	s_lshl_b64 s[0:1], s[0:1], 14
	s_add_u32 s0, s36, s0
	v_add_lshl_u32 v66, s38, v71, 7
	s_addc_u32 s1, s37, s1
	v_lshl_add_u64 v[78:79], s[0:1], 0, v[66:67]
	s_add_i32 s0, s7, s5
	v_lshl_add_u64 v[78:79], v[78:79], 0, v[64:65]
	s_cmp_ge_i32 s0, s6
	s_waitcnt lgkmcnt(0)
	global_store_dwordx4 v[78:79], v[74:77], off nt
	s_cbranch_scc1 .LBB0_595
	s_ashr_i32 s1, s0, 31
	s_lshr_b32 s1, s1, 22
	s_add_i32 s1, s0, s1
	s_ashr_i32 s36, s1, 10
	s_and_b32 s1, s1, 0xfffffc00
	s_sub_i32 s0, s0, s1
	s_ashr_i32 s1, s0, 31
	s_lshr_b32 s1, s1, 26
	s_add_i32 s0, s0, s1
	s_ashr_i32 s38, s0, 6
	s_ashr_i32 s37, s36, 31
	s_lshl_b64 s[0:1], s[36:37], 25
	v_lshl_add_u32 v4, s38, 7, v69
	s_add_u32 s0, s80, s0
	v_ashrrev_i32_e32 v5, 31, v4
	s_addc_u32 s1, s81, s1
	v_lshlrev_b64 v[4:5], 14, v[4:5]
	v_lshl_add_u64 v[4:5], s[0:1], 0, v[4:5]
	s_lshl_b32 s0, s38, 12
	s_lshl_b32 s1, s36, 16
	s_add_i32 s0, s0, s1
	s_add_i32 s1, s30, s9
	s_sub_i32 s0, s1, s0
	s_ashr_i32 s1, s0, 31
	v_lshl_add_u64 v[4:5], s[0:1], 2, v[4:5]
	v_lshlrev_b32_e32 v66, 2, v68
	v_lshl_add_u64 v[12:13], v[4:5], 0, v[66:67]
	v_add_co_u32_e32 v8, vcc, s31, v12
	s_nop 1
	v_addc_co_u32_e32 v9, vcc, 0, v13, vcc
	v_add_co_u32_e32 v14, vcc, s34, v12
	global_load_dwordx4 v[4:7], v[12:13], off nt
	s_nop 0
	global_load_dwordx4 v[8:11], v[8:9], off nt
	v_addc_co_u32_e32 v15, vcc, 0, v13, vcc
	v_add_co_u32_e32 v16, vcc, s35, v12
	s_nop 1
	v_addc_co_u32_e32 v17, vcc, 0, v13, vcc
	global_load_dwordx4 v[12:15], v[14:15], off nt
	s_nop 0
	global_load_dwordx4 v[16:19], v[16:17], off nt
	s_bitset1_b32 s98, 0
.LBB0_595:
	s_add_i32 s36, s5, s4
	s_cmp_ge_i32 s36, s6
	s_mov_b64 s[0:1], -1
	s_cbranch_scc1 .LBB0_592
	s_waitcnt vmcnt(12)
	s_cmp_eq_u32 s98, 15
	s_cbranch_scc1 .Lcvw_26
	s_waitcnt vmcnt(0)
.Lcvw_26:
	s_bitset0_b32 s98, 1
	s_ashr_i32 s0, s36, 31
	s_lshr_b32 s0, s0, 22
	v_mul_f32_e32 v66, 0x42800000, v0
	v_mul_f32_e32 v74, 0x42800000, v20
	v_mov_b32_e32 v77, v67
	s_add_i32 s1, s36, s0
	v_cvt_pk_fp8_f32 v77, v66, v74
	v_mul_f32_e32 v66, 0x42800000, v1
	v_mul_f32_e32 v74, 0x42800000, v21
	v_mov_b32_e32 v78, v67
	s_ashr_i32 s0, s1, 10
	s_and_b32 s1, s1, 0xfffffc00
	v_cvt_pk_fp8_f32 v78, v66, v74
	s_sub_i32 s1, s36, s1
	s_ashr_i32 s37, s1, 31
	s_lshr_b32 s37, s37, 26
	v_mul_f32_e32 v66, 0x42800000, v25
	v_mul_f32_e32 v74, 0x42800000, v29
	s_add_i32 s1, s1, s37
	v_cvt_pk_fp8_f32 v78, v66, v74 op_sel:[0,0,1]
	v_mul_f32_e32 v66, 0x42800000, v2
	v_mul_f32_e32 v74, 0x42800000, v22
	v_mov_b32_e32 v79, v67
	s_ashr_i32 s37, s1, 6
	s_ashr_i32 s1, s0, 31
	v_cvt_pk_fp8_f32 v79, v66, v74
	v_mul_f32_e32 v66, 0x42800000, v3
	v_mul_f32_e32 v74, 0x42800000, v23
	v_mov_b32_e32 v80, v67
	s_lshl_b64 s[38:39], s[0:1], 23
	v_cvt_pk_fp8_f32 v80, v66, v74
	s_add_u32 s38, s74, s38
	s_addc_u32 s39, s75, s39
	s_lshl_b32 s1, s37, 9
	s_lshl_b32 s0, s0, 13
	v_mul_f32_e32 v75, 0x42800000, v24
	v_mul_f32_e32 v76, 0x42800000, v28
	s_add_i32 s1, s1, s0
	s_add_i32 s0, s12, s13
	v_cvt_pk_fp8_f32 v77, v75, v76 op_sel:[0,0,1]
	v_mul_f32_e32 v75, 0x42800000, v26
	v_mul_f32_e32 v76, 0x42800000, v30
	v_mul_f32_e32 v66, 0x42800000, v27
	v_mul_f32_e32 v74, 0x42800000, v31
	s_sub_i32 s0, s0, s1
	v_cvt_pk_fp8_f32 v79, v75, v76 op_sel:[0,0,1]
	v_cvt_pk_fp8_f32 v80, v66, v74 op_sel:[0,0,1]
	s_and_b32 s0, s0, -16
	s_add_i32 s0, s0, s37
	v_add_u32_e32 v74, 0x2000, v72
	v_add_u32_e32 v75, 0x2200, v73
	s_ashr_i32 s1, s0, 31
	s_add_i32 s37, s17, s9
	ds_write2_b32 v74, v77, v78 offset0:128 offset1:161
	ds_write2_b32 v74, v79, v80 offset0:194 offset1:227
	s_waitcnt lgkmcnt(0)
	s_barrier
	v_add_u32_e32 v76, 0x2208, v73
	ds_read2_b32 v[78:79], v75 offset1:1
	ds_read2_b32 v[80:81], v76 offset1:1
	s_and_b32 s37, s37, 64
	s_lshl_b64 s[0:1], s[0:1], 14
	s_add_u32 s0, s38, s0
	v_add_lshl_u32 v66, s37, v71, 7
	s_addc_u32 s1, s39, s1
	v_lshl_add_u64 v[82:83], s[0:1], 0, v[66:67]
	s_add_i32 s0, s18, s5
	v_lshl_add_u64 v[82:83], v[82:83], 0, v[64:65]
	s_cmp_ge_i32 s0, s6
	s_waitcnt lgkmcnt(0)
	global_store_dwordx4 v[82:83], v[78:81], off nt
	s_cbranch_scc1 .LBB0_598
	s_ashr_i32 s1, s0, 31
	s_lshr_b32 s1, s1, 22
	s_add_i32 s1, s0, s1
	s_ashr_i32 s38, s1, 10
	s_and_b32 s1, s1, 0xfffffc00
	s_sub_i32 s0, s0, s1
	s_ashr_i32 s1, s0, 31
	s_lshr_b32 s1, s1, 26
	s_add_i32 s0, s0, s1
	s_ashr_i32 s37, s0, 6
	s_ashr_i32 s39, s38, 31
	s_lshl_b64 s[0:1], s[38:39], 25
	v_lshl_add_u32 v0, s37, 7, v69
	s_add_u32 s0, s80, s0
	v_ashrrev_i32_e32 v1, 31, v0
	s_addc_u32 s1, s81, s1
	v_lshlrev_b64 v[0:1], 14, v[0:1]
	v_lshl_add_u64 v[0:1], s[0:1], 0, v[0:1]
	s_lshl_b32 s0, s37, 12
	s_lshl_b32 s1, s38, 16
	s_add_i32 s0, s0, s1
	s_add_i32 s1, s19, s9
	s_sub_i32 s0, s1, s0
	s_ashr_i32 s1, s0, 31
	v_lshl_add_u64 v[0:1], s[0:1], 2, v[0:1]
	v_lshlrev_b32_e32 v66, 2, v68
	v_lshl_add_u64 v[24:25], v[0:1], 0, v[66:67]
	v_add_co_u32_e32 v20, vcc, s31, v24
	s_nop 1
	v_addc_co_u32_e32 v21, vcc, 0, v25, vcc
	v_add_co_u32_e32 v26, vcc, s34, v24
	global_load_dwordx4 v[0:3], v[24:25], off nt
	s_nop 0
	global_load_dwordx4 v[20:23], v[20:21], off nt
	v_addc_co_u32_e32 v27, vcc, 0, v25, vcc
	v_add_co_u32_e32 v28, vcc, s35, v24
	s_nop 1
	v_addc_co_u32_e32 v29, vcc, 0, v25, vcc
	global_load_dwordx4 v[24:27], v[26:27], off nt
	s_nop 0
	global_load_dwordx4 v[28:31], v[28:29], off nt
	s_bitset1_b32 s98, 1
.LBB0_598:
	s_add_i32 s37, s20, s5
	s_cmp_ge_i32 s37, s6
	s_mov_b64 s[0:1], -1
	s_cbranch_scc1 .LBB0_592
	s_waitcnt vmcnt(12)
	s_cmp_eq_u32 s98, 15
	s_cbranch_scc1 .Lcvw_27
	s_waitcnt vmcnt(0)
.Lcvw_27:
	s_bitset0_b32 s98, 2
	s_ashr_i32 s0, s37, 31
	s_lshr_b32 s0, s0, 22
	v_mul_f32_e32 v66, 0x42800000, v32
	v_mul_f32_e32 v77, 0x42800000, v36
	v_mov_b32_e32 v80, v67
	s_add_i32 s1, s37, s0
	v_cvt_pk_fp8_f32 v80, v66, v77
	v_mul_f32_e32 v66, 0x42800000, v33
	v_mul_f32_e32 v77, 0x42800000, v37
	v_mov_b32_e32 v81, v67
	s_ashr_i32 s0, s1, 10
	s_and_b32 s1, s1, 0xfffffc00
	v_cvt_pk_fp8_f32 v81, v66, v77
	s_sub_i32 s1, s37, s1
	s_ashr_i32 s37, s1, 31
	s_lshr_b32 s37, s37, 26
	v_mul_f32_e32 v66, 0x42800000, v41
	v_mul_f32_e32 v77, 0x42800000, v45
	s_add_i32 s1, s1, s37
	v_cvt_pk_fp8_f32 v81, v66, v77 op_sel:[0,0,1]
	v_mul_f32_e32 v66, 0x42800000, v34
	v_mul_f32_e32 v77, 0x42800000, v38
	v_mov_b32_e32 v82, v67
	s_ashr_i32 s37, s1, 6
	s_ashr_i32 s1, s0, 31
	v_cvt_pk_fp8_f32 v82, v66, v77
	v_mul_f32_e32 v66, 0x42800000, v35
	v_mul_f32_e32 v77, 0x42800000, v39
	v_mov_b32_e32 v83, v67
	s_lshl_b64 s[38:39], s[0:1], 23
	v_cvt_pk_fp8_f32 v83, v66, v77
	s_add_u32 s38, s74, s38
	s_addc_u32 s39, s75, s39
	s_lshl_b32 s1, s37, 9
	s_lshl_b32 s0, s0, 13
	v_mul_f32_e32 v78, 0x42800000, v40
	v_mul_f32_e32 v79, 0x42800000, v44
	s_add_i32 s1, s1, s0
	s_add_i32 s0, s21, s13
	v_cvt_pk_fp8_f32 v80, v78, v79 op_sel:[0,0,1]
	v_mul_f32_e32 v78, 0x42800000, v42
	v_mul_f32_e32 v79, 0x42800000, v46
	v_mul_f32_e32 v66, 0x42800000, v43
	v_mul_f32_e32 v77, 0x42800000, v47
	s_sub_i32 s0, s0, s1
	v_cvt_pk_fp8_f32 v82, v78, v79 op_sel:[0,0,1]
	v_cvt_pk_fp8_f32 v83, v66, v77 op_sel:[0,0,1]
	s_and_b32 s0, s0, -16
	s_add_i32 s0, s0, s37
	s_ashr_i32 s1, s0, 31
	s_add_i32 s37, s22, s9
	ds_write2_b32 v72, v80, v81 offset1:33
	ds_write2_b32 v72, v82, v83 offset0:66 offset1:99
	s_waitcnt lgkmcnt(0)
	s_barrier
	ds_read2_b32 v[78:79], v73 offset1:1
	ds_read2_b32 v[80:81], v73 offset0:2 offset1:3
	s_and_b32 s37, s37, 64
	s_lshl_b64 s[0:1], s[0:1], 14
	s_add_u32 s0, s38, s0
	v_add_lshl_u32 v66, s37, v71, 7
	s_addc_u32 s1, s39, s1
	v_lshl_add_u64 v[82:83], s[0:1], 0, v[66:67]
	s_add_i32 s0, s23, s5
	v_lshl_add_u64 v[82:83], v[82:83], 0, v[64:65]
	s_cmp_ge_i32 s0, s6
	s_waitcnt lgkmcnt(0)
	global_store_dwordx4 v[82:83], v[78:81], off nt
	s_cbranch_scc1 .LBB0_601
	s_ashr_i32 s1, s0, 31
	s_lshr_b32 s1, s1, 22
	s_add_i32 s1, s0, s1
	s_ashr_i32 s38, s1, 10
	s_and_b32 s1, s1, 0xfffffc00
	s_sub_i32 s0, s0, s1
	s_ashr_i32 s1, s0, 31
	s_lshr_b32 s1, s1, 26
	s_add_i32 s0, s0, s1
	s_ashr_i32 s37, s0, 6
	s_ashr_i32 s39, s38, 31
	s_lshl_b64 s[0:1], s[38:39], 25
	v_lshl_add_u32 v32, s37, 7, v69
	s_add_u32 s0, s80, s0
	v_ashrrev_i32_e32 v33, 31, v32
	s_addc_u32 s1, s81, s1
	v_lshlrev_b64 v[32:33], 14, v[32:33]
	v_lshl_add_u64 v[32:33], s[0:1], 0, v[32:33]
	s_lshl_b32 s0, s37, 12
	s_lshl_b32 s1, s38, 16
	s_add_i32 s0, s0, s1
	s_add_i32 s1, s24, s9
	s_sub_i32 s0, s1, s0
	s_ashr_i32 s1, s0, 31
	v_lshl_add_u64 v[32:33], s[0:1], 2, v[32:33]
	v_lshlrev_b32_e32 v66, 2, v68
	v_lshl_add_u64 v[40:41], v[32:33], 0, v[66:67]
	v_add_co_u32_e32 v36, vcc, 0x4000, v40
	s_nop 1
	v_addc_co_u32_e32 v37, vcc, 0, v41, vcc
	v_add_co_u32_e32 v42, vcc, 0x8000, v40
	global_load_dwordx4 v[32:35], v[40:41], off nt
	s_nop 0
	global_load_dwordx4 v[36:39], v[36:37], off nt
	v_addc_co_u32_e32 v43, vcc, 0, v41, vcc
	v_add_co_u32_e32 v44, vcc, 0xc000, v40
	s_nop 1
	v_addc_co_u32_e32 v45, vcc, 0, v41, vcc
	global_load_dwordx4 v[40:43], v[42:43], off nt
	s_nop 0
	global_load_dwordx4 v[44:47], v[44:45], off nt
	s_bitset1_b32 s98, 2
.LBB0_601:
	s_add_i32 s37, s25, s5
	s_cmp_ge_i32 s37, s6
	s_mov_b64 s[0:1], -1
	s_cbranch_scc1 .LBB0_592
	s_waitcnt vmcnt(12)
	s_cmp_eq_u32 s98, 15
	s_cbranch_scc1 .Lcvw_28
	s_waitcnt vmcnt(0)
.Lcvw_28:
	s_bitset0_b32 s98, 3
	s_ashr_i32 s0, s37, 31
	s_lshr_b32 s0, s0, 22
	v_mul_f32_e32 v66, 0x42800000, v48
	v_mul_f32_e32 v77, 0x42800000, v52
	v_mov_b32_e32 v80, v67
	s_add_i32 s1, s37, s0
	v_cvt_pk_fp8_f32 v80, v66, v77
	v_mul_f32_e32 v66, 0x42800000, v49
	v_mul_f32_e32 v77, 0x42800000, v53
	v_mov_b32_e32 v81, v67
	s_ashr_i32 s0, s1, 10
	s_and_b32 s1, s1, 0xfffffc00
	v_cvt_pk_fp8_f32 v81, v66, v77
	s_sub_i32 s1, s37, s1
	s_ashr_i32 s37, s1, 31
	s_lshr_b32 s37, s37, 26
	v_mul_f32_e32 v66, 0x42800000, v57
	v_mul_f32_e32 v77, 0x42800000, v61
	s_add_i32 s1, s1, s37
	v_cvt_pk_fp8_f32 v81, v66, v77 op_sel:[0,0,1]
	v_mul_f32_e32 v66, 0x42800000, v50
	v_mul_f32_e32 v77, 0x42800000, v54
	v_mov_b32_e32 v82, v67
	s_ashr_i32 s37, s1, 6
	s_ashr_i32 s1, s0, 31
	v_cvt_pk_fp8_f32 v82, v66, v77
	v_mul_f32_e32 v66, 0x42800000, v51
	v_mul_f32_e32 v77, 0x42800000, v55
	v_mov_b32_e32 v83, v67
	s_lshl_b64 s[38:39], s[0:1], 23
	v_cvt_pk_fp8_f32 v83, v66, v77
	s_add_u32 s38, s74, s38
	s_addc_u32 s39, s75, s39
	s_lshl_b32 s1, s37, 9
	s_lshl_b32 s0, s0, 13
	v_mul_f32_e32 v78, 0x42800000, v56
	v_mul_f32_e32 v79, 0x42800000, v60
	s_add_i32 s1, s1, s0
	s_add_i32 s0, s26, s13
	v_cvt_pk_fp8_f32 v80, v78, v79 op_sel:[0,0,1]
	v_mul_f32_e32 v78, 0x42800000, v58
	v_mul_f32_e32 v79, 0x42800000, v62
	v_mul_f32_e32 v66, 0x42800000, v59
	v_mul_f32_e32 v77, 0x42800000, v63
	s_sub_i32 s0, s0, s1
	v_cvt_pk_fp8_f32 v82, v78, v79 op_sel:[0,0,1]
	v_cvt_pk_fp8_f32 v83, v66, v77 op_sel:[0,0,1]
	s_and_b32 s0, s0, -16
	s_add_i32 s0, s0, s37
	s_ashr_i32 s1, s0, 31
	s_add_i32 s37, s27, s9
	ds_write2_b32 v74, v80, v81 offset0:128 offset1:161
	ds_write2_b32 v74, v82, v83 offset0:194 offset1:227
	s_waitcnt lgkmcnt(0)
	s_barrier
	ds_read2_b32 v[74:75], v75 offset1:1
	ds_read2_b32 v[76:77], v76 offset1:1
	s_and_b32 s37, s37, 64
	s_lshl_b64 s[0:1], s[0:1], 14
	s_add_u32 s0, s38, s0
	v_add_lshl_u32 v66, s37, v71, 7
	s_addc_u32 s1, s39, s1
	v_lshl_add_u64 v[78:79], s[0:1], 0, v[66:67]
	s_add_i32 s0, s28, s5
	v_lshl_add_u64 v[78:79], v[78:79], 0, v[64:65]
	s_cmp_ge_i32 s0, s6
	s_waitcnt lgkmcnt(0)
	global_store_dwordx4 v[78:79], v[74:77], off nt
	s_cbranch_scc1 .LBB0_591
	s_ashr_i32 s1, s0, 31
	s_lshr_b32 s1, s1, 22
	s_add_i32 s1, s0, s1
	s_ashr_i32 s38, s1, 10
	s_and_b32 s1, s1, 0xfffffc00
	s_sub_i32 s0, s0, s1
	s_ashr_i32 s1, s0, 31
	s_lshr_b32 s1, s1, 26
	s_add_i32 s0, s0, s1
	s_ashr_i32 s5, s0, 6
	s_ashr_i32 s39, s38, 31
	s_lshl_b64 s[0:1], s[38:39], 25
	v_lshl_add_u32 v48, s5, 7, v69
	s_add_u32 s0, s80, s0
	v_ashrrev_i32_e32 v49, 31, v48
	s_addc_u32 s1, s81, s1
	v_lshlrev_b64 v[48:49], 14, v[48:49]
	v_lshl_add_u64 v[48:49], s[0:1], 0, v[48:49]
	s_lshl_b32 s0, s5, 12
	s_lshl_b32 s1, s38, 16
	s_add_i32 s0, s0, s1
	s_add_i32 s1, s29, s9
	s_sub_i32 s0, s1, s0
	s_ashr_i32 s1, s0, 31
	v_lshl_add_u64 v[48:49], s[0:1], 2, v[48:49]
	v_lshlrev_b32_e32 v66, 2, v68
	v_lshl_add_u64 v[56:57], v[48:49], 0, v[66:67]
	v_add_co_u32_e32 v52, vcc, 0x4000, v56
	s_nop 1
	v_addc_co_u32_e32 v53, vcc, 0, v57, vcc
	v_add_co_u32_e32 v58, vcc, 0x8000, v56
	global_load_dwordx4 v[48:51], v[56:57], off nt
	s_nop 0
	global_load_dwordx4 v[52:55], v[52:53], off nt
	v_addc_co_u32_e32 v59, vcc, 0, v57, vcc
	v_add_co_u32_e32 v60, vcc, 0xc000, v56
	s_nop 1
	v_addc_co_u32_e32 v61, vcc, 0, v57, vcc
	global_load_dwordx4 v[56:59], v[58:59], off nt
	s_nop 0
	global_load_dwordx4 v[60:63], v[60:61], off nt
	s_bitset1_b32 s98, 3
	s_branch .LBB0_591

.LBB0_672:
	s_cmp_lt_i32 s25, s16
	s_cselect_b32 s8, 4, 2
	s_and_b64 s[6:7], s[6:7], exec
	s_cselect_b32 s6, 8, s8
	s_ashr_i32 s7, s10, 31
	s_lshr_b32 s7, s7, 22
	s_add_i32 s7, s10, s7
	s_ashr_i32 s8, s7, 10
	s_and_b32 s7, s7, 0xfffffc00
	s_sub_i32 s7, s10, s7
	s_ashr_i32 s9, s7, 31
	s_lshr_b32 s9, s9, 26
	s_add_i32 s9, s7, s9
	s_ashr_i32 s25, s9, 6
	s_ashr_i32 s9, s8, 31
	s_lshl_b64 s[8:9], s[8:9], 25
	v_lshl_add_u32 v0, s25, 7, v72
	s_add_u32 s8, s80, s8
	v_ashrrev_i32_e32 v1, 31, v0
	s_addc_u32 s9, s81, s9
	v_lshlrev_b64 v[0:1], 14, v[0:1]
	v_lshl_add_u64 v[0:1], s[8:9], 0, v[0:1]
	s_lshl_b32 s8, s25, 12
	s_lshl_b32 s7, s7, 6
	s_sub_i32 s8, s7, s8
	s_ashr_i32 s9, s8, 31
	v_lshl_add_u64 v[0:1], s[8:9], 2, v[0:1]
	v_mov_b32_e32 v69, v65
	s_waitcnt vmcnt(1)
	v_lshl_add_u64 v[8:9], v[0:1], 0, v[68:69]
	v_add_co_u32_e32 v4, vcc, s22, v8
	s_nop 1
	v_addc_co_u32_e32 v5, vcc, 0, v9, vcc
	v_add_co_u32_e32 v10, vcc, 0x8000, v8
	s_mov_b32 s98, 0
	s_barrier
	s_nop 0
	v_addc_co_u32_e32 v11, vcc, 0, v9, vcc
	s_waitcnt vmcnt(0)
	v_add_co_u32_e32 v12, vcc, 0xc000, v8
	s_nop 1
	v_addc_co_u32_e32 v13, vcc, 0, v9, vcc
	global_load_dwordx4 v[0:3], v[8:9], off nt
	s_nop 0
	global_load_dwordx4 v[4:7], v[4:5], off nt
	s_nop 0
	global_load_dwordx4 v[8:11], v[10:11], off nt
	s_nop 0
	global_load_dwordx4 v[12:15], v[12:13], off nt
	s_bitset1_b32 s98, 0
	s_add_i32 s7, s10, 1
	v_mov_b32_e32 v16, 0
	s_cmp_le_i32 s13, s7
	v_mov_b32_e32 v17, v16
	v_mov_b32_e32 v18, v16
	v_mov_b32_e32 v19, v16
	v_mov_b32_e32 v20, v16
	v_mov_b32_e32 v21, v16
	v_mov_b32_e32 v22, v16
	v_mov_b32_e32 v23, v16
	v_mov_b32_e32 v24, v16
	v_mov_b32_e32 v25, v16
	v_mov_b32_e32 v26, v16
	v_mov_b32_e32 v27, v16
	v_mov_b32_e32 v28, v16
	v_mov_b32_e32 v29, v16
	v_mov_b32_e32 v30, v16
	v_mov_b32_e32 v31, v16
	s_cbranch_scc1 .LBB0_674
	s_ashr_i32 s8, s7, 31
	s_lshr_b32 s8, s8, 22
	s_add_i32 s9, s7, s8
	s_ashr_i32 s8, s9, 10
	s_and_b32 s9, s9, 0xfffffc00
	s_sub_i32 s7, s7, s9
	s_ashr_i32 s9, s7, 31
	s_lshr_b32 s9, s9, 26
	s_add_i32 s9, s7, s9
	s_ashr_i32 s25, s9, 6
	s_ashr_i32 s9, s8, 31
	s_lshl_b64 s[8:9], s[8:9], 25
	v_lshl_add_u32 v16, s25, 7, v72
	s_add_u32 s8, s80, s8
	v_ashrrev_i32_e32 v17, 31, v16
	s_addc_u32 s9, s81, s9
	v_lshlrev_b64 v[16:17], 14, v[16:17]
	v_lshl_add_u64 v[16:17], s[8:9], 0, v[16:17]
	s_lshl_b32 s8, s25, 12
	s_lshl_b32 s7, s7, 6
	s_sub_i32 s8, s7, s8
	s_ashr_i32 s9, s8, 31
	v_lshl_add_u64 v[16:17], s[8:9], 2, v[16:17]
	v_lshl_add_u64 v[24:25], v[16:17], 0, v[68:69]
	v_add_co_u32_e32 v20, vcc, s22, v24
	s_nop 1
	v_addc_co_u32_e32 v21, vcc, 0, v25, vcc
	v_add_co_u32_e32 v26, vcc, s23, v24
	global_load_dwordx4 v[16:19], v[24:25], off nt
	s_nop 0
	global_load_dwordx4 v[20:23], v[20:21], off nt
	v_addc_co_u32_e32 v27, vcc, 0, v25, vcc
	v_add_co_u32_e32 v28, vcc, s24, v24
	s_nop 1
	v_addc_co_u32_e32 v29, vcc, 0, v25, vcc
	global_load_dwordx4 v[24:27], v[26:27], off nt
	s_nop 0
	global_load_dwordx4 v[28:31], v[28:29], off nt
	s_bitset1_b32 s98, 1
.LBB0_674:
	s_add_i32 s6, s10, s6
	s_min_i32 s8, s6, s13
	s_add_i32 s6, s10, 2
	s_cmp_ge_i32 s6, s8
	s_cbranch_scc1 .LBB0_676
	s_ashr_i32 s7, s6, 31
	s_lshr_b32 s7, s7, 22
	s_add_i32 s7, s6, s7
	s_ashr_i32 s26, s7, 10
	s_and_b32 s7, s7, 0xfffffc00
	s_sub_i32 s9, s6, s7
	s_ashr_i32 s6, s9, 31
	s_lshr_b32 s6, s6, 26
	s_add_i32 s6, s9, s6
	s_ashr_i32 s25, s6, 6
	s_ashr_i32 s27, s26, 31
	s_lshl_b64 s[6:7], s[26:27], 25
	v_lshl_add_u32 v32, s25, 7, v72
	s_add_u32 s6, s80, s6
	v_ashrrev_i32_e32 v33, 31, v32
	s_addc_u32 s7, s81, s7
	v_lshlrev_b64 v[32:33], 14, v[32:33]
	v_lshl_add_u64 v[32:33], s[6:7], 0, v[32:33]
	s_lshl_b32 s6, s25, 12
	s_lshl_b32 s7, s9, 6
	s_sub_i32 s6, s7, s6
	s_ashr_i32 s7, s6, 31
	v_lshl_add_u64 v[32:33], s[6:7], 2, v[32:33]
	v_mov_b32_e32 v69, v65
	v_lshl_add_u64 v[40:41], v[32:33], 0, v[68:69]
	v_add_co_u32_e32 v36, vcc, 0x4000, v40
	s_nop 1
	v_addc_co_u32_e32 v37, vcc, 0, v41, vcc
	v_add_co_u32_e32 v42, vcc, 0x8000, v40
	global_load_dwordx4 v[32:35], v[40:41], off nt
	s_nop 0
	global_load_dwordx4 v[36:39], v[36:37], off nt
	v_addc_co_u32_e32 v43, vcc, 0, v41, vcc
	v_add_co_u32_e32 v44, vcc, 0xc000, v40
	s_nop 1
	v_addc_co_u32_e32 v45, vcc, 0, v41, vcc
	global_load_dwordx4 v[40:43], v[42:43], off nt
	s_nop 0
	global_load_dwordx4 v[44:47], v[44:45], off nt
	s_bitset1_b32 s98, 2
.LBB0_676:
	s_add_i32 s6, s10, 3
	s_cmp_ge_i32 s6, s8
	s_cbranch_scc1 .LBB0_678
	s_ashr_i32 s7, s6, 31
	s_lshr_b32 s7, s7, 22
	s_add_i32 s7, s6, s7
	s_ashr_i32 s26, s7, 10
	s_and_b32 s7, s7, 0xfffffc00
	s_sub_i32 s9, s6, s7
	s_ashr_i32 s6, s9, 31
	s_lshr_b32 s6, s6, 26
	s_add_i32 s6, s9, s6
	s_ashr_i32 s10, s6, 6
	s_ashr_i32 s27, s26, 31
	s_lshl_b64 s[6:7], s[26:27], 25
	v_lshl_add_u32 v48, s10, 7, v72
	s_add_u32 s6, s80, s6
	v_ashrrev_i32_e32 v49, 31, v48
	s_addc_u32 s7, s81, s7
	v_lshlrev_b64 v[48:49], 14, v[48:49]
	v_lshl_add_u64 v[48:49], s[6:7], 0, v[48:49]
	s_lshl_b32 s6, s10, 12
	s_lshl_b32 s7, s9, 6
	s_sub_i32 s6, s7, s6
	s_ashr_i32 s7, s6, 31
	v_lshl_add_u64 v[48:49], s[6:7], 2, v[48:49]
	v_mov_b32_e32 v69, v65
	v_lshl_add_u64 v[56:57], v[48:49], 0, v[68:69]
	v_add_co_u32_e32 v52, vcc, 0x4000, v56
	s_nop 1
	v_addc_co_u32_e32 v53, vcc, 0, v57, vcc
	v_add_co_u32_e32 v58, vcc, 0x8000, v56
	global_load_dwordx4 v[48:51], v[56:57], off nt
	s_nop 0
	global_load_dwordx4 v[52:55], v[52:53], off nt
	v_addc_co_u32_e32 v59, vcc, 0, v57, vcc
	v_add_co_u32_e32 v60, vcc, 0xc000, v56
	s_nop 1
	v_addc_co_u32_e32 v61, vcc, 0, v57, vcc
	global_load_dwordx4 v[56:59], v[58:59], off nt
	s_nop 0
	global_load_dwordx4 v[60:63], v[60:61], off nt
	s_bitset1_b32 s98, 3

.Lcvw_29:
	s_bitset0_b32 s98, 0
	s_add_i32 s6, s10, -7
	s_ashr_i32 s7, s6, 31
	s_lshr_b32 s7, s7, 22
	s_add_i32 s7, s6, s7
	v_mul_f32_e32 v64, 0x42800000, v0
	v_mul_f32_e32 v69, 0x42800000, v4
	v_mov_b32_e32 v78, v65
	s_ashr_i32 s6, s7, 10
	s_and_b32 s7, s7, 0xfffffc00
	v_cvt_pk_fp8_f32 v78, v64, v69
	v_mul_f32_e32 v64, 0x42800000, v1
	v_mul_f32_e32 v69, 0x42800000, v5
	v_mov_b32_e32 v79, v65
	s_sub_i32 s7, s10, s7
	v_cvt_pk_fp8_f32 v79, v64, v69
	s_add_i32 s7, s7, -7
	s_ashr_i32 s26, s7, 31
	s_lshr_b32 s26, s26, 26
	v_mul_f32_e32 v64, 0x42800000, v9
	v_mul_f32_e32 v69, 0x42800000, v13
	s_add_i32 s7, s7, s26
	v_cvt_pk_fp8_f32 v79, v64, v69 op_sel:[0,0,1]
	v_mul_f32_e32 v64, 0x42800000, v2
	v_mul_f32_e32 v69, 0x42800000, v6
	v_mov_b32_e32 v80, v65
	s_ashr_i32 s29, s7, 6
	s_ashr_i32 s7, s6, 31
	v_cvt_pk_fp8_f32 v80, v64, v69
	v_mul_f32_e32 v64, 0x42800000, v3
	v_mul_f32_e32 v69, 0x42800000, v7
	v_mov_b32_e32 v81, v65
	s_lshl_b64 s[26:27], s[6:7], 23
	v_cvt_pk_fp8_f32 v81, v64, v69
	s_add_u32 s26, s74, s26
	s_addc_u32 s30, s75, s27
	s_lshl_b32 s7, s29, 9
	s_lshl_b32 s6, s6, 13
	v_mul_f32_e32 v76, 0x42800000, v8
	v_mul_f32_e32 v77, 0x42800000, v12
	s_add_i32 s7, s7, s6
	s_add_i32 s28, s11, s25
	v_cvt_pk_fp8_f32 v78, v76, v77 op_sel:[0,0,1]
	v_mul_f32_e32 v76, 0x42800000, v10
	v_mul_f32_e32 v77, 0x42800000, v14
	v_mul_f32_e32 v64, 0x42800000, v11
	v_mul_f32_e32 v69, 0x42800000, v15
	s_sub_i32 s6, s28, s7
	v_cvt_pk_fp8_f32 v80, v76, v77 op_sel:[0,0,1]
	v_cvt_pk_fp8_f32 v81, v64, v69 op_sel:[0,0,1]
	s_and_b32 s6, s6, -16
	s_add_i32 s6, s6, s29
	v_add_u32_e32 v76, v74, v66
	s_ashr_i32 s7, s6, 31
	s_add_i32 s27, s18, s9
	ds_write2_b32 v75, v78, v79 offset1:33
	ds_write2_b32 v75, v80, v81 offset0:66 offset1:99
	s_waitcnt lgkmcnt(0)
	s_barrier
	ds_read2_b32 v[78:79], v76 offset1:1
	ds_read2_b32 v[80:81], v76 offset0:2 offset1:3
	s_and_b32 s29, s27, 64
	s_lshl_b64 s[6:7], s[6:7], 14
	s_add_u32 s6, s26, s6
	v_add_lshl_u32 v64, s29, v71, 7
	s_addc_u32 s7, s30, s7
	v_lshl_add_u64 v[82:83], s[6:7], 0, v[64:65]
	s_add_i32 s26, s10, -3
	v_lshl_add_u64 v[82:83], v[82:83], 0, v[66:67]
	s_cmp_ge_i32 s26, s8
	s_waitcnt lgkmcnt(0)
	global_store_dwordx4 v[82:83], v[78:81], off nt
	s_cbranch_scc1 .LBB0_683
	s_ashr_i32 s6, s26, 31
	s_lshr_b32 s6, s6, 22
	s_add_i32 s7, s26, s6
	s_ashr_i32 s6, s7, 10
	s_and_b32 s7, s7, 0xfffffc00
	s_sub_i32 s7, s10, s7
	s_add_i32 s7, s7, -3
	s_ashr_i32 s29, s7, 31
	s_lshr_b32 s29, s29, 26
	s_add_i32 s7, s7, s29
	s_ashr_i32 s29, s7, 6
	s_ashr_i32 s7, s6, 31
	s_lshl_b64 s[30:31], s[6:7], 25
	s_add_u32 s30, s80, s30
	s_addc_u32 s31, s81, s31
	s_lshl_b32 s7, s29, 12
	s_lshl_b32 s6, s6, 16
	v_lshl_add_u32 v0, s29, 7, v72
	s_add_i32 s7, s7, s6
	v_ashrrev_i32_e32 v1, 31, v0
	s_sub_i32 s6, s27, s7
	v_lshlrev_b64 v[0:1], 14, v[0:1]
	s_addk_i32 s6, 0x100
	v_lshl_add_u64 v[0:1], s[30:31], 0, v[0:1]
	s_ashr_i32 s7, s6, 31
	v_lshl_add_u64 v[0:1], s[6:7], 2, v[0:1]
	v_mov_b32_e32 v69, v65
	v_lshl_add_u64 v[8:9], v[0:1], 0, v[68:69]
	v_add_co_u32_e32 v4, vcc, s22, v8
	s_nop 1
	v_addc_co_u32_e32 v5, vcc, 0, v9, vcc
	v_add_co_u32_e32 v10, vcc, s23, v8
	global_load_dwordx4 v[0:3], v[8:9], off nt
	s_nop 0
	global_load_dwordx4 v[4:7], v[4:5], off nt
	v_addc_co_u32_e32 v11, vcc, 0, v9, vcc
	v_add_co_u32_e32 v12, vcc, s24, v8
	s_nop 1
	v_addc_co_u32_e32 v13, vcc, 0, v9, vcc
	global_load_dwordx4 v[8:11], v[10:11], off nt
	s_nop 0
	global_load_dwordx4 v[12:15], v[12:13], off nt
	s_bitset1_b32 s98, 0
.LBB0_683:
	s_add_i32 s29, s10, -6
	s_cmp_ge_i32 s29, s8
	s_mov_b64 s[6:7], -1
	s_cbranch_scc1 .LBB0_680
	s_waitcnt vmcnt(12)
	s_cmp_eq_u32 s98, 15
	s_cbranch_scc1 .Lcvw_30
	s_waitcnt vmcnt(0)
.Lcvw_30:
	s_bitset0_b32 s98, 1
	s_ashr_i32 s6, s29, 31
	s_lshr_b32 s6, s6, 22
	s_add_i32 s29, s29, s6
	s_and_b32 s7, s29, 0xfffffc00
	v_mul_f32_e32 v69, 0x42800000, v16
	v_mul_f32_e32 v77, 0x42800000, v20
	v_mov_b32_e32 v80, v65
	s_sub_i32 s7, s10, s7
	v_cvt_pk_fp8_f32 v80, v69, v77
	v_mul_f32_e32 v69, 0x42800000, v17
	v_mul_f32_e32 v77, 0x42800000, v21
	v_mov_b32_e32 v81, v65
	s_add_i32 s7, s7, -6
	v_cvt_pk_fp8_f32 v81, v69, v77
	s_ashr_i32 s6, s29, 10
	s_ashr_i32 s29, s7, 31
	s_lshr_b32 s29, s29, 26
	s_add_i32 s7, s7, s29
	v_mul_f32_e32 v69, 0x42800000, v25
	v_mul_f32_e32 v77, 0x42800000, v29
	s_ashr_i32 s29, s7, 6
	s_ashr_i32 s7, s6, 31
	v_cvt_pk_fp8_f32 v81, v69, v77 op_sel:[0,0,1]
	v_mul_f32_e32 v69, 0x42800000, v18
	v_mul_f32_e32 v77, 0x42800000, v22
	v_mov_b32_e32 v82, v65
	s_lshl_b64 s[30:31], s[6:7], 23
	v_cvt_pk_fp8_f32 v82, v69, v77
	v_mul_f32_e32 v69, 0x42800000, v19
	v_mul_f32_e32 v77, 0x42800000, v23
	v_mov_b32_e32 v83, v65
	s_add_u32 s30, s74, s30
	v_cvt_pk_fp8_f32 v83, v69, v77
	s_addc_u32 s31, s75, s31
	s_lshl_b32 s7, s29, 9
	s_lshl_b32 s6, s6, 13
	s_add_i32 s7, s7, s6
	v_mul_f32_e32 v78, 0x42800000, v24
	v_mul_f32_e32 v79, 0x42800000, v28
	s_sub_i32 s6, s28, s7
	v_cvt_pk_fp8_f32 v80, v78, v79 op_sel:[0,0,1]
	v_mul_f32_e32 v78, 0x42800000, v26
	v_mul_f32_e32 v79, 0x42800000, v30
	v_mul_f32_e32 v69, 0x42800000, v27
	v_mul_f32_e32 v77, 0x42800000, v31
	s_add_i32 s6, s6, 8
	v_cvt_pk_fp8_f32 v82, v78, v79 op_sel:[0,0,1]
	v_cvt_pk_fp8_f32 v83, v69, v77 op_sel:[0,0,1]
	s_and_b32 s6, s6, -16
	s_add_i32 s6, s6, s29
	v_add_u32_e32 v77, 0x2000, v75
	v_add_u32_e32 v78, 0x2200, v76
	s_ashr_i32 s7, s6, 31
	s_add_i32 s29, s27, 64
	ds_write2_b32 v77, v80, v81 offset0:128 offset1:161
	ds_write2_b32 v77, v82, v83 offset0:194 offset1:227
	s_waitcnt lgkmcnt(0)
	s_barrier
	v_add_u32_e32 v79, 0x2208, v76
	ds_read2_b32 v[80:81], v78 offset1:1
	ds_read2_b32 v[82:83], v79 offset1:1
	s_and_b32 s29, s29, 64
	s_lshl_b64 s[6:7], s[6:7], 14
	s_add_u32 s6, s30, s6
	v_add_lshl_u32 v84, s29, v71, 7
	v_mov_b32_e32 v85, v65
	s_addc_u32 s7, s31, s7
	v_lshl_add_u64 v[84:85], s[6:7], 0, v[84:85]
	s_add_i32 s6, s10, -2
	v_lshl_add_u64 v[84:85], v[84:85], 0, v[66:67]
	s_cmp_ge_i32 s6, s8
	s_waitcnt lgkmcnt(0)
	global_store_dwordx4 v[84:85], v[80:83], off nt
	s_cbranch_scc1 .LBB0_686
	s_ashr_i32 s7, s6, 31
	s_lshr_b32 s7, s7, 22
	s_add_i32 s7, s6, s7
	s_ashr_i32 s6, s7, 10
	s_and_b32 s7, s7, 0xfffffc00
	s_sub_i32 s7, s10, s7
	s_add_i32 s7, s7, -2
	s_ashr_i32 s29, s7, 31
	s_lshr_b32 s29, s29, 26
	s_add_i32 s7, s7, s29
	s_ashr_i32 s29, s7, 6
	s_ashr_i32 s7, s6, 31
	s_lshl_b64 s[30:31], s[6:7], 25
	s_add_u32 s30, s80, s30
	s_addc_u32 s31, s81, s31
	s_lshl_b32 s7, s29, 12
	s_lshl_b32 s6, s6, 16
	v_lshl_add_u32 v16, s29, 7, v72
	s_add_i32 s7, s7, s6
	v_ashrrev_i32_e32 v17, 31, v16
	s_sub_i32 s6, s27, s7
	v_lshlrev_b64 v[16:17], 14, v[16:17]
	s_addk_i32 s6, 0x140
	v_lshl_add_u64 v[16:17], s[30:31], 0, v[16:17]
	s_ashr_i32 s7, s6, 31
	v_lshl_add_u64 v[16:17], s[6:7], 2, v[16:17]
	v_mov_b32_e32 v69, v65
	v_lshl_add_u64 v[24:25], v[16:17], 0, v[68:69]
	v_add_co_u32_e32 v20, vcc, s22, v24
	s_nop 1
	v_addc_co_u32_e32 v21, vcc, 0, v25, vcc
	v_add_co_u32_e32 v26, vcc, s23, v24
	global_load_dwordx4 v[16:19], v[24:25], off nt
	s_nop 0
	global_load_dwordx4 v[20:23], v[20:21], off nt
	v_addc_co_u32_e32 v27, vcc, 0, v25, vcc
	v_add_co_u32_e32 v28, vcc, s24, v24
	s_nop 1
	v_addc_co_u32_e32 v29, vcc, 0, v25, vcc
	global_load_dwordx4 v[24:27], v[26:27], off nt
	s_nop 0
	global_load_dwordx4 v[28:31], v[28:29], off nt
	s_bitset1_b32 s98, 1
.LBB0_686:
	s_add_i32 s29, s10, -5
	s_cmp_ge_i32 s29, s8
	s_mov_b64 s[6:7], -1
	s_cbranch_scc1 .LBB0_680
	s_waitcnt vmcnt(12)
	s_cmp_eq_u32 s98, 15
	s_cbranch_scc1 .Lcvw_31
	s_waitcnt vmcnt(0)
.Lcvw_31:
	s_bitset0_b32 s98, 2
	s_ashr_i32 s6, s29, 31
	s_lshr_b32 s6, s6, 22
	s_add_i32 s29, s29, s6
	s_and_b32 s7, s29, 0xfffffc00
	v_mul_f32_e32 v69, 0x42800000, v32
	v_mul_f32_e32 v80, 0x42800000, v36
	v_mov_b32_e32 v83, v65
	s_sub_i32 s7, s10, s7
	v_cvt_pk_fp8_f32 v83, v69, v80
	v_mul_f32_e32 v69, 0x42800000, v33
	v_mul_f32_e32 v80, 0x42800000, v37
	v_mov_b32_e32 v84, v65
	s_add_i32 s7, s7, -5
	v_cvt_pk_fp8_f32 v84, v69, v80
	s_ashr_i32 s6, s29, 10
	s_ashr_i32 s29, s7, 31
	s_lshr_b32 s29, s29, 26
	s_add_i32 s7, s7, s29
	v_mul_f32_e32 v69, 0x42800000, v41
	v_mul_f32_e32 v80, 0x42800000, v45
	s_ashr_i32 s29, s7, 6
	s_ashr_i32 s7, s6, 31
	v_cvt_pk_fp8_f32 v84, v69, v80 op_sel:[0,0,1]
	v_mul_f32_e32 v69, 0x42800000, v34
	v_mul_f32_e32 v80, 0x42800000, v38
	v_mov_b32_e32 v85, v65
	s_lshl_b64 s[30:31], s[6:7], 23
	v_cvt_pk_fp8_f32 v85, v69, v80
	v_mul_f32_e32 v69, 0x42800000, v35
	v_mul_f32_e32 v80, 0x42800000, v39
	v_mov_b32_e32 v86, v65
	s_add_u32 s30, s74, s30
	v_cvt_pk_fp8_f32 v86, v69, v80
	s_addc_u32 s31, s75, s31
	s_lshl_b32 s7, s29, 9
	s_lshl_b32 s6, s6, 13
	s_add_i32 s7, s7, s6
	v_mul_f32_e32 v81, 0x42800000, v40
	v_mul_f32_e32 v82, 0x42800000, v44
	s_sub_i32 s6, s28, s7
	v_cvt_pk_fp8_f32 v83, v81, v82 op_sel:[0,0,1]
	v_mul_f32_e32 v81, 0x42800000, v42
	v_mul_f32_e32 v82, 0x42800000, v46
	v_mul_f32_e32 v69, 0x42800000, v43
	v_mul_f32_e32 v80, 0x42800000, v47
	s_add_i32 s6, s6, 16
	v_cvt_pk_fp8_f32 v85, v81, v82 op_sel:[0,0,1]
	v_cvt_pk_fp8_f32 v86, v69, v80 op_sel:[0,0,1]
	s_and_b32 s6, s6, -16
	s_add_i32 s6, s6, s29
	s_ashr_i32 s7, s6, 31
	ds_write2_b32 v75, v83, v84 offset1:33
	ds_write2_b32 v75, v85, v86 offset0:66 offset1:99
	s_waitcnt lgkmcnt(0)
	s_barrier
	ds_read2_b32 v[80:81], v76 offset1:1
	ds_read2_b32 v[82:83], v76 offset0:2 offset1:3
	s_lshl_b64 s[6:7], s[6:7], 14
	s_add_u32 s6, s30, s6
	s_addc_u32 s7, s31, s7
	v_lshl_add_u64 v[84:85], s[6:7], 0, v[64:65]
	s_add_i32 s6, s10, -1
	v_lshl_add_u64 v[84:85], v[84:85], 0, v[66:67]
	s_cmp_ge_i32 s6, s8
	s_waitcnt lgkmcnt(0)
	global_store_dwordx4 v[84:85], v[80:83], off nt
	s_cbranch_scc1 .LBB0_689
	s_ashr_i32 s7, s6, 31
	s_lshr_b32 s7, s7, 22
	s_add_i32 s7, s6, s7
	s_ashr_i32 s6, s7, 10
	s_orn2_b32 s7, 0x3ff, s7
	s_add_i32 s7, s7, s10
	s_ashr_i32 s29, s7, 31
	s_lshr_b32 s29, s29, 26
	s_add_i32 s7, s7, s29
	s_ashr_i32 s29, s7, 6
	s_ashr_i32 s7, s6, 31
	s_lshl_b64 s[30:31], s[6:7], 25
	s_add_u32 s30, s80, s30
	s_addc_u32 s31, s81, s31
	s_lshl_b32 s7, s29, 12
	s_lshl_b32 s6, s6, 16
	v_lshl_add_u32 v32, s29, 7, v72
	s_add_i32 s7, s7, s6
	v_ashrrev_i32_e32 v33, 31, v32
	s_sub_i32 s6, s27, s7
	v_lshlrev_b64 v[32:33], 14, v[32:33]
	s_addk_i32 s6, 0x180
	v_lshl_add_u64 v[32:33], s[30:31], 0, v[32:33]
	s_ashr_i32 s7, s6, 31
	v_lshl_add_u64 v[32:33], s[6:7], 2, v[32:33]
	v_mov_b32_e32 v69, v65
	v_lshl_add_u64 v[40:41], v[32:33], 0, v[68:69]
	v_add_co_u32_e32 v36, vcc, 0x4000, v40
	s_nop 1
	v_addc_co_u32_e32 v37, vcc, 0, v41, vcc
	v_add_co_u32_e32 v42, vcc, 0x8000, v40
	global_load_dwordx4 v[32:35], v[40:41], off nt
	s_nop 0
	global_load_dwordx4 v[36:39], v[36:37], off nt
	v_addc_co_u32_e32 v43, vcc, 0, v41, vcc
	v_add_co_u32_e32 v44, vcc, 0xc000, v40
	s_nop 1
	v_addc_co_u32_e32 v45, vcc, 0, v41, vcc
	global_load_dwordx4 v[40:43], v[42:43], off nt
	s_nop 0
	global_load_dwordx4 v[44:47], v[44:45], off nt
	s_bitset1_b32 s98, 2
.LBB0_689:
	s_add_i32 s29, s10, -4
	s_cmp_ge_i32 s29, s8
	s_mov_b64 s[6:7], -1
	s_cbranch_scc1 .LBB0_680
	s_waitcnt vmcnt(12)
	s_cmp_eq_u32 s98, 15
	s_cbranch_scc1 .Lcvw_32
	s_waitcnt vmcnt(0)
.Lcvw_32:
	s_bitset0_b32 s98, 3
	s_ashr_i32 s6, s29, 31
	s_lshr_b32 s6, s6, 22
	s_add_i32 s29, s29, s6
	s_and_b32 s7, s29, 0xfffffc00
	v_mul_f32_e32 v64, 0x42800000, v48
	v_mul_f32_e32 v69, 0x42800000, v52
	v_mov_b32_e32 v81, v65
	s_sub_i32 s7, s10, s7
	v_cvt_pk_fp8_f32 v81, v64, v69
	v_mul_f32_e32 v64, 0x42800000, v49
	v_mul_f32_e32 v69, 0x42800000, v53
	v_mov_b32_e32 v82, v65
	s_add_i32 s7, s7, -4
	v_cvt_pk_fp8_f32 v82, v64, v69
	s_ashr_i32 s6, s29, 10
	s_ashr_i32 s29, s7, 31
	s_lshr_b32 s29, s29, 26
	s_add_i32 s7, s7, s29
	v_mul_f32_e32 v64, 0x42800000, v57
	v_mul_f32_e32 v69, 0x42800000, v61
	s_ashr_i32 s29, s7, 6
	s_ashr_i32 s7, s6, 31
	v_cvt_pk_fp8_f32 v82, v64, v69 op_sel:[0,0,1]
	v_mul_f32_e32 v64, 0x42800000, v50
	v_mul_f32_e32 v69, 0x42800000, v54
	v_mov_b32_e32 v83, v65
	s_lshl_b64 s[30:31], s[6:7], 23
	v_cvt_pk_fp8_f32 v83, v64, v69
	v_mul_f32_e32 v64, 0x42800000, v51
	v_mul_f32_e32 v69, 0x42800000, v55
	v_mov_b32_e32 v84, v65
	s_add_u32 s30, s74, s30
	v_cvt_pk_fp8_f32 v84, v64, v69
	s_addc_u32 s31, s75, s31
	s_lshl_b32 s7, s29, 9
	s_lshl_b32 s6, s6, 13
	s_add_i32 s7, s7, s6
	v_mul_f32_e32 v76, 0x42800000, v56
	v_mul_f32_e32 v80, 0x42800000, v60
	s_sub_i32 s6, s28, s7
	v_cvt_pk_fp8_f32 v81, v76, v80 op_sel:[0,0,1]
	v_mul_f32_e32 v76, 0x42800000, v58
	v_mul_f32_e32 v80, 0x42800000, v62
	v_mul_f32_e32 v64, 0x42800000, v59
	v_mul_f32_e32 v69, 0x42800000, v63
	s_add_i32 s6, s6, 24
	v_cvt_pk_fp8_f32 v83, v76, v80 op_sel:[0,0,1]
	v_cvt_pk_fp8_f32 v84, v64, v69 op_sel:[0,0,1]
	s_and_b32 s6, s6, -16
	s_add_i32 s6, s6, s29
	s_ashr_i32 s7, s6, 31
	s_add_i32 s28, s27, 0xc0
	ds_write2_b32 v77, v81, v82 offset0:128 offset1:161
	ds_write2_b32 v77, v83, v84 offset0:194 offset1:227
	s_waitcnt lgkmcnt(0)
	s_barrier
	ds_read2_b32 v[76:77], v78 offset1:1
	ds_read2_b32 v[78:79], v79 offset1:1
	s_and_b32 s28, s28, 64
	s_lshl_b64 s[6:7], s[6:7], 14
	s_add_u32 s6, s30, s6
	v_add_lshl_u32 v64, s28, v71, 7
	s_addc_u32 s7, s31, s7
	v_lshl_add_u64 v[80:81], s[6:7], 0, v[64:65]
	v_lshl_add_u64 v[80:81], v[80:81], 0, v[66:67]
	s_cmp_ge_i32 s10, s8
	s_waitcnt lgkmcnt(0)
	global_store_dwordx4 v[80:81], v[76:79], off nt
	s_cbranch_scc1 .LBB0_679
	s_ashr_i32 s6, s10, 31
	s_lshr_b32 s6, s6, 22
	s_add_i32 s7, s10, s6
	s_ashr_i32 s6, s7, 10
	s_and_b32 s7, s7, 0xfffffc00
	s_sub_i32 s7, s10, s7
	s_ashr_i32 s28, s7, 31
	s_lshr_b32 s28, s28, 26
	s_add_i32 s7, s7, s28
	s_ashr_i32 s30, s7, 6
	s_ashr_i32 s7, s6, 31
	s_lshl_b64 s[28:29], s[6:7], 25
	s_add_u32 s28, s80, s28
	s_addc_u32 s29, s81, s29
	s_lshl_b32 s7, s30, 12
	s_lshl_b32 s6, s6, 16
	v_lshl_add_u32 v48, s30, 7, v72
	s_add_i32 s7, s7, s6
	v_ashrrev_i32_e32 v49, 31, v48
	s_sub_i32 s6, s27, s7
	v_lshlrev_b64 v[48:49], 14, v[48:49]
	s_addk_i32 s6, 0x1c0
	v_lshl_add_u64 v[48:49], s[28:29], 0, v[48:49]
	s_ashr_i32 s7, s6, 31
	v_lshl_add_u64 v[48:49], s[6:7], 2, v[48:49]
	v_mov_b32_e32 v69, v65
	v_lshl_add_u64 v[56:57], v[48:49], 0, v[68:69]
	v_add_co_u32_e32 v52, vcc, 0x4000, v56
	s_nop 1
	v_addc_co_u32_e32 v53, vcc, 0, v57, vcc
	v_add_co_u32_e32 v58, vcc, 0x8000, v56
	global_load_dwordx4 v[48:51], v[56:57], off nt
	s_nop 0
	global_load_dwordx4 v[52:55], v[52:53], off nt
	v_addc_co_u32_e32 v59, vcc, 0, v57, vcc
	v_add_co_u32_e32 v60, vcc, 0xc000, v56
	s_nop 1
	v_addc_co_u32_e32 v61, vcc, 0, v57, vcc
	global_load_dwordx4 v[56:59], v[58:59], off nt
	s_nop 0
	global_load_dwordx4 v[60:63], v[60:61], off nt
	s_bitset1_b32 s98, 3
	s_branch .LBB0_679
.LBB0_692:
	s_cmp_lt_i32 s94, 8
	s_cselect_b64 s[4:5], -1, 0
	s_add_u32 s38, s90, 0x44a20000
	s_addc_u32 s39, s91, 0
	s_and_b64 s[0:1], s[4:5], s[0:1]
	s_and_b64 s[4:5], s[70:71], s[0:1]
	s_andn2_b64 vcc, exec, s[4:5]
	s_mul_i32 s41, s40, 56
	s_cbranch_vccnz .LBB0_701
	s_waitcnt vmcnt(3)
	v_lshrrev_b32_e32 v1, 4, v178
	v_and_b32_e32 v66, 15, v178
	s_cmp_lt_i32 s76, s41
	s_waitcnt lgkmcnt(0)
	v_mov_b32_e32 v0, 0
	s_cselect_b64 s[4:5], -1, 0
	s_cmp_ge_i32 s76, s41
	v_lshlrev_b32_e32 v69, 2, v1
	v_lshlrev_b32_e32 v64, 4, v66
	s_waitcnt vmcnt(2)
	v_mov_b32_e32 v4, 0
	v_mov_b32_e32 v5, 0
	v_mov_b32_e32 v6, 0
	v_mov_b32_e32 v7, 0
	s_waitcnt vmcnt(1)
	v_mov_b32_e32 v8, 0
	v_mov_b32_e32 v9, 0
	v_mov_b32_e32 v10, 0
	v_mov_b32_e32 v11, 0
	s_waitcnt vmcnt(0)
	v_mov_b32_e32 v12, 0
	v_mov_b32_e32 v13, 0
	v_mov_b32_e32 v14, 0
	v_mov_b32_e32 v15, 0
	v_mov_b32_e32 v16, 0
	v_mov_b32_e32 v17, 0
	v_mov_b32_e32 v18, 0
	v_mov_b32_e32 v19, 0
	s_mov_b32 s98, 0
	s_barrier
	s_cbranch_scc1 .LBB0_695
	s_ashr_i32 s6, s76, 31
	s_lshr_b32 s6, s6, 23
	s_add_i32 s7, s76, s6
	s_ashr_i32 s6, s7, 9
	s_and_b32 s7, s7, 0xfffffe00
	s_sub_i32 s8, s76, s7
	s_ashr_i32 s7, s8, 31
	s_lshr_b32 s7, s7, 27
	s_add_i32 s7, s8, s7
	s_ashr_i32 s9, s7, 5
	s_ashr_i32 s7, s6, 31
	s_lshl_b64 s[6:7], s[6:7], 24
	v_lshl_add_u32 v2, s9, 7, v69
	s_add_u32 s6, s84, s6
	v_ashrrev_i32_e32 v3, 31, v2
	s_addc_u32 s7, s85, s7
	v_lshlrev_b64 v[2:3], 13, v[2:3]
	v_lshl_add_u64 v[2:3], s[6:7], 0, v[2:3]
	s_lshl_b32 s6, s9, 11
	s_lshl_b32 s7, s8, 6
	s_sub_i32 s6, s7, s6
	s_ashr_i32 s7, s6, 31
	v_lshl_add_u64 v[2:3], s[6:7], 2, v[2:3]
	v_mov_b32_e32 v65, 0
	v_lshl_add_u64 v[2:3], v[2:3], 0, v[64:65]
	s_movk_i32 s6, 0x2000
	v_add_co_u32_e32 v12, vcc, s6, v2
	s_movk_i32 s6, 0x4000
	s_nop 0
	v_addc_co_u32_e32 v13, vcc, 0, v3, vcc
	v_add_co_u32_e32 v20, vcc, s6, v2
	s_movk_i32 s6, 0x6000
	s_nop 0
	v_addc_co_u32_e32 v21, vcc, 0, v3, vcc
	global_load_dwordx4 v[4:7], v[2:3], off nt
	global_load_dwordx4 v[8:11], v[12:13], off nt
	v_add_co_u32_e32 v2, vcc, s6, v2
	s_nop 1
	v_addc_co_u32_e32 v3, vcc, 0, v3, vcc
	global_load_dwordx4 v[12:15], v[20:21], off nt
	global_load_dwordx4 v[16:19], v[2:3], off nt
	s_bitset1_b32 s98, 0
.LBB0_695:
	s_add_i32 s6, s40, s76
	s_cmp_ge_i32 s6, s41
	v_mov_b32_e32 v1, 0
	v_mov_b32_e32 v2, 0
	v_mov_b32_e32 v3, 0
	v_mov_b32_e32 v20, 0
	v_mov_b32_e32 v21, 0
	v_mov_b32_e32 v22, 0
	v_mov_b32_e32 v23, 0
	v_mov_b32_e32 v24, 0
	v_mov_b32_e32 v25, 0
	v_mov_b32_e32 v26, 0
	v_mov_b32_e32 v27, 0
	v_mov_b32_e32 v28, 0
	v_mov_b32_e32 v29, 0
	v_mov_b32_e32 v30, 0
	v_mov_b32_e32 v31, 0
	s_cbranch_scc1 .LBB0_697
	s_ashr_i32 s7, s6, 31
	s_lshr_b32 s7, s7, 23
	s_add_i32 s7, s6, s7
	s_ashr_i32 s8, s7, 9
	s_and_b32 s7, s7, 0xfffffe00
	s_sub_i32 s7, s6, s7
	s_ashr_i32 s9, s7, 31
	s_lshr_b32 s9, s9, 27
	s_add_i32 s9, s7, s9
	s_ashr_i32 s10, s9, 5
	s_ashr_i32 s9, s8, 31
	s_lshl_b64 s[8:9], s[8:9], 24
	v_lshl_add_u32 v0, s10, 7, v69
	s_add_u32 s8, s84, s8
	v_ashrrev_i32_e32 v1, 31, v0
	s_addc_u32 s9, s85, s9
	v_lshlrev_b64 v[0:1], 13, v[0:1]
	v_lshl_add_u64 v[0:1], s[8:9], 0, v[0:1]
	s_lshl_b32 s8, s10, 11
	s_lshl_b32 s7, s7, 6
	s_sub_i32 s8, s7, s8
	s_ashr_i32 s9, s8, 31
	v_lshl_add_u64 v[0:1], s[8:9], 2, v[0:1]
	v_mov_b32_e32 v65, 0
	v_lshl_add_u64 v[24:25], v[0:1], 0, v[64:65]
	s_movk_i32 s7, 0x2000
	v_add_co_u32_e32 v26, vcc, s7, v24
	s_movk_i32 s7, 0x4000
	s_nop 0
	v_addc_co_u32_e32 v27, vcc, 0, v25, vcc
	v_add_co_u32_e32 v32, vcc, s7, v24
	s_movk_i32 s7, 0x6000
	s_nop 0
	v_addc_co_u32_e32 v33, vcc, 0, v25, vcc
	v_add_co_u32_e32 v34, vcc, s7, v24
	global_load_dwordx4 v[0:3], v[24:25], off nt
	global_load_dwordx4 v[20:23], v[26:27], off nt
	v_addc_co_u32_e32 v35, vcc, 0, v25, vcc
	global_load_dwordx4 v[24:27], v[32:33], off nt
	global_load_dwordx4 v[28:31], v[34:35], off nt
	s_bitset1_b32 s98, 1
.LBB0_697:
	s_add_i32 s6, s6, s40
	s_cmp_ge_i32 s6, s41
	s_cbranch_scc1 .LBB0_699
	s_ashr_i32 s7, s6, 31
	s_lshr_b32 s7, s7, 23
	s_add_i32 s7, s6, s7
	s_ashr_i32 s8, s7, 9
	s_and_b32 s7, s7, 0xfffffe00
	s_sub_i32 s7, s6, s7
	s_ashr_i32 s9, s7, 31
	s_lshr_b32 s9, s9, 27
	s_add_i32 s9, s7, s9
	s_ashr_i32 s10, s9, 5
	s_ashr_i32 s9, s8, 31
	s_lshl_b64 s[8:9], s[8:9], 24
	v_lshl_add_u32 v32, s10, 7, v69
	s_add_u32 s8, s84, s8
	v_ashrrev_i32_e32 v33, 31, v32
	s_addc_u32 s9, s85, s9
	v_lshlrev_b64 v[32:33], 13, v[32:33]
	v_lshl_add_u64 v[32:33], s[8:9], 0, v[32:33]
	s_lshl_b32 s8, s10, 11
	s_lshl_b32 s7, s7, 6
	s_sub_i32 s8, s7, s8
	s_ashr_i32 s9, s8, 31
	v_lshl_add_u64 v[32:33], s[8:9], 2, v[32:33]
	v_mov_b32_e32 v65, 0
	v_lshl_add_u64 v[40:41], v[32:33], 0, v[64:65]
	s_movk_i32 s7, 0x2000
	v_add_co_u32_e32 v42, vcc, s7, v40
	s_nop 1
	v_addc_co_u32_e32 v43, vcc, 0, v41, vcc
	v_add_co_u32_e32 v48, vcc, 0x4000, v40
	global_load_dwordx4 v[32:35], v[40:41], off nt
	global_load_dwordx4 v[36:39], v[42:43], off nt
	v_addc_co_u32_e32 v49, vcc, 0, v41, vcc
	v_add_co_u32_e32 v50, vcc, 0x6000, v40
	s_nop 1
	v_addc_co_u32_e32 v51, vcc, 0, v41, vcc
	global_load_dwordx4 v[40:43], v[48:49], off nt
	global_load_dwordx4 v[44:47], v[50:51], off nt
	s_bitset1_b32 s98, 2
.LBB0_699:
	s_add_i32 s6, s6, s40
	s_cmp_ge_i32 s6, s41
	s_cbranch_scc1 .LBB0_712
	s_ashr_i32 s7, s6, 31
	s_lshr_b32 s7, s7, 23
	s_add_i32 s7, s6, s7
	s_ashr_i32 s8, s7, 9
	s_and_b32 s7, s7, 0xfffffe00
	s_sub_i32 s10, s6, s7
	s_ashr_i32 s6, s10, 31
	s_lshr_b32 s6, s6, 27
	s_add_i32 s6, s10, s6
	s_ashr_i32 s11, s6, 5
	s_ashr_i32 s9, s8, 31
	s_lshl_b64 s[6:7], s[8:9], 24
	v_lshl_add_u32 v48, s11, 7, v69
	s_add_u32 s6, s84, s6
	v_ashrrev_i32_e32 v49, 31, v48
	s_addc_u32 s7, s85, s7
	v_lshlrev_b64 v[48:49], 13, v[48:49]
	v_lshl_add_u64 v[48:49], s[6:7], 0, v[48:49]
	s_lshl_b32 s6, s11, 11
	s_lshl_b32 s7, s10, 6
	s_sub_i32 s6, s7, s6
	s_ashr_i32 s7, s6, 31
	v_lshl_add_u64 v[48:49], s[6:7], 2, v[48:49]
	v_mov_b32_e32 v65, 0
	v_lshl_add_u64 v[56:57], v[48:49], 0, v[64:65]
	s_movk_i32 s6, 0x2000
	v_add_co_u32_e32 v58, vcc, s6, v56
	s_nop 1
	v_addc_co_u32_e32 v59, vcc, 0, v57, vcc
	v_add_co_u32_e32 v64, vcc, 0x4000, v56
	global_load_dwordx4 v[48:51], v[56:57], off nt
	global_load_dwordx4 v[52:55], v[58:59], off nt
	v_addc_co_u32_e32 v65, vcc, 0, v57, vcc
	v_add_co_u32_e32 v72, vcc, 0x6000, v56
	s_nop 1
	v_addc_co_u32_e32 v73, vcc, 0, v57, vcc
	global_load_dwordx4 v[56:59], v[64:65], off nt
	global_load_dwordx4 v[60:63], v[72:73], off nt
	s_bitset1_b32 s98, 3
	s_andn2_b64 vcc, exec, s[4:5]
	s_cbranch_vccnz .LBB0_727
	s_branch .LBB0_713

.Lcvw_33:
	s_bitset0_b32 s98, 0
	s_ashr_i32 s4, s76, 31
	s_lshr_b32 s4, s4, 23
	v_mul_f32_e32 v66, 0x42800000, v4
	v_mul_f32_e32 v74, 0x42800000, v8
	v_mov_b32_e32 v77, 0
	s_add_i32 s5, s76, s4
	v_cvt_pk_fp8_f32 v77, v66, v74
	v_mul_f32_e32 v66, 0x42800000, v5
	v_mul_f32_e32 v74, 0x42800000, v9
	v_mov_b32_e32 v78, 0
	s_ashr_i32 s4, s5, 9
	s_and_b32 s5, s5, 0xfffffe00
	v_cvt_pk_fp8_f32 v78, v66, v74
	s_sub_i32 s5, s76, s5
	s_ashr_i32 s28, s5, 31
	s_lshr_b32 s28, s28, 27
	v_mul_f32_e32 v66, 0x42800000, v13
	v_mul_f32_e32 v74, 0x42800000, v17
	s_add_i32 s5, s5, s28
	v_cvt_pk_fp8_f32 v78, v66, v74 op_sel:[0,0,1]
	v_mul_f32_e32 v66, 0x42800000, v6
	v_mul_f32_e32 v74, 0x42800000, v10
	v_mov_b32_e32 v79, 0
	s_ashr_i32 s30, s5, 5
	s_ashr_i32 s5, s4, 31
	v_cvt_pk_fp8_f32 v79, v66, v74
	v_mul_f32_e32 v66, 0x42800000, v7
	v_mul_f32_e32 v74, 0x42800000, v11
	v_mov_b32_e32 v80, 0
	s_lshl_b64 s[28:29], s[4:5], 22
	v_cvt_pk_fp8_f32 v80, v66, v74
	s_add_u32 s28, s38, s28
	s_addc_u32 s29, s39, s29
	s_lshl_b32 s5, s30, 8
	s_lshl_b32 s4, s4, 12
	v_mul_f32_e32 v75, 0x42800000, v12
	v_mul_f32_e32 v76, 0x42800000, v16
	s_add_i32 s5, s5, s4
	v_cvt_pk_fp8_f32 v77, v75, v76 op_sel:[0,0,1]
	v_mul_f32_e32 v75, 0x42800000, v14
	v_mul_f32_e32 v76, 0x42800000, v18
	v_mul_f32_e32 v66, 0x42800000, v15
	v_mul_f32_e32 v74, 0x42800000, v19
	s_sub_i32 s4, s10, s5
	v_cvt_pk_fp8_f32 v79, v75, v76 op_sel:[0,0,1]
	v_cvt_pk_fp8_f32 v80, v66, v74 op_sel:[0,0,1]
	s_and_b32 s4, s4, -16
	s_add_i32 s4, s4, s30
	s_ashr_i32 s5, s4, 31
	ds_write2_b32 v72, v77, v78 offset1:33
	ds_write2_b32 v72, v79, v80 offset0:66 offset1:99
	s_waitcnt lgkmcnt(0)
	s_barrier
	ds_read2_b32 v[74:75], v73 offset1:1
	ds_read2_b32 v[76:77], v73 offset0:2 offset1:3
	s_and_b32 s30, s7, 64
	s_lshl_b64 s[4:5], s[4:5], 14
	s_add_u32 s4, s28, s4
	v_add_lshl_u32 v66, s30, v71, 7
	s_addc_u32 s5, s29, s5
	v_lshl_add_u64 v[78:79], s[4:5], 0, v[66:67]
	s_add_i32 s4, s6, s76
	v_lshl_add_u64 v[78:79], v[78:79], 0, v[64:65]
	s_cmp_ge_i32 s4, s41
	s_waitcnt lgkmcnt(0)
	global_store_dwordx4 v[78:79], v[74:77], off nt
	s_cbranch_scc1 .LBB0_718
	s_ashr_i32 s5, s4, 31
	s_lshr_b32 s5, s5, 23
	s_add_i32 s5, s4, s5
	s_ashr_i32 s28, s5, 9
	s_and_b32 s5, s5, 0xfffffe00
	s_sub_i32 s4, s4, s5
	s_ashr_i32 s5, s4, 31
	s_lshr_b32 s5, s5, 27
	s_add_i32 s4, s4, s5
	s_ashr_i32 s30, s4, 5
	s_ashr_i32 s29, s28, 31
	s_lshl_b64 s[4:5], s[28:29], 24
	v_lshl_add_u32 v4, s30, 7, v69
	s_add_u32 s4, s84, s4
	v_ashrrev_i32_e32 v5, 31, v4
	s_addc_u32 s5, s85, s5
	v_lshlrev_b64 v[4:5], 13, v[4:5]
	v_lshl_add_u64 v[4:5], s[4:5], 0, v[4:5]
	s_lshl_b32 s4, s30, 11
	s_lshl_b32 s5, s28, 15
	s_add_i32 s4, s4, s5
	s_add_i32 s5, s8, s7
	s_sub_i32 s4, s5, s4
	s_ashr_i32 s5, s4, 31
	v_lshl_add_u64 v[4:5], s[4:5], 2, v[4:5]
	v_lshlrev_b32_e32 v66, 2, v68
	v_lshl_add_u64 v[12:13], v[4:5], 0, v[66:67]
	v_add_co_u32_e32 v8, vcc, s25, v12
	s_nop 1
	v_addc_co_u32_e32 v9, vcc, 0, v13, vcc
	v_add_co_u32_e32 v14, vcc, s26, v12
	global_load_dwordx4 v[4:7], v[12:13], off nt
	s_nop 0
	global_load_dwordx4 v[8:11], v[8:9], off nt
	v_addc_co_u32_e32 v15, vcc, 0, v13, vcc
	v_add_co_u32_e32 v16, vcc, s27, v12
	s_nop 1
	v_addc_co_u32_e32 v17, vcc, 0, v13, vcc
	global_load_dwordx4 v[12:15], v[14:15], off nt
	s_nop 0
	global_load_dwordx4 v[16:19], v[16:17], off nt
	s_bitset1_b32 s98, 0
.LBB0_718:
	s_add_i32 s28, s76, s40
	s_cmp_ge_i32 s28, s41
	s_mov_b64 s[4:5], -1
	s_cbranch_scc1 .LBB0_715
	s_waitcnt vmcnt(12)
	s_cmp_eq_u32 s98, 15
	s_cbranch_scc1 .Lcvw_34
	s_waitcnt vmcnt(0)
.Lcvw_34:
	s_bitset0_b32 s98, 1
	s_ashr_i32 s4, s28, 31
	s_lshr_b32 s4, s4, 23
	v_mul_f32_e32 v66, 0x42800000, v0
	v_mul_f32_e32 v74, 0x42800000, v20
	v_mov_b32_e32 v77, v67
	s_add_i32 s5, s28, s4
	v_cvt_pk_fp8_f32 v77, v66, v74
	v_mul_f32_e32 v66, 0x42800000, v1
	v_mul_f32_e32 v74, 0x42800000, v21
	v_mov_b32_e32 v78, v67
	s_ashr_i32 s4, s5, 9
	s_and_b32 s5, s5, 0xfffffe00
	v_cvt_pk_fp8_f32 v78, v66, v74
	s_sub_i32 s5, s28, s5
	s_ashr_i32 s29, s5, 31
	s_lshr_b32 s29, s29, 27
	v_mul_f32_e32 v66, 0x42800000, v25
	v_mul_f32_e32 v74, 0x42800000, v29
	s_add_i32 s5, s5, s29
	v_cvt_pk_fp8_f32 v78, v66, v74 op_sel:[0,0,1]
	v_mul_f32_e32 v66, 0x42800000, v2
	v_mul_f32_e32 v74, 0x42800000, v22
	v_mov_b32_e32 v79, v67
	s_ashr_i32 s29, s5, 5
	s_ashr_i32 s5, s4, 31
	v_cvt_pk_fp8_f32 v79, v66, v74
	v_mul_f32_e32 v66, 0x42800000, v3
	v_mul_f32_e32 v74, 0x42800000, v23
	v_mov_b32_e32 v80, v67
	s_lshl_b64 s[30:31], s[4:5], 22
	v_cvt_pk_fp8_f32 v80, v66, v74
	s_add_u32 s30, s38, s30
	s_addc_u32 s31, s39, s31
	s_lshl_b32 s5, s29, 8
	s_lshl_b32 s4, s4, 12
	v_mul_f32_e32 v75, 0x42800000, v24
	v_mul_f32_e32 v76, 0x42800000, v28
	s_add_i32 s5, s5, s4
	s_add_i32 s4, s9, s10
	v_cvt_pk_fp8_f32 v77, v75, v76 op_sel:[0,0,1]
	v_mul_f32_e32 v75, 0x42800000, v26
	v_mul_f32_e32 v76, 0x42800000, v30
	v_mul_f32_e32 v66, 0x42800000, v27
	v_mul_f32_e32 v74, 0x42800000, v31
	s_sub_i32 s4, s4, s5
	v_cvt_pk_fp8_f32 v79, v75, v76 op_sel:[0,0,1]
	v_cvt_pk_fp8_f32 v80, v66, v74 op_sel:[0,0,1]
	s_and_b32 s4, s4, -16
	s_add_i32 s4, s4, s29
	v_add_u32_e32 v74, 0x2000, v72
	v_add_u32_e32 v75, 0x2200, v73
	s_ashr_i32 s5, s4, 31
	s_add_i32 s29, s12, s7
	ds_write2_b32 v74, v77, v78 offset0:128 offset1:161
	ds_write2_b32 v74, v79, v80 offset0:194 offset1:227
	s_waitcnt lgkmcnt(0)
	s_barrier
	v_add_u32_e32 v76, 0x2208, v73
	ds_read2_b32 v[78:79], v75 offset1:1
	ds_read2_b32 v[80:81], v76 offset1:1
	s_and_b32 s29, s29, 64
	s_lshl_b64 s[4:5], s[4:5], 14
	s_add_u32 s4, s30, s4
	v_add_lshl_u32 v66, s29, v71, 7
	s_addc_u32 s5, s31, s5
	v_lshl_add_u64 v[82:83], s[4:5], 0, v[66:67]
	s_add_i32 s4, s13, s76
	v_lshl_add_u64 v[82:83], v[82:83], 0, v[64:65]
	s_cmp_ge_i32 s4, s41
	s_waitcnt lgkmcnt(0)
	global_store_dwordx4 v[82:83], v[78:81], off nt
	s_cbranch_scc1 .LBB0_721
	s_ashr_i32 s5, s4, 31
	s_lshr_b32 s5, s5, 23
	s_add_i32 s5, s4, s5
	s_ashr_i32 s30, s5, 9
	s_and_b32 s5, s5, 0xfffffe00
	s_sub_i32 s4, s4, s5
	s_ashr_i32 s5, s4, 31
	s_lshr_b32 s5, s5, 27
	s_add_i32 s4, s4, s5
	s_ashr_i32 s29, s4, 5
	s_ashr_i32 s31, s30, 31
	s_lshl_b64 s[4:5], s[30:31], 24
	v_lshl_add_u32 v0, s29, 7, v69
	s_add_u32 s4, s84, s4
	v_ashrrev_i32_e32 v1, 31, v0
	s_addc_u32 s5, s85, s5
	v_lshlrev_b64 v[0:1], 13, v[0:1]
	v_lshl_add_u64 v[0:1], s[4:5], 0, v[0:1]
	s_lshl_b32 s4, s29, 11
	s_lshl_b32 s5, s30, 15
	s_add_i32 s4, s4, s5
	s_add_i32 s5, s14, s7
	s_sub_i32 s4, s5, s4
	s_ashr_i32 s5, s4, 31
	v_lshl_add_u64 v[0:1], s[4:5], 2, v[0:1]
	v_lshlrev_b32_e32 v66, 2, v68
	v_lshl_add_u64 v[24:25], v[0:1], 0, v[66:67]
	v_add_co_u32_e32 v20, vcc, s25, v24
	s_nop 1
	v_addc_co_u32_e32 v21, vcc, 0, v25, vcc
	v_add_co_u32_e32 v26, vcc, s26, v24
	global_load_dwordx4 v[0:3], v[24:25], off nt
	s_nop 0
	global_load_dwordx4 v[20:23], v[20:21], off nt
	v_addc_co_u32_e32 v27, vcc, 0, v25, vcc
	v_add_co_u32_e32 v28, vcc, s27, v24
	s_nop 1
	v_addc_co_u32_e32 v29, vcc, 0, v25, vcc
	global_load_dwordx4 v[24:27], v[26:27], off nt
	s_nop 0
	global_load_dwordx4 v[28:31], v[28:29], off nt
	s_bitset1_b32 s98, 1
.LBB0_721:
	s_add_i32 s29, s15, s76
	s_cmp_ge_i32 s29, s41
	s_mov_b64 s[4:5], -1
	s_cbranch_scc1 .LBB0_715
	s_waitcnt vmcnt(12)
	s_cmp_eq_u32 s98, 15
	s_cbranch_scc1 .Lcvw_35
	s_waitcnt vmcnt(0)
.Lcvw_35:
	s_bitset0_b32 s98, 2
	s_ashr_i32 s4, s29, 31
	s_lshr_b32 s4, s4, 23
	v_mul_f32_e32 v66, 0x42800000, v32
	v_mul_f32_e32 v77, 0x42800000, v36
	v_mov_b32_e32 v80, v67
	s_add_i32 s5, s29, s4
	v_cvt_pk_fp8_f32 v80, v66, v77
	v_mul_f32_e32 v66, 0x42800000, v33
	v_mul_f32_e32 v77, 0x42800000, v37
	v_mov_b32_e32 v81, v67
	s_ashr_i32 s4, s5, 9
	s_and_b32 s5, s5, 0xfffffe00
	v_cvt_pk_fp8_f32 v81, v66, v77
	s_sub_i32 s5, s29, s5
	s_ashr_i32 s29, s5, 31
	s_lshr_b32 s29, s29, 27
	v_mul_f32_e32 v66, 0x42800000, v41
	v_mul_f32_e32 v77, 0x42800000, v45
	s_add_i32 s5, s5, s29
	v_cvt_pk_fp8_f32 v81, v66, v77 op_sel:[0,0,1]
	v_mul_f32_e32 v66, 0x42800000, v34
	v_mul_f32_e32 v77, 0x42800000, v38
	v_mov_b32_e32 v82, v67
	s_ashr_i32 s29, s5, 5
	s_ashr_i32 s5, s4, 31
	v_cvt_pk_fp8_f32 v82, v66, v77
	v_mul_f32_e32 v66, 0x42800000, v35
	v_mul_f32_e32 v77, 0x42800000, v39
	v_mov_b32_e32 v83, v67
	s_lshl_b64 s[30:31], s[4:5], 22
	v_cvt_pk_fp8_f32 v83, v66, v77
	s_add_u32 s30, s38, s30
	s_addc_u32 s31, s39, s31
	s_lshl_b32 s5, s29, 8
	s_lshl_b32 s4, s4, 12
	v_mul_f32_e32 v78, 0x42800000, v40
	v_mul_f32_e32 v79, 0x42800000, v44
	s_add_i32 s5, s5, s4
	s_add_i32 s4, s16, s10
	v_cvt_pk_fp8_f32 v80, v78, v79 op_sel:[0,0,1]
	v_mul_f32_e32 v78, 0x42800000, v42
	v_mul_f32_e32 v79, 0x42800000, v46
	v_mul_f32_e32 v66, 0x42800000, v43
	v_mul_f32_e32 v77, 0x42800000, v47
	s_sub_i32 s4, s4, s5
	v_cvt_pk_fp8_f32 v82, v78, v79 op_sel:[0,0,1]
	v_cvt_pk_fp8_f32 v83, v66, v77 op_sel:[0,0,1]
	s_and_b32 s4, s4, -16
	s_add_i32 s4, s4, s29
	s_ashr_i32 s5, s4, 31
	s_add_i32 s29, s17, s7
	ds_write2_b32 v72, v80, v81 offset1:33
	ds_write2_b32 v72, v82, v83 offset0:66 offset1:99
	s_waitcnt lgkmcnt(0)
	s_barrier
	ds_read2_b32 v[78:79], v73 offset1:1
	ds_read2_b32 v[80:81], v73 offset0:2 offset1:3
	s_and_b32 s29, s29, 64
	s_lshl_b64 s[4:5], s[4:5], 14
	s_add_u32 s4, s30, s4
	v_add_lshl_u32 v66, s29, v71, 7
	s_addc_u32 s5, s31, s5
	v_lshl_add_u64 v[82:83], s[4:5], 0, v[66:67]
	s_add_i32 s4, s18, s76
	v_lshl_add_u64 v[82:83], v[82:83], 0, v[64:65]
	s_cmp_ge_i32 s4, s41
	s_waitcnt lgkmcnt(0)
	global_store_dwordx4 v[82:83], v[78:81], off nt
	s_cbranch_scc1 .LBB0_724
	s_ashr_i32 s5, s4, 31
	s_lshr_b32 s5, s5, 23
	s_add_i32 s5, s4, s5
	s_ashr_i32 s30, s5, 9
	s_and_b32 s5, s5, 0xfffffe00
	s_sub_i32 s4, s4, s5
	s_ashr_i32 s5, s4, 31
	s_lshr_b32 s5, s5, 27
	s_add_i32 s4, s4, s5
	s_ashr_i32 s29, s4, 5
	s_ashr_i32 s31, s30, 31
	s_lshl_b64 s[4:5], s[30:31], 24
	v_lshl_add_u32 v32, s29, 7, v69
	s_add_u32 s4, s84, s4
	v_ashrrev_i32_e32 v33, 31, v32
	s_addc_u32 s5, s85, s5
	v_lshlrev_b64 v[32:33], 13, v[32:33]
	v_lshl_add_u64 v[32:33], s[4:5], 0, v[32:33]
	s_lshl_b32 s4, s29, 11
	s_lshl_b32 s5, s30, 15
	s_add_i32 s4, s4, s5
	s_add_i32 s5, s19, s7
	s_sub_i32 s4, s5, s4
	s_ashr_i32 s5, s4, 31
	v_lshl_add_u64 v[32:33], s[4:5], 2, v[32:33]
	v_lshlrev_b32_e32 v66, 2, v68
	v_lshl_add_u64 v[40:41], v[32:33], 0, v[66:67]
	v_add_co_u32_e32 v36, vcc, 0x2000, v40
	s_nop 1
	v_addc_co_u32_e32 v37, vcc, 0, v41, vcc
	v_add_co_u32_e32 v42, vcc, 0x4000, v40
	global_load_dwordx4 v[32:35], v[40:41], off nt
	s_nop 0
	global_load_dwordx4 v[36:39], v[36:37], off nt
	v_addc_co_u32_e32 v43, vcc, 0, v41, vcc
	v_add_co_u32_e32 v44, vcc, 0x6000, v40
	s_nop 1
	v_addc_co_u32_e32 v45, vcc, 0, v41, vcc
	global_load_dwordx4 v[40:43], v[42:43], off nt
	s_nop 0
	global_load_dwordx4 v[44:47], v[44:45], off nt
	s_bitset1_b32 s98, 2
.LBB0_724:
	s_add_i32 s29, s20, s76
	s_cmp_ge_i32 s29, s41
	s_mov_b64 s[4:5], -1
	s_cbranch_scc1 .LBB0_715
	s_waitcnt vmcnt(12)
	s_cmp_eq_u32 s98, 15
	s_cbranch_scc1 .Lcvw_36
	s_waitcnt vmcnt(0)
.Lcvw_36:
	s_bitset0_b32 s98, 3
	s_ashr_i32 s4, s29, 31
	s_lshr_b32 s4, s4, 23
	v_mul_f32_e32 v66, 0x42800000, v48
	v_mul_f32_e32 v77, 0x42800000, v52
	v_mov_b32_e32 v80, v67
	s_add_i32 s5, s29, s4
	v_cvt_pk_fp8_f32 v80, v66, v77
	v_mul_f32_e32 v66, 0x42800000, v49
	v_mul_f32_e32 v77, 0x42800000, v53
	v_mov_b32_e32 v81, v67
	s_ashr_i32 s4, s5, 9
	s_and_b32 s5, s5, 0xfffffe00
	v_cvt_pk_fp8_f32 v81, v66, v77
	s_sub_i32 s5, s29, s5
	s_ashr_i32 s29, s5, 31
	s_lshr_b32 s29, s29, 27
	v_mul_f32_e32 v66, 0x42800000, v57
	v_mul_f32_e32 v77, 0x42800000, v61
	s_add_i32 s5, s5, s29
	v_cvt_pk_fp8_f32 v81, v66, v77 op_sel:[0,0,1]
	v_mul_f32_e32 v66, 0x42800000, v50
	v_mul_f32_e32 v77, 0x42800000, v54
	v_mov_b32_e32 v82, v67
	s_ashr_i32 s29, s5, 5
	s_ashr_i32 s5, s4, 31
	v_cvt_pk_fp8_f32 v82, v66, v77
	v_mul_f32_e32 v66, 0x42800000, v51
	v_mul_f32_e32 v77, 0x42800000, v55
	v_mov_b32_e32 v83, v67
	s_lshl_b64 s[30:31], s[4:5], 22
	v_cvt_pk_fp8_f32 v83, v66, v77
	s_add_u32 s30, s38, s30
	s_addc_u32 s31, s39, s31
	s_lshl_b32 s5, s29, 8
	s_lshl_b32 s4, s4, 12
	v_mul_f32_e32 v78, 0x42800000, v56
	v_mul_f32_e32 v79, 0x42800000, v60
	s_add_i32 s5, s5, s4
	s_add_i32 s4, s21, s10
	v_cvt_pk_fp8_f32 v80, v78, v79 op_sel:[0,0,1]
	v_mul_f32_e32 v78, 0x42800000, v58
	v_mul_f32_e32 v79, 0x42800000, v62
	v_mul_f32_e32 v66, 0x42800000, v59
	v_mul_f32_e32 v77, 0x42800000, v63
	s_sub_i32 s4, s4, s5
	v_cvt_pk_fp8_f32 v82, v78, v79 op_sel:[0,0,1]
	v_cvt_pk_fp8_f32 v83, v66, v77 op_sel:[0,0,1]
	s_and_b32 s4, s4, -16
	s_add_i32 s4, s4, s29
	s_ashr_i32 s5, s4, 31
	s_add_i32 s29, s22, s7
	ds_write2_b32 v74, v80, v81 offset0:128 offset1:161
	ds_write2_b32 v74, v82, v83 offset0:194 offset1:227
	s_waitcnt lgkmcnt(0)
	s_barrier
	ds_read2_b32 v[74:75], v75 offset1:1
	ds_read2_b32 v[76:77], v76 offset1:1
	s_and_b32 s29, s29, 64
	s_lshl_b64 s[4:5], s[4:5], 14
	s_add_u32 s4, s30, s4
	v_add_lshl_u32 v66, s29, v71, 7
	s_addc_u32 s5, s31, s5
	v_lshl_add_u64 v[78:79], s[4:5], 0, v[66:67]
	s_add_i32 s4, s23, s76
	v_lshl_add_u64 v[78:79], v[78:79], 0, v[64:65]
	s_cmp_ge_i32 s4, s41
	s_waitcnt lgkmcnt(0)
	global_store_dwordx4 v[78:79], v[74:77], off nt
	s_cbranch_scc1 .LBB0_714
	s_ashr_i32 s5, s4, 31
	s_lshr_b32 s5, s5, 23
	s_add_i32 s5, s4, s5
	s_ashr_i32 s30, s5, 9
	s_and_b32 s5, s5, 0xfffffe00
	s_sub_i32 s4, s4, s5
	s_ashr_i32 s5, s4, 31
	s_lshr_b32 s5, s5, 27
	s_add_i32 s4, s4, s5
	s_ashr_i32 s29, s4, 5
	s_ashr_i32 s31, s30, 31
	s_lshl_b64 s[4:5], s[30:31], 24
	v_lshl_add_u32 v48, s29, 7, v69
	s_add_u32 s4, s84, s4
	v_ashrrev_i32_e32 v49, 31, v48
	s_addc_u32 s5, s85, s5
	v_lshlrev_b64 v[48:49], 13, v[48:49]
	v_lshl_add_u64 v[48:49], s[4:5], 0, v[48:49]
	s_lshl_b32 s4, s29, 11
	s_lshl_b32 s5, s30, 15
	s_add_i32 s4, s4, s5
	s_add_i32 s5, s24, s7
	s_sub_i32 s4, s5, s4
	s_ashr_i32 s5, s4, 31
	v_lshl_add_u64 v[48:49], s[4:5], 2, v[48:49]
	v_lshlrev_b32_e32 v66, 2, v68
	v_lshl_add_u64 v[56:57], v[48:49], 0, v[66:67]
	v_add_co_u32_e32 v52, vcc, 0x2000, v56
	s_nop 1
	v_addc_co_u32_e32 v53, vcc, 0, v57, vcc
	v_add_co_u32_e32 v58, vcc, 0x4000, v56
	global_load_dwordx4 v[48:51], v[56:57], off nt
	s_nop 0
	global_load_dwordx4 v[52:55], v[52:53], off nt
	v_addc_co_u32_e32 v59, vcc, 0, v57, vcc
	v_add_co_u32_e32 v60, vcc, 0x6000, v56
	s_nop 1
	v_addc_co_u32_e32 v61, vcc, 0, v57, vcc
	global_load_dwordx4 v[56:59], v[58:59], off nt
	s_nop 0
	global_load_dwordx4 v[60:63], v[60:61], off nt
	s_bitset1_b32 s98, 3
	s_branch .LBB0_714

.LBB0_848:
	s_cmp_lt_i32 s20, s12
	s_cselect_b32 s6, 4, 2
	s_and_b64 s[4:5], s[4:5], exec
	s_cselect_b32 s4, 8, s6
	s_ashr_i32 s5, s8, 31
	s_lshr_b32 s5, s5, 23
	s_add_i32 s5, s8, s5
	s_ashr_i32 s6, s5, 9
	s_and_b32 s5, s5, 0xfffffe00
	s_sub_i32 s5, s8, s5
	s_ashr_i32 s7, s5, 31
	s_lshr_b32 s7, s7, 27
	s_add_i32 s7, s5, s7
	s_ashr_i32 s20, s7, 5
	s_ashr_i32 s7, s6, 31
	s_lshl_b64 s[6:7], s[6:7], 24
	v_lshl_add_u32 v0, s20, 7, v70
	s_add_u32 s6, s84, s6
	v_ashrrev_i32_e32 v1, 31, v0
	s_addc_u32 s7, s85, s7
	v_lshlrev_b64 v[0:1], 13, v[0:1]
	v_lshl_add_u64 v[0:1], s[6:7], 0, v[0:1]
	s_lshl_b32 s6, s20, 11
	s_lshl_b32 s5, s5, 6
	s_sub_i32 s6, s5, s6
	s_ashr_i32 s7, s6, 31
	v_lshl_add_u64 v[0:1], s[6:7], 2, v[0:1]
	v_mov_b32_e32 v69, v65
	s_waitcnt vmcnt(1)
	v_lshl_add_u64 v[8:9], v[0:1], 0, v[68:69]
	v_add_co_u32_e32 v10, vcc, s17, v8
	s_nop 1
	v_addc_co_u32_e32 v11, vcc, 0, v9, vcc
	s_waitcnt vmcnt(0)
	v_add_co_u32_e32 v16, vcc, 0x4000, v8
	s_mov_b32 s98, 0
	s_barrier
	s_nop 0
	v_addc_co_u32_e32 v17, vcc, 0, v9, vcc
	v_add_co_u32_e32 v18, vcc, 0x6000, v8
	global_load_dwordx4 v[0:3], v[8:9], off nt
	global_load_dwordx4 v[4:7], v[10:11], off nt
	v_addc_co_u32_e32 v19, vcc, 0, v9, vcc
	global_load_dwordx4 v[8:11], v[16:17], off nt
	global_load_dwordx4 v[12:15], v[18:19], off nt
	s_bitset1_b32 s98, 0
	s_add_i32 s5, s8, 1
	v_mov_b32_e32 v16, 0
	s_cmp_le_i32 s37, s5
	v_mov_b32_e32 v17, v16
	v_mov_b32_e32 v18, v16
	v_mov_b32_e32 v19, v16
	v_mov_b32_e32 v20, v16
	v_mov_b32_e32 v21, v16
	v_mov_b32_e32 v22, v16
	v_mov_b32_e32 v23, v16
	v_mov_b32_e32 v24, v16
	v_mov_b32_e32 v25, v16
	v_mov_b32_e32 v26, v16
	v_mov_b32_e32 v27, v16
	v_mov_b32_e32 v28, v16
	v_mov_b32_e32 v29, v16
	v_mov_b32_e32 v30, v16
	v_mov_b32_e32 v31, v16
	s_cbranch_scc1 .LBB0_850
	s_ashr_i32 s6, s5, 31
	s_lshr_b32 s6, s6, 23
	s_add_i32 s7, s5, s6
	s_ashr_i32 s6, s7, 9
	s_and_b32 s7, s7, 0xfffffe00
	s_sub_i32 s5, s5, s7
	s_ashr_i32 s7, s5, 31
	s_lshr_b32 s7, s7, 27
	s_add_i32 s7, s5, s7
	s_ashr_i32 s20, s7, 5
	s_ashr_i32 s7, s6, 31
	s_lshl_b64 s[6:7], s[6:7], 24
	v_lshl_add_u32 v16, s20, 7, v70
	s_add_u32 s6, s84, s6
	v_ashrrev_i32_e32 v17, 31, v16
	s_addc_u32 s7, s85, s7
	v_lshlrev_b64 v[16:17], 13, v[16:17]
	v_lshl_add_u64 v[16:17], s[6:7], 0, v[16:17]
	s_lshl_b32 s6, s20, 11
	s_lshl_b32 s5, s5, 6
	s_sub_i32 s6, s5, s6
	s_ashr_i32 s7, s6, 31
	v_lshl_add_u64 v[16:17], s[6:7], 2, v[16:17]
	v_lshl_add_u64 v[24:25], v[16:17], 0, v[68:69]
	v_add_co_u32_e32 v26, vcc, s17, v24
	s_nop 1
	v_addc_co_u32_e32 v27, vcc, 0, v25, vcc
	v_add_co_u32_e32 v32, vcc, s18, v24
	global_load_dwordx4 v[16:19], v[24:25], off nt
	global_load_dwordx4 v[20:23], v[26:27], off nt
	v_addc_co_u32_e32 v33, vcc, 0, v25, vcc
	v_add_co_u32_e32 v34, vcc, s19, v24
	s_nop 1
	v_addc_co_u32_e32 v35, vcc, 0, v25, vcc
	global_load_dwordx4 v[24:27], v[32:33], off nt
	global_load_dwordx4 v[28:31], v[34:35], off nt
	s_bitset1_b32 s98, 1
.LBB0_850:
	s_add_i32 s4, s8, s4
	s_min_i32 s6, s4, s37
	s_add_i32 s4, s8, 2
	s_cmp_ge_i32 s4, s6
	s_cbranch_scc1 .LBB0_852
	s_ashr_i32 s5, s4, 31
	s_lshr_b32 s5, s5, 23
	s_add_i32 s5, s4, s5
	s_ashr_i32 s20, s5, 9
	s_and_b32 s5, s5, 0xfffffe00
	s_sub_i32 s7, s4, s5
	s_ashr_i32 s4, s7, 31
	s_lshr_b32 s4, s4, 27
	s_add_i32 s4, s7, s4
	s_ashr_i32 s22, s4, 5
	s_ashr_i32 s21, s20, 31
	s_lshl_b64 s[4:5], s[20:21], 24
	v_lshl_add_u32 v32, s22, 7, v70
	s_add_u32 s4, s84, s4
	v_ashrrev_i32_e32 v33, 31, v32
	s_addc_u32 s5, s85, s5
	v_lshlrev_b64 v[32:33], 13, v[32:33]
	v_lshl_add_u64 v[32:33], s[4:5], 0, v[32:33]
	s_lshl_b32 s4, s22, 11
	s_lshl_b32 s5, s7, 6
	s_sub_i32 s4, s5, s4
	s_ashr_i32 s5, s4, 31
	v_lshl_add_u64 v[32:33], s[4:5], 2, v[32:33]
	v_mov_b32_e32 v69, v65
	v_lshl_add_u64 v[40:41], v[32:33], 0, v[68:69]
	v_add_co_u32_e32 v42, vcc, 0x2000, v40
	s_nop 1
	v_addc_co_u32_e32 v43, vcc, 0, v41, vcc
	v_add_co_u32_e32 v48, vcc, 0x4000, v40
	global_load_dwordx4 v[32:35], v[40:41], off nt
	global_load_dwordx4 v[36:39], v[42:43], off nt
	v_addc_co_u32_e32 v49, vcc, 0, v41, vcc
	v_add_co_u32_e32 v50, vcc, 0x6000, v40
	s_nop 1
	v_addc_co_u32_e32 v51, vcc, 0, v41, vcc
	global_load_dwordx4 v[40:43], v[48:49], off nt
	global_load_dwordx4 v[44:47], v[50:51], off nt
	s_bitset1_b32 s98, 2
.LBB0_852:
	s_add_i32 s4, s8, 3
	s_cmp_ge_i32 s4, s6
	s_cbranch_scc1 .LBB0_854
	s_ashr_i32 s5, s4, 31
	s_lshr_b32 s5, s5, 23
	s_add_i32 s5, s4, s5
	s_ashr_i32 s20, s5, 9
	s_and_b32 s5, s5, 0xfffffe00
	s_sub_i32 s7, s4, s5
	s_ashr_i32 s4, s7, 31
	s_lshr_b32 s4, s4, 27
	s_add_i32 s4, s7, s4
	s_ashr_i32 s8, s4, 5
	s_ashr_i32 s21, s20, 31
	s_lshl_b64 s[4:5], s[20:21], 24
	v_lshl_add_u32 v48, s8, 7, v70
	s_add_u32 s4, s84, s4
	v_ashrrev_i32_e32 v49, 31, v48
	s_addc_u32 s5, s85, s5
	v_lshlrev_b64 v[48:49], 13, v[48:49]
	v_lshl_add_u64 v[48:49], s[4:5], 0, v[48:49]
	s_lshl_b32 s4, s8, 11
	s_lshl_b32 s5, s7, 6
	s_sub_i32 s4, s5, s4
	s_ashr_i32 s5, s4, 31
	v_lshl_add_u64 v[48:49], s[4:5], 2, v[48:49]
	v_mov_b32_e32 v69, v65
	v_lshl_add_u64 v[56:57], v[48:49], 0, v[68:69]
	v_add_co_u32_e32 v58, vcc, 0x2000, v56
	s_nop 1
	v_addc_co_u32_e32 v59, vcc, 0, v57, vcc
	v_add_co_u32_e32 v74, vcc, 0x4000, v56
	global_load_dwordx4 v[48:51], v[56:57], off nt
	global_load_dwordx4 v[52:55], v[58:59], off nt
	v_addc_co_u32_e32 v75, vcc, 0, v57, vcc
	v_add_co_u32_e32 v76, vcc, 0x6000, v56
	s_nop 1
	v_addc_co_u32_e32 v77, vcc, 0, v57, vcc
	global_load_dwordx4 v[56:59], v[74:75], off nt
	global_load_dwordx4 v[60:63], v[76:77], off nt
	s_bitset1_b32 s98, 3

.Lcvw_37:
	s_bitset0_b32 s98, 0
	s_add_i32 s4, s8, -7
	s_ashr_i32 s5, s4, 31
	s_lshr_b32 s5, s5, 23
	s_add_i32 s5, s4, s5
	v_mul_f32_e32 v64, 0x42800000, v0
	v_mul_f32_e32 v69, 0x42800000, v4
	v_mov_b32_e32 v76, v65
	s_ashr_i32 s4, s5, 9
	s_and_b32 s5, s5, 0xfffffe00
	v_cvt_pk_fp8_f32 v76, v64, v69
	v_mul_f32_e32 v64, 0x42800000, v1
	v_mul_f32_e32 v69, 0x42800000, v5
	v_mov_b32_e32 v77, v65
	s_sub_i32 s5, s8, s5
	v_cvt_pk_fp8_f32 v77, v64, v69
	s_add_i32 s5, s5, -7
	s_ashr_i32 s20, s5, 31
	s_lshr_b32 s20, s20, 27
	v_mul_f32_e32 v64, 0x42800000, v9
	v_mul_f32_e32 v69, 0x42800000, v13
	s_add_i32 s5, s5, s20
	v_cvt_pk_fp8_f32 v77, v64, v69 op_sel:[0,0,1]
	v_mul_f32_e32 v64, 0x42800000, v2
	v_mul_f32_e32 v69, 0x42800000, v6
	v_mov_b32_e32 v78, v65
	s_ashr_i32 s22, s5, 5
	s_ashr_i32 s5, s4, 31
	v_cvt_pk_fp8_f32 v78, v64, v69
	v_mul_f32_e32 v64, 0x42800000, v3
	v_mul_f32_e32 v69, 0x42800000, v7
	v_mov_b32_e32 v79, v65
	s_lshl_b64 s[20:21], s[4:5], 22
	v_cvt_pk_fp8_f32 v79, v64, v69
	s_add_u32 s20, s38, s20
	s_addc_u32 s21, s39, s21
	s_lshl_b32 s5, s22, 8
	s_lshl_b32 s4, s4, 12
	v_mul_f32_e32 v74, 0x42800000, v8
	v_mul_f32_e32 v75, 0x42800000, v12
	s_add_i32 s5, s5, s4
	v_cvt_pk_fp8_f32 v76, v74, v75 op_sel:[0,0,1]
	v_mul_f32_e32 v74, 0x42800000, v10
	v_mul_f32_e32 v75, 0x42800000, v14
	v_mul_f32_e32 v64, 0x42800000, v11
	v_mul_f32_e32 v69, 0x42800000, v15
	s_sub_i32 s4, s9, s5
	v_cvt_pk_fp8_f32 v78, v74, v75 op_sel:[0,0,1]
	v_cvt_pk_fp8_f32 v79, v64, v69 op_sel:[0,0,1]
	s_and_b32 s4, s4, -16
	s_add_i32 s4, s4, s22
	v_add_u32_e32 v74, v72, v66
	s_ashr_i32 s5, s4, 31
	ds_write2_b32 v73, v76, v77 offset1:33
	ds_write2_b32 v73, v78, v79 offset0:66 offset1:99
	s_waitcnt lgkmcnt(0)
	s_barrier
	ds_read2_b32 v[76:77], v74 offset1:1
	ds_read2_b32 v[78:79], v74 offset0:2 offset1:3
	s_and_b32 s22, s7, 64
	s_lshl_b64 s[4:5], s[4:5], 14
	s_add_u32 s4, s20, s4
	v_add_lshl_u32 v64, s22, v198, 7
	s_addc_u32 s5, s21, s5
	v_lshl_add_u64 v[80:81], s[4:5], 0, v[64:65]
	s_add_i32 s20, s8, -3
	v_lshl_add_u64 v[80:81], v[80:81], 0, v[66:67]
	s_cmp_ge_i32 s20, s6
	s_waitcnt lgkmcnt(0)
	global_store_dwordx4 v[80:81], v[76:79], off nt
	s_cbranch_scc1 .LBB0_859
	s_ashr_i32 s4, s20, 31
	s_lshr_b32 s4, s4, 23
	s_add_i32 s5, s20, s4
	s_ashr_i32 s4, s5, 9
	s_and_b32 s5, s5, 0xfffffe00
	s_sub_i32 s5, s8, s5
	s_add_i32 s5, s5, -3
	s_ashr_i32 s21, s5, 31
	s_lshr_b32 s21, s21, 27
	s_add_i32 s5, s5, s21
	s_ashr_i32 s21, s5, 5
	s_ashr_i32 s5, s4, 31
	s_lshl_b64 s[22:23], s[4:5], 24
	s_add_u32 s22, s84, s22
	s_addc_u32 s23, s85, s23
	s_lshl_b32 s5, s21, 11
	s_lshl_b32 s4, s4, 15
	v_lshl_add_u32 v0, s21, 7, v70
	s_add_i32 s5, s5, s4
	v_ashrrev_i32_e32 v1, 31, v0
	s_sub_i32 s4, s7, s5
	v_lshlrev_b64 v[0:1], 13, v[0:1]
	s_addk_i32 s4, 0x100
	v_lshl_add_u64 v[0:1], s[22:23], 0, v[0:1]
	s_ashr_i32 s5, s4, 31
	v_lshl_add_u64 v[0:1], s[4:5], 2, v[0:1]
	v_mov_b32_e32 v69, v65
	v_lshl_add_u64 v[8:9], v[0:1], 0, v[68:69]
	v_add_co_u32_e32 v10, vcc, s17, v8
	s_nop 1
	v_addc_co_u32_e32 v11, vcc, 0, v9, vcc
	v_add_co_u32_e32 v76, vcc, s18, v8
	global_load_dwordx4 v[0:3], v[8:9], off nt
	global_load_dwordx4 v[4:7], v[10:11], off nt
	v_addc_co_u32_e32 v77, vcc, 0, v9, vcc
	v_add_co_u32_e32 v78, vcc, s19, v8
	s_nop 1
	v_addc_co_u32_e32 v79, vcc, 0, v9, vcc
	global_load_dwordx4 v[8:11], v[76:77], off nt
	global_load_dwordx4 v[12:15], v[78:79], off nt
	s_bitset1_b32 s98, 0
.LBB0_859:
	s_add_i32 s21, s8, -6
	s_cmp_ge_i32 s21, s6
	s_mov_b64 s[4:5], -1
	s_cbranch_scc1 .LBB0_856
	s_waitcnt vmcnt(12)
	s_cmp_eq_u32 s98, 15
	s_cbranch_scc1 .Lcvw_38
	s_waitcnt vmcnt(0)
.Lcvw_38:
	s_bitset0_b32 s98, 1
	s_ashr_i32 s4, s21, 31
	s_lshr_b32 s4, s4, 23
	s_add_i32 s21, s21, s4
	s_and_b32 s5, s21, 0xfffffe00
	v_mul_f32_e32 v69, 0x42800000, v16
	v_mul_f32_e32 v75, 0x42800000, v20
	v_mov_b32_e32 v78, v65
	s_sub_i32 s5, s8, s5
	v_cvt_pk_fp8_f32 v78, v69, v75
	v_mul_f32_e32 v69, 0x42800000, v17
	v_mul_f32_e32 v75, 0x42800000, v21
	v_mov_b32_e32 v79, v65
	s_add_i32 s5, s5, -6
	v_cvt_pk_fp8_f32 v79, v69, v75
	s_ashr_i32 s4, s21, 9
	s_ashr_i32 s21, s5, 31
	s_lshr_b32 s21, s21, 27
	s_add_i32 s5, s5, s21
	v_mul_f32_e32 v69, 0x42800000, v25
	v_mul_f32_e32 v75, 0x42800000, v29
	s_ashr_i32 s21, s5, 5
	s_ashr_i32 s5, s4, 31
	v_cvt_pk_fp8_f32 v79, v69, v75 op_sel:[0,0,1]
	v_mul_f32_e32 v69, 0x42800000, v18
	v_mul_f32_e32 v75, 0x42800000, v22
	v_mov_b32_e32 v80, v65
	s_lshl_b64 s[22:23], s[4:5], 22
	v_cvt_pk_fp8_f32 v80, v69, v75
	v_mul_f32_e32 v69, 0x42800000, v19
	v_mul_f32_e32 v75, 0x42800000, v23
	v_mov_b32_e32 v81, v65
	s_add_u32 s22, s38, s22
	v_cvt_pk_fp8_f32 v81, v69, v75
	s_addc_u32 s23, s39, s23
	s_lshl_b32 s5, s21, 8
	s_lshl_b32 s4, s4, 12
	s_add_i32 s5, s5, s4
	v_mul_f32_e32 v76, 0x42800000, v24
	v_mul_f32_e32 v77, 0x42800000, v28
	s_sub_i32 s4, s9, s5
	v_cvt_pk_fp8_f32 v78, v76, v77 op_sel:[0,0,1]
	v_mul_f32_e32 v76, 0x42800000, v26
	v_mul_f32_e32 v77, 0x42800000, v30
	v_mul_f32_e32 v69, 0x42800000, v27
	v_mul_f32_e32 v75, 0x42800000, v31
	s_add_i32 s4, s4, 8
	v_cvt_pk_fp8_f32 v80, v76, v77 op_sel:[0,0,1]
	v_cvt_pk_fp8_f32 v81, v69, v75 op_sel:[0,0,1]
	s_and_b32 s4, s4, -16
	s_add_i32 s4, s4, s21
	v_add_u32_e32 v75, 0x2000, v73
	v_add_u32_e32 v76, 0x2200, v74
	s_ashr_i32 s5, s4, 31
	s_add_i32 s21, s7, 64
	ds_write2_b32 v75, v78, v79 offset0:128 offset1:161
	ds_write2_b32 v75, v80, v81 offset0:194 offset1:227
	s_waitcnt lgkmcnt(0)
	s_barrier
	v_add_u32_e32 v77, 0x2208, v74
	ds_read2_b32 v[78:79], v76 offset1:1
	ds_read2_b32 v[80:81], v77 offset1:1
	s_and_b32 s21, s21, 64
	s_lshl_b64 s[4:5], s[4:5], 14
	s_add_u32 s4, s22, s4
	v_add_lshl_u32 v82, s21, v198, 7
	v_mov_b32_e32 v83, v65
	s_addc_u32 s5, s23, s5
	v_lshl_add_u64 v[82:83], s[4:5], 0, v[82:83]
	s_add_i32 s4, s8, -2
	v_lshl_add_u64 v[82:83], v[82:83], 0, v[66:67]
	s_cmp_ge_i32 s4, s6
	s_waitcnt lgkmcnt(0)
	global_store_dwordx4 v[82:83], v[78:81], off nt
	s_cbranch_scc1 .LBB0_862
	s_ashr_i32 s5, s4, 31
	s_lshr_b32 s5, s5, 23
	s_add_i32 s5, s4, s5
	s_ashr_i32 s4, s5, 9
	s_and_b32 s5, s5, 0xfffffe00
	s_sub_i32 s5, s8, s5
	s_add_i32 s5, s5, -2
	s_ashr_i32 s21, s5, 31
	s_lshr_b32 s21, s21, 27
	s_add_i32 s5, s5, s21
	s_ashr_i32 s21, s5, 5
	s_ashr_i32 s5, s4, 31
	s_lshl_b64 s[22:23], s[4:5], 24
	s_add_u32 s22, s84, s22
	s_addc_u32 s23, s85, s23
	s_lshl_b32 s5, s21, 11
	s_lshl_b32 s4, s4, 15
	v_lshl_add_u32 v16, s21, 7, v70
	s_add_i32 s5, s5, s4
	v_ashrrev_i32_e32 v17, 31, v16
	s_sub_i32 s4, s7, s5
	v_lshlrev_b64 v[16:17], 13, v[16:17]
	s_addk_i32 s4, 0x140
	v_lshl_add_u64 v[16:17], s[22:23], 0, v[16:17]
	s_ashr_i32 s5, s4, 31
	v_lshl_add_u64 v[16:17], s[4:5], 2, v[16:17]
	v_mov_b32_e32 v69, v65
	v_lshl_add_u64 v[24:25], v[16:17], 0, v[68:69]
	v_add_co_u32_e32 v26, vcc, s17, v24
	s_nop 1
	v_addc_co_u32_e32 v27, vcc, 0, v25, vcc
	v_add_co_u32_e32 v78, vcc, s18, v24
	global_load_dwordx4 v[16:19], v[24:25], off nt
	global_load_dwordx4 v[20:23], v[26:27], off nt
	v_addc_co_u32_e32 v79, vcc, 0, v25, vcc
	v_add_co_u32_e32 v80, vcc, s19, v24
	s_nop 1
	v_addc_co_u32_e32 v81, vcc, 0, v25, vcc
	global_load_dwordx4 v[24:27], v[78:79], off nt
	global_load_dwordx4 v[28:31], v[80:81], off nt
	s_bitset1_b32 s98, 1
.LBB0_862:
	s_add_i32 s21, s8, -5
	s_cmp_ge_i32 s21, s6
	s_mov_b64 s[4:5], -1
	s_cbranch_scc1 .LBB0_856
	s_waitcnt vmcnt(12)
	s_cmp_eq_u32 s98, 15
	s_cbranch_scc1 .Lcvw_39
	s_waitcnt vmcnt(0)
.Lcvw_39:
	s_bitset0_b32 s98, 2
	s_ashr_i32 s4, s21, 31
	s_lshr_b32 s4, s4, 23
	s_add_i32 s21, s21, s4
	s_and_b32 s5, s21, 0xfffffe00
	v_mul_f32_e32 v69, 0x42800000, v32
	v_mul_f32_e32 v78, 0x42800000, v36
	v_mov_b32_e32 v81, v65
	s_sub_i32 s5, s8, s5
	v_cvt_pk_fp8_f32 v81, v69, v78
	v_mul_f32_e32 v69, 0x42800000, v33
	v_mul_f32_e32 v78, 0x42800000, v37
	v_mov_b32_e32 v82, v65
	s_add_i32 s5, s5, -5
	v_cvt_pk_fp8_f32 v82, v69, v78
	s_ashr_i32 s4, s21, 9
	s_ashr_i32 s21, s5, 31
	s_lshr_b32 s21, s21, 27
	s_add_i32 s5, s5, s21
	v_mul_f32_e32 v69, 0x42800000, v41
	v_mul_f32_e32 v78, 0x42800000, v45
	s_ashr_i32 s21, s5, 5
	s_ashr_i32 s5, s4, 31
	v_cvt_pk_fp8_f32 v82, v69, v78 op_sel:[0,0,1]
	v_mul_f32_e32 v69, 0x42800000, v34
	v_mul_f32_e32 v78, 0x42800000, v38
	v_mov_b32_e32 v83, v65
	s_lshl_b64 s[22:23], s[4:5], 22
	v_cvt_pk_fp8_f32 v83, v69, v78
	v_mul_f32_e32 v69, 0x42800000, v35
	v_mul_f32_e32 v78, 0x42800000, v39
	v_mov_b32_e32 v84, v65
	s_add_u32 s22, s38, s22
	v_cvt_pk_fp8_f32 v84, v69, v78
	s_addc_u32 s23, s39, s23
	s_lshl_b32 s5, s21, 8
	s_lshl_b32 s4, s4, 12
	s_add_i32 s5, s5, s4
	v_mul_f32_e32 v79, 0x42800000, v40
	v_mul_f32_e32 v80, 0x42800000, v44
	s_sub_i32 s4, s9, s5
	v_cvt_pk_fp8_f32 v81, v79, v80 op_sel:[0,0,1]
	v_mul_f32_e32 v79, 0x42800000, v42
	v_mul_f32_e32 v80, 0x42800000, v46
	v_mul_f32_e32 v69, 0x42800000, v43
	v_mul_f32_e32 v78, 0x42800000, v47
	s_add_i32 s4, s4, 16
	v_cvt_pk_fp8_f32 v83, v79, v80 op_sel:[0,0,1]
	v_cvt_pk_fp8_f32 v84, v69, v78 op_sel:[0,0,1]
	s_and_b32 s4, s4, -16
	s_add_i32 s4, s4, s21
	s_ashr_i32 s5, s4, 31
	ds_write2_b32 v73, v81, v82 offset1:33
	ds_write2_b32 v73, v83, v84 offset0:66 offset1:99
	s_waitcnt lgkmcnt(0)
	s_barrier
	ds_read2_b32 v[78:79], v74 offset1:1
	ds_read2_b32 v[80:81], v74 offset0:2 offset1:3
	s_lshl_b64 s[4:5], s[4:5], 14
	s_add_u32 s4, s22, s4
	s_addc_u32 s5, s23, s5
	v_lshl_add_u64 v[82:83], s[4:5], 0, v[64:65]
	s_add_i32 s4, s8, -1
	v_lshl_add_u64 v[82:83], v[82:83], 0, v[66:67]
	s_cmp_ge_i32 s4, s6
	s_waitcnt lgkmcnt(0)
	global_store_dwordx4 v[82:83], v[78:81], off nt
	s_cbranch_scc1 .LBB0_865
	s_ashr_i32 s5, s4, 31
	s_lshr_b32 s5, s5, 23
	s_add_i32 s5, s4, s5
	s_ashr_i32 s4, s5, 9
	s_orn2_b32 s5, 0x1ff, s5
	s_add_i32 s5, s5, s8
	s_ashr_i32 s21, s5, 31
	s_lshr_b32 s21, s21, 27
	s_add_i32 s5, s5, s21
	s_ashr_i32 s21, s5, 5
	s_ashr_i32 s5, s4, 31
	s_lshl_b64 s[22:23], s[4:5], 24
	s_add_u32 s22, s84, s22
	s_addc_u32 s23, s85, s23
	s_lshl_b32 s5, s21, 11
	s_lshl_b32 s4, s4, 15
	v_lshl_add_u32 v32, s21, 7, v70
	s_add_i32 s5, s5, s4
	v_ashrrev_i32_e32 v33, 31, v32
	s_sub_i32 s4, s7, s5
	v_lshlrev_b64 v[32:33], 13, v[32:33]
	s_addk_i32 s4, 0x180
	v_lshl_add_u64 v[32:33], s[22:23], 0, v[32:33]
	s_ashr_i32 s5, s4, 31
	v_lshl_add_u64 v[32:33], s[4:5], 2, v[32:33]
	v_mov_b32_e32 v69, v65
	v_lshl_add_u64 v[40:41], v[32:33], 0, v[68:69]
	v_add_co_u32_e32 v42, vcc, 0x2000, v40
	s_nop 1
	v_addc_co_u32_e32 v43, vcc, 0, v41, vcc
	v_add_co_u32_e32 v78, vcc, 0x4000, v40
	global_load_dwordx4 v[32:35], v[40:41], off nt
	global_load_dwordx4 v[36:39], v[42:43], off nt
	v_addc_co_u32_e32 v79, vcc, 0, v41, vcc
	v_add_co_u32_e32 v80, vcc, 0x6000, v40
	s_nop 1
	v_addc_co_u32_e32 v81, vcc, 0, v41, vcc
	global_load_dwordx4 v[40:43], v[78:79], off nt
	global_load_dwordx4 v[44:47], v[80:81], off nt
	s_bitset1_b32 s98, 2
.LBB0_865:
	s_add_i32 s21, s8, -4
	s_cmp_ge_i32 s21, s6
	s_mov_b64 s[4:5], -1
	s_cbranch_scc1 .LBB0_856
	s_waitcnt vmcnt(12)
	s_cmp_eq_u32 s98, 15
	s_cbranch_scc1 .Lcvw_40
	s_waitcnt vmcnt(0)
.Lcvw_40:
	s_bitset0_b32 s98, 3
	s_ashr_i32 s4, s21, 31
	s_lshr_b32 s4, s4, 23
	s_add_i32 s21, s21, s4
	s_and_b32 s5, s21, 0xfffffe00
	v_mul_f32_e32 v64, 0x42800000, v48
	v_mul_f32_e32 v69, 0x42800000, v52
	v_mov_b32_e32 v79, v65
	s_sub_i32 s5, s8, s5
	v_cvt_pk_fp8_f32 v79, v64, v69
	v_mul_f32_e32 v64, 0x42800000, v49
	v_mul_f32_e32 v69, 0x42800000, v53
	v_mov_b32_e32 v80, v65
	s_add_i32 s5, s5, -4
	v_cvt_pk_fp8_f32 v80, v64, v69
	s_ashr_i32 s4, s21, 9
	s_ashr_i32 s21, s5, 31
	s_lshr_b32 s21, s21, 27
	s_add_i32 s5, s5, s21
	v_mul_f32_e32 v64, 0x42800000, v57
	v_mul_f32_e32 v69, 0x42800000, v61
	s_ashr_i32 s21, s5, 5
	s_ashr_i32 s5, s4, 31
	v_cvt_pk_fp8_f32 v80, v64, v69 op_sel:[0,0,1]
	v_mul_f32_e32 v64, 0x42800000, v50
	v_mul_f32_e32 v69, 0x42800000, v54
	v_mov_b32_e32 v81, v65
	s_lshl_b64 s[22:23], s[4:5], 22
	v_cvt_pk_fp8_f32 v81, v64, v69
	v_mul_f32_e32 v64, 0x42800000, v51
	v_mul_f32_e32 v69, 0x42800000, v55
	v_mov_b32_e32 v82, v65
	s_add_u32 s22, s38, s22
	v_cvt_pk_fp8_f32 v82, v64, v69
	s_addc_u32 s23, s39, s23
	s_lshl_b32 s5, s21, 8
	s_lshl_b32 s4, s4, 12
	s_add_i32 s5, s5, s4
	v_mul_f32_e32 v74, 0x42800000, v56
	v_mul_f32_e32 v78, 0x42800000, v60
	s_sub_i32 s4, s9, s5
	v_cvt_pk_fp8_f32 v79, v74, v78 op_sel:[0,0,1]
	v_mul_f32_e32 v74, 0x42800000, v58
	v_mul_f32_e32 v78, 0x42800000, v62
	v_mul_f32_e32 v64, 0x42800000, v59
	v_mul_f32_e32 v69, 0x42800000, v63
	s_add_i32 s4, s4, 24
	v_cvt_pk_fp8_f32 v81, v74, v78 op_sel:[0,0,1]
	v_cvt_pk_fp8_f32 v82, v64, v69 op_sel:[0,0,1]
	s_and_b32 s4, s4, -16
	s_add_i32 s4, s4, s21
	s_ashr_i32 s5, s4, 31
	s_add_i32 s21, s7, 0xc0
	ds_write2_b32 v75, v79, v80 offset0:128 offset1:161
	ds_write2_b32 v75, v81, v82 offset0:194 offset1:227
	s_waitcnt lgkmcnt(0)
	s_barrier
	ds_read2_b32 v[74:75], v76 offset1:1
	ds_read2_b32 v[76:77], v77 offset1:1
	s_and_b32 s21, s21, 64
	s_lshl_b64 s[4:5], s[4:5], 14
	s_add_u32 s4, s22, s4
	v_add_lshl_u32 v64, s21, v198, 7
	s_addc_u32 s5, s23, s5
	v_lshl_add_u64 v[78:79], s[4:5], 0, v[64:65]
	v_lshl_add_u64 v[78:79], v[78:79], 0, v[66:67]
	s_cmp_ge_i32 s8, s6
	s_waitcnt lgkmcnt(0)
	global_store_dwordx4 v[78:79], v[74:77], off nt
	s_cbranch_scc1 .LBB0_855
	s_ashr_i32 s4, s8, 31
	s_lshr_b32 s4, s4, 23
	s_add_i32 s5, s8, s4
	s_ashr_i32 s4, s5, 9
	s_and_b32 s5, s5, 0xfffffe00
	s_sub_i32 s5, s8, s5
	s_ashr_i32 s21, s5, 31
	s_lshr_b32 s21, s21, 27
	s_add_i32 s5, s5, s21
	s_ashr_i32 s21, s5, 5
	s_ashr_i32 s5, s4, 31
	s_lshl_b64 s[22:23], s[4:5], 24
	s_add_u32 s22, s84, s22
	s_addc_u32 s23, s85, s23
	s_lshl_b32 s5, s21, 11
	s_lshl_b32 s4, s4, 15
	v_lshl_add_u32 v48, s21, 7, v70
	s_add_i32 s5, s5, s4
	v_ashrrev_i32_e32 v49, 31, v48
	s_sub_i32 s4, s7, s5
	v_lshlrev_b64 v[48:49], 13, v[48:49]
	s_addk_i32 s4, 0x1c0
	v_lshl_add_u64 v[48:49], s[22:23], 0, v[48:49]
	s_ashr_i32 s5, s4, 31
	v_lshl_add_u64 v[48:49], s[4:5], 2, v[48:49]
	v_mov_b32_e32 v69, v65
	v_lshl_add_u64 v[56:57], v[48:49], 0, v[68:69]
	v_add_co_u32_e32 v58, vcc, 0x2000, v56
	s_nop 1
	v_addc_co_u32_e32 v59, vcc, 0, v57, vcc
	v_add_co_u32_e32 v74, vcc, 0x4000, v56
	global_load_dwordx4 v[48:51], v[56:57], off nt
	global_load_dwordx4 v[52:55], v[58:59], off nt
	v_addc_co_u32_e32 v75, vcc, 0, v57, vcc
	v_add_co_u32_e32 v76, vcc, 0x6000, v56
	s_nop 1
	v_addc_co_u32_e32 v77, vcc, 0, v57, vcc
	global_load_dwordx4 v[56:59], v[74:75], off nt
	global_load_dwordx4 v[60:63], v[76:77], off nt
	s_bitset1_b32 s98, 3
	s_branch .LBB0_855

.LBB0_893:
	s_cmp_lt_i32 s94, 9
	s_cselect_b64 s[0:1], -1, 0
	s_and_b64 s[0:1], s[0:1], s[4:5]
	s_cmp_gt_i32 s36, 0
	s_cselect_b64 s[4:5], -1, 0
	s_and_b64 s[4:5], s[0:1], s[4:5]
	s_andn2_b64 vcc, exec, s[4:5]
	s_cbranch_vccnz .LBB0_923
	s_ashr_i32 s5, s96, 31
	s_lshr_b32 s5, s5, 29
	s_add_i32 s5, s96, s5
	s_ashr_i32 s14, s5, 3
	s_ashr_i32 s5, s33, 31
	s_lshr_b32 s5, s5, 29
	s_add_i32 s5, s33, s5
	s_and_b32 s7, s5, -8
	s_mul_hi_u32 s4, s36, 0xaaaaaaab
	s_sub_i32 s7, s33, s7
	s_lshr_b32 s6, s4, 4
	s_mul_i32 s14, s14, s7
	s_ashr_i32 s13, s5, 3
	s_sub_i32 s4, s96, s6
	s_add_i32 s12, s14, s13
	s_cmp_lt_i32 s12, s4
	s_cbranch_scc1 .LBB0_923
	s_sub_i32 s7, s12, s4
	s_add_i32 s7, s7, s37
	v_lshrrev_b32_e32 v1, 4, v178
	v_and_b32_e32 v66, 15, v178
	s_cmp_lt_i32 s7, s97
	s_waitcnt lgkmcnt(0)
	v_mov_b32_e32 v0, 0
	s_cselect_b64 s[4:5], -1, 0
	s_cmp_ge_i32 s7, s97
	v_lshlrev_b32_e32 v70, 2, v1
	v_lshlrev_b32_e32 v64, 4, v66
	s_waitcnt vmcnt(2)
	v_mov_b32_e32 v4, 0
	v_mov_b32_e32 v5, 0
	v_mov_b32_e32 v6, 0
	v_mov_b32_e32 v7, 0
	s_waitcnt vmcnt(1)
	v_mov_b32_e32 v8, 0
	v_mov_b32_e32 v9, 0
	v_mov_b32_e32 v10, 0
	v_mov_b32_e32 v11, 0
	s_waitcnt vmcnt(0)
	v_mov_b32_e32 v12, 0
	v_mov_b32_e32 v13, 0
	v_mov_b32_e32 v14, 0
	v_mov_b32_e32 v15, 0
	v_mov_b32_e32 v16, 0
	v_mov_b32_e32 v17, 0
	v_mov_b32_e32 v18, 0
	v_mov_b32_e32 v19, 0
	s_mov_b32 s98, 0
	s_barrier
	s_cbranch_scc1 .LBB0_897
	s_ashr_i32 s8, s7, 31
	s_lshr_b32 s8, s8, 23
	s_add_i32 s9, s7, s8
	s_ashr_i32 s8, s9, 9
	s_and_b32 s9, s9, 0xfffffe00
	s_sub_i32 s10, s7, s9
	s_ashr_i32 s9, s10, 31
	s_lshr_b32 s9, s9, 27
	s_add_i32 s9, s10, s9
	s_ashr_i32 s11, s9, 5
	s_ashr_i32 s9, s8, 31
	s_lshl_b64 s[8:9], s[8:9], 24
	v_lshl_add_u32 v2, s11, 7, v70
	s_add_u32 s8, s84, s8
	v_ashrrev_i32_e32 v3, 31, v2
	s_addc_u32 s9, s85, s9
	v_lshlrev_b64 v[2:3], 13, v[2:3]
	v_lshl_add_u64 v[2:3], s[8:9], 0, v[2:3]
	s_lshl_b32 s8, s11, 11
	s_lshl_b32 s9, s10, 6
	s_sub_i32 s8, s9, s8
	s_ashr_i32 s9, s8, 31
	v_lshl_add_u64 v[2:3], s[8:9], 2, v[2:3]
	v_mov_b32_e32 v65, 0
	v_lshl_add_u64 v[2:3], v[2:3], 0, v[64:65]
	s_movk_i32 s8, 0x2000
	v_add_co_u32_e32 v12, vcc, s8, v2
	s_movk_i32 s8, 0x4000
	s_nop 0
	v_addc_co_u32_e32 v13, vcc, 0, v3, vcc
	v_add_co_u32_e32 v20, vcc, s8, v2
	s_movk_i32 s8, 0x6000
	s_nop 0
	v_addc_co_u32_e32 v21, vcc, 0, v3, vcc
	global_load_dwordx4 v[4:7], v[2:3], off nt
	global_load_dwordx4 v[8:11], v[12:13], off nt
	v_add_co_u32_e32 v2, vcc, s8, v2
	s_nop 1
	v_addc_co_u32_e32 v3, vcc, 0, v3, vcc
	global_load_dwordx4 v[12:15], v[20:21], off nt
	global_load_dwordx4 v[16:19], v[2:3], off nt
	s_bitset1_b32 s98, 0
.LBB0_897:
	s_add_i32 s7, s7, s6
	s_cmp_ge_i32 s7, s97
	v_mov_b32_e32 v1, 0
	v_mov_b32_e32 v2, 0
	v_mov_b32_e32 v3, 0
	v_mov_b32_e32 v20, 0
	v_mov_b32_e32 v21, 0
	v_mov_b32_e32 v22, 0
	v_mov_b32_e32 v23, 0
	v_mov_b32_e32 v24, 0
	v_mov_b32_e32 v25, 0
	v_mov_b32_e32 v26, 0
	v_mov_b32_e32 v27, 0
	v_mov_b32_e32 v28, 0
	v_mov_b32_e32 v29, 0
	v_mov_b32_e32 v30, 0
	v_mov_b32_e32 v31, 0
	s_cbranch_scc1 .LBB0_899
	s_ashr_i32 s8, s7, 31
	s_lshr_b32 s8, s8, 23
	s_add_i32 s9, s7, s8
	s_ashr_i32 s8, s9, 9
	s_and_b32 s9, s9, 0xfffffe00
	s_sub_i32 s10, s7, s9
	s_ashr_i32 s9, s10, 31
	s_lshr_b32 s9, s9, 27
	s_add_i32 s9, s10, s9
	s_ashr_i32 s11, s9, 5
	s_ashr_i32 s9, s8, 31
	s_lshl_b64 s[8:9], s[8:9], 24
	v_lshl_add_u32 v0, s11, 7, v70
	s_add_u32 s8, s84, s8
	v_ashrrev_i32_e32 v1, 31, v0
	s_addc_u32 s9, s85, s9
	v_lshlrev_b64 v[0:1], 13, v[0:1]
	v_lshl_add_u64 v[0:1], s[8:9], 0, v[0:1]
	s_lshl_b32 s8, s11, 11
	s_lshl_b32 s9, s10, 6
	s_sub_i32 s8, s9, s8
	s_ashr_i32 s9, s8, 31
	v_lshl_add_u64 v[0:1], s[8:9], 2, v[0:1]
	v_mov_b32_e32 v65, 0
	v_lshl_add_u64 v[24:25], v[0:1], 0, v[64:65]
	s_movk_i32 s8, 0x2000
	v_add_co_u32_e32 v26, vcc, s8, v24
	s_movk_i32 s8, 0x4000
	s_nop 0
	v_addc_co_u32_e32 v27, vcc, 0, v25, vcc
	v_add_co_u32_e32 v32, vcc, s8, v24
	s_movk_i32 s8, 0x6000
	s_nop 0
	v_addc_co_u32_e32 v33, vcc, 0, v25, vcc
	v_add_co_u32_e32 v34, vcc, s8, v24
	global_load_dwordx4 v[0:3], v[24:25], off nt
	global_load_dwordx4 v[20:23], v[26:27], off nt
	v_addc_co_u32_e32 v35, vcc, 0, v25, vcc
	global_load_dwordx4 v[24:27], v[32:33], off nt
	global_load_dwordx4 v[28:31], v[34:35], off nt
	s_bitset1_b32 s98, 1
.LBB0_899:
	s_add_i32 s7, s7, s6
	s_cmp_ge_i32 s7, s97
	s_cbranch_scc1 .LBB0_901
	s_ashr_i32 s8, s7, 31
	s_lshr_b32 s8, s8, 23
	s_add_i32 s9, s7, s8
	s_ashr_i32 s8, s9, 9
	s_and_b32 s9, s9, 0xfffffe00
	s_sub_i32 s10, s7, s9
	s_ashr_i32 s9, s10, 31
	s_lshr_b32 s9, s9, 27
	s_add_i32 s9, s10, s9
	s_ashr_i32 s11, s9, 5
	s_ashr_i32 s9, s8, 31
	s_lshl_b64 s[8:9], s[8:9], 24
	v_lshl_add_u32 v32, s11, 7, v70
	s_add_u32 s8, s84, s8
	v_ashrrev_i32_e32 v33, 31, v32
	s_addc_u32 s9, s85, s9
	v_lshlrev_b64 v[32:33], 13, v[32:33]
	v_lshl_add_u64 v[32:33], s[8:9], 0, v[32:33]
	s_lshl_b32 s8, s11, 11
	s_lshl_b32 s9, s10, 6
	s_sub_i32 s8, s9, s8
	s_ashr_i32 s9, s8, 31
	v_lshl_add_u64 v[32:33], s[8:9], 2, v[32:33]
	v_mov_b32_e32 v65, 0
	v_lshl_add_u64 v[40:41], v[32:33], 0, v[64:65]
	s_movk_i32 s8, 0x2000
	v_add_co_u32_e32 v42, vcc, s8, v40
	s_nop 1
	v_addc_co_u32_e32 v43, vcc, 0, v41, vcc
	v_add_co_u32_e32 v48, vcc, 0x4000, v40
	global_load_dwordx4 v[32:35], v[40:41], off nt
	global_load_dwordx4 v[36:39], v[42:43], off nt
	v_addc_co_u32_e32 v49, vcc, 0, v41, vcc
	v_add_co_u32_e32 v50, vcc, 0x6000, v40
	s_nop 1
	v_addc_co_u32_e32 v51, vcc, 0, v41, vcc
	global_load_dwordx4 v[40:43], v[48:49], off nt
	global_load_dwordx4 v[44:47], v[50:51], off nt
	s_bitset1_b32 s98, 2
.LBB0_901:
	s_add_i32 s7, s7, s6
	s_cmp_ge_i32 s7, s97
	s_cbranch_scc1 .LBB0_903
	s_ashr_i32 s8, s7, 31
	s_lshr_b32 s8, s8, 23
	s_add_i32 s9, s7, s8
	s_ashr_i32 s8, s9, 9
	s_and_b32 s9, s9, 0xfffffe00
	s_sub_i32 s7, s7, s9
	s_ashr_i32 s9, s7, 31
	s_lshr_b32 s9, s9, 27
	s_add_i32 s9, s7, s9
	s_ashr_i32 s10, s9, 5
	s_ashr_i32 s9, s8, 31
	s_lshl_b64 s[8:9], s[8:9], 24
	v_lshl_add_u32 v48, s10, 7, v70
	s_add_u32 s8, s84, s8
	v_ashrrev_i32_e32 v49, 31, v48
	s_addc_u32 s9, s85, s9
	v_lshlrev_b64 v[48:49], 13, v[48:49]
	v_lshl_add_u64 v[48:49], s[8:9], 0, v[48:49]
	s_lshl_b32 s8, s10, 11
	s_lshl_b32 s7, s7, 6
	s_sub_i32 s8, s7, s8
	s_ashr_i32 s9, s8, 31
	v_lshl_add_u64 v[48:49], s[8:9], 2, v[48:49]
	v_mov_b32_e32 v65, 0
	v_lshl_add_u64 v[56:57], v[48:49], 0, v[64:65]
	s_movk_i32 s7, 0x2000
	v_add_co_u32_e32 v58, vcc, s7, v56
	s_nop 1
	v_addc_co_u32_e32 v59, vcc, 0, v57, vcc
	v_add_co_u32_e32 v64, vcc, 0x4000, v56
	global_load_dwordx4 v[48:51], v[56:57], off nt
	global_load_dwordx4 v[52:55], v[58:59], off nt
	v_addc_co_u32_e32 v65, vcc, 0, v57, vcc
	v_add_co_u32_e32 v72, vcc, 0x6000, v56
	s_nop 1
	v_addc_co_u32_e32 v73, vcc, 0, v57, vcc
	global_load_dwordx4 v[56:59], v[64:65], off nt
	global_load_dwordx4 v[60:63], v[72:73], off nt
	s_bitset1_b32 s98, 3
	s_andn2_b64 vcc, exec, s[4:5]
	s_cbranch_vccnz .LBB0_919
	s_branch .LBB0_904

.Lcvw_41:
	s_bitset0_b32 s98, 0
	s_add_i32 s5, s6, s31
	s_ashr_i32 s4, s5, 31
	s_lshr_b32 s4, s4, 23
	v_mul_f32_e32 v66, 0x42800000, v4
	v_mul_f32_e32 v74, 0x42800000, v8
	v_mov_b32_e32 v77, 0
	s_add_i32 s34, s5, s4
	v_cvt_pk_fp8_f32 v77, v66, v74
	v_mul_f32_e32 v66, 0x42800000, v5
	v_mul_f32_e32 v74, 0x42800000, v9
	v_mov_b32_e32 v78, 0
	s_ashr_i32 s4, s34, 9
	s_and_b32 s34, s34, 0xfffffe00
	v_cvt_pk_fp8_f32 v78, v66, v74
	s_sub_i32 s5, s5, s34
	s_ashr_i32 s34, s5, 31
	s_lshr_b32 s34, s34, 27
	v_mul_f32_e32 v66, 0x42800000, v13
	v_mul_f32_e32 v74, 0x42800000, v17
	s_add_i32 s5, s5, s34
	v_cvt_pk_fp8_f32 v78, v66, v74 op_sel:[0,0,1]
	v_mul_f32_e32 v66, 0x42800000, v6
	v_mul_f32_e32 v74, 0x42800000, v10
	v_mov_b32_e32 v79, 0
	s_ashr_i32 s40, s5, 5
	s_ashr_i32 s5, s4, 31
	v_cvt_pk_fp8_f32 v79, v66, v74
	v_mul_f32_e32 v66, 0x42800000, v7
	v_mul_f32_e32 v74, 0x42800000, v11
	v_mov_b32_e32 v80, 0
	s_lshl_b64 s[34:35], s[4:5], 22
	v_cvt_pk_fp8_f32 v80, v66, v74
	s_add_u32 s34, s38, s34
	s_addc_u32 s35, s39, s35
	s_lshl_b32 s5, s40, 8
	s_lshl_b32 s4, s4, 12
	v_mul_f32_e32 v75, 0x42800000, v12
	v_mul_f32_e32 v76, 0x42800000, v16
	s_add_i32 s5, s5, s4
	s_add_i32 s4, s24, s13
	v_cvt_pk_fp8_f32 v77, v75, v76 op_sel:[0,0,1]
	v_mul_f32_e32 v75, 0x42800000, v14
	v_mul_f32_e32 v76, 0x42800000, v18
	v_mul_f32_e32 v66, 0x42800000, v15
	v_mul_f32_e32 v74, 0x42800000, v19
	s_sub_i32 s4, s4, s5
	v_cvt_pk_fp8_f32 v79, v75, v76 op_sel:[0,0,1]
	v_cvt_pk_fp8_f32 v80, v66, v74 op_sel:[0,0,1]
	s_and_b32 s4, s4, -16
	s_add_i32 s4, s4, s40
	s_ashr_i32 s5, s4, 31
	s_add_i32 s40, s8, s9
	ds_write2_b32 v72, v77, v78 offset1:33
	ds_write2_b32 v72, v79, v80 offset0:66 offset1:99
	s_waitcnt lgkmcnt(0)
	s_barrier
	ds_read2_b32 v[74:75], v73 offset1:1
	ds_read2_b32 v[76:77], v73 offset0:2 offset1:3
	s_and_b32 s40, s40, 64
	s_lshl_b64 s[4:5], s[4:5], 14
	s_add_u32 s4, s34, s4
	v_add_lshl_u32 v66, s40, v71, 7
	s_addc_u32 s5, s35, s5
	v_lshl_add_u64 v[78:79], s[4:5], 0, v[66:67]
	s_add_i32 s4, s26, s31
	v_lshl_add_u64 v[78:79], v[78:79], 0, v[64:65]
	s_cmp_ge_i32 s4, s97
	s_waitcnt lgkmcnt(0)
	global_store_dwordx4 v[78:79], v[74:77], off nt
	s_cbranch_scc1 .LBB0_910
	s_ashr_i32 s5, s4, 31
	s_lshr_b32 s5, s5, 23
	s_add_i32 s5, s4, s5
	s_ashr_i32 s34, s5, 9
	s_and_b32 s5, s5, 0xfffffe00
	s_sub_i32 s4, s4, s5
	s_ashr_i32 s5, s4, 31
	s_lshr_b32 s5, s5, 27
	s_add_i32 s4, s4, s5
	s_ashr_i32 s40, s4, 5
	s_ashr_i32 s35, s34, 31
	s_lshl_b64 s[4:5], s[34:35], 24
	v_lshl_add_u32 v4, s40, 7, v70
	s_add_u32 s4, s84, s4
	v_ashrrev_i32_e32 v5, 31, v4
	s_addc_u32 s5, s85, s5
	v_lshlrev_b64 v[4:5], 13, v[4:5]
	v_lshl_add_u64 v[4:5], s[4:5], 0, v[4:5]
	s_lshl_b32 s4, s40, 11
	s_lshl_b32 s5, s34, 15
	s_add_i32 s4, s4, s5
	s_add_i32 s5, s8, s27
	s_sub_i32 s4, s5, s4
	s_ashr_i32 s5, s4, 31
	v_lshl_add_u64 v[4:5], s[4:5], 2, v[4:5]
	v_lshlrev_b32_e32 v66, 2, v68
	v_lshl_add_u64 v[12:13], v[4:5], 0, v[66:67]
	v_add_co_u32_e32 v8, vcc, s28, v12
	s_nop 1
	v_addc_co_u32_e32 v9, vcc, 0, v13, vcc
	v_add_co_u32_e32 v14, vcc, s29, v12
	global_load_dwordx4 v[4:7], v[12:13], off nt
	s_nop 0
	global_load_dwordx4 v[8:11], v[8:9], off nt
	v_addc_co_u32_e32 v15, vcc, 0, v13, vcc
	v_add_co_u32_e32 v16, vcc, s30, v12
	s_nop 1
	v_addc_co_u32_e32 v17, vcc, 0, v13, vcc
	global_load_dwordx4 v[12:15], v[14:15], off nt
	s_nop 0
	global_load_dwordx4 v[16:19], v[16:17], off nt
	s_bitset1_b32 s98, 0
	s_add_i32 s34, s11, s31
	s_cmp_ge_i32 s34, s97
	s_mov_b64 s[4:5], -1
	s_cbranch_scc1 .LBB0_907
	s_branch .LBB0_911

.Lcvw_42:
	s_bitset0_b32 s98, 1
	s_ashr_i32 s4, s34, 31
	s_lshr_b32 s4, s4, 23
	v_mul_f32_e32 v66, 0x42800000, v0
	v_mul_f32_e32 v74, 0x42800000, v20
	v_mov_b32_e32 v77, v67
	s_add_i32 s5, s34, s4
	v_cvt_pk_fp8_f32 v77, v66, v74
	v_mul_f32_e32 v66, 0x42800000, v1
	v_mul_f32_e32 v74, 0x42800000, v21
	v_mov_b32_e32 v78, v67
	s_ashr_i32 s4, s5, 9
	s_and_b32 s5, s5, 0xfffffe00
	v_cvt_pk_fp8_f32 v78, v66, v74
	s_sub_i32 s5, s34, s5
	s_ashr_i32 s34, s5, 31
	s_lshr_b32 s34, s34, 27
	v_mul_f32_e32 v66, 0x42800000, v25
	v_mul_f32_e32 v74, 0x42800000, v29
	s_add_i32 s5, s5, s34
	v_cvt_pk_fp8_f32 v78, v66, v74 op_sel:[0,0,1]
	v_mul_f32_e32 v66, 0x42800000, v2
	v_mul_f32_e32 v74, 0x42800000, v22
	v_mov_b32_e32 v79, v67
	s_ashr_i32 s40, s5, 5
	s_ashr_i32 s5, s4, 31
	v_cvt_pk_fp8_f32 v79, v66, v74
	v_mul_f32_e32 v66, 0x42800000, v3
	v_mul_f32_e32 v74, 0x42800000, v23
	v_mov_b32_e32 v80, v67
	s_lshl_b64 s[34:35], s[4:5], 22
	v_cvt_pk_fp8_f32 v80, v66, v74
	s_add_u32 s34, s38, s34
	s_addc_u32 s35, s39, s35
	s_lshl_b32 s5, s40, 8
	s_lshl_b32 s4, s4, 12
	v_mul_f32_e32 v75, 0x42800000, v24
	v_mul_f32_e32 v76, 0x42800000, v28
	s_add_i32 s5, s5, s4
	s_add_i32 s4, s12, s13
	v_cvt_pk_fp8_f32 v77, v75, v76 op_sel:[0,0,1]
	v_mul_f32_e32 v75, 0x42800000, v26
	v_mul_f32_e32 v76, 0x42800000, v30
	v_mul_f32_e32 v66, 0x42800000, v27
	v_mul_f32_e32 v74, 0x42800000, v31
	s_sub_i32 s4, s4, s5
	v_cvt_pk_fp8_f32 v79, v75, v76 op_sel:[0,0,1]
	v_cvt_pk_fp8_f32 v80, v66, v74 op_sel:[0,0,1]
	s_and_b32 s4, s4, -16
	s_add_i32 s4, s4, s40
	v_add_u32_e32 v74, 0x2000, v72
	v_add_u32_e32 v75, 0x2200, v73
	s_ashr_i32 s5, s4, 31
	s_add_i32 s40, s8, s15
	ds_write2_b32 v74, v77, v78 offset0:128 offset1:161
	ds_write2_b32 v74, v79, v80 offset0:194 offset1:227
	s_waitcnt lgkmcnt(0)
	s_barrier
	v_add_u32_e32 v76, 0x2208, v73
	ds_read2_b32 v[78:79], v75 offset1:1
	ds_read2_b32 v[80:81], v76 offset1:1
	s_and_b32 s40, s40, 64
	s_lshl_b64 s[4:5], s[4:5], 14
	s_add_u32 s4, s34, s4
	v_add_lshl_u32 v66, s40, v71, 7
	s_addc_u32 s5, s35, s5
	v_lshl_add_u64 v[82:83], s[4:5], 0, v[66:67]
	s_add_i32 s4, s16, s31
	v_lshl_add_u64 v[82:83], v[82:83], 0, v[64:65]
	s_cmp_ge_i32 s4, s97
	s_waitcnt lgkmcnt(0)
	global_store_dwordx4 v[82:83], v[78:81], off nt
	s_cbranch_scc1 .LBB0_913
	s_ashr_i32 s5, s4, 31
	s_lshr_b32 s5, s5, 23
	s_add_i32 s5, s4, s5
	s_ashr_i32 s34, s5, 9
	s_and_b32 s5, s5, 0xfffffe00
	s_sub_i32 s4, s4, s5
	s_ashr_i32 s5, s4, 31
	s_lshr_b32 s5, s5, 27
	s_add_i32 s4, s4, s5
	s_ashr_i32 s40, s4, 5
	s_ashr_i32 s35, s34, 31
	s_lshl_b64 s[4:5], s[34:35], 24
	v_lshl_add_u32 v0, s40, 7, v70
	s_add_u32 s4, s84, s4
	v_ashrrev_i32_e32 v1, 31, v0
	s_addc_u32 s5, s85, s5
	v_lshlrev_b64 v[0:1], 13, v[0:1]
	v_lshl_add_u64 v[0:1], s[4:5], 0, v[0:1]
	s_lshl_b32 s4, s40, 11
	s_lshl_b32 s5, s34, 15
	s_add_i32 s4, s4, s5
	s_add_i32 s5, s8, s17
	s_sub_i32 s4, s5, s4
	s_ashr_i32 s5, s4, 31
	v_lshl_add_u64 v[0:1], s[4:5], 2, v[0:1]
	v_lshlrev_b32_e32 v66, 2, v68
	v_lshl_add_u64 v[24:25], v[0:1], 0, v[66:67]
	v_add_co_u32_e32 v20, vcc, s28, v24
	s_nop 1
	v_addc_co_u32_e32 v21, vcc, 0, v25, vcc
	v_add_co_u32_e32 v26, vcc, s29, v24
	global_load_dwordx4 v[0:3], v[24:25], off nt
	s_nop 0
	global_load_dwordx4 v[20:23], v[20:21], off nt
	v_addc_co_u32_e32 v27, vcc, 0, v25, vcc
	v_add_co_u32_e32 v28, vcc, s30, v24
	s_nop 1
	v_addc_co_u32_e32 v29, vcc, 0, v25, vcc
	global_load_dwordx4 v[24:27], v[26:27], off nt
	s_nop 0
	global_load_dwordx4 v[28:31], v[28:29], off nt
	s_bitset1_b32 s98, 1
.LBB0_913:
	s_add_i32 s35, s18, s31
	s_cmp_ge_i32 s35, s97
	s_mov_b64 s[4:5], -1
	s_cbranch_scc1 .LBB0_906
	s_waitcnt vmcnt(12)
	s_cmp_eq_u32 s98, 15
	s_cbranch_scc1 .Lcvw_43
	s_waitcnt vmcnt(0)
.Lcvw_43:
	s_bitset0_b32 s98, 2
	s_ashr_i32 s4, s35, 31
	s_lshr_b32 s4, s4, 23
	v_mul_f32_e32 v66, 0x42800000, v32
	v_mul_f32_e32 v77, 0x42800000, v36
	v_mov_b32_e32 v80, v67
	s_add_i32 s5, s35, s4
	v_cvt_pk_fp8_f32 v80, v66, v77
	v_mul_f32_e32 v66, 0x42800000, v33
	v_mul_f32_e32 v77, 0x42800000, v37
	v_mov_b32_e32 v81, v67
	s_ashr_i32 s4, s5, 9
	s_and_b32 s5, s5, 0xfffffe00
	v_cvt_pk_fp8_f32 v81, v66, v77
	s_sub_i32 s5, s35, s5
	s_ashr_i32 s34, s5, 31
	s_lshr_b32 s34, s34, 27
	v_mul_f32_e32 v66, 0x42800000, v41
	v_mul_f32_e32 v77, 0x42800000, v45
	s_add_i32 s5, s5, s34
	v_cvt_pk_fp8_f32 v81, v66, v77 op_sel:[0,0,1]
	v_mul_f32_e32 v66, 0x42800000, v34
	v_mul_f32_e32 v77, 0x42800000, v38
	v_mov_b32_e32 v82, v67
	s_ashr_i32 s40, s5, 5
	s_ashr_i32 s5, s4, 31
	v_cvt_pk_fp8_f32 v82, v66, v77
	v_mul_f32_e32 v66, 0x42800000, v35
	v_mul_f32_e32 v77, 0x42800000, v39
	v_mov_b32_e32 v83, v67
	s_lshl_b64 s[34:35], s[4:5], 22
	v_cvt_pk_fp8_f32 v83, v66, v77
	s_add_u32 s34, s38, s34
	s_addc_u32 s35, s39, s35
	s_lshl_b32 s5, s40, 8
	s_lshl_b32 s4, s4, 12
	v_mul_f32_e32 v78, 0x42800000, v40
	v_mul_f32_e32 v79, 0x42800000, v44
	s_add_i32 s5, s5, s4
	s_add_i32 s4, s19, s13
	v_cvt_pk_fp8_f32 v80, v78, v79 op_sel:[0,0,1]
	v_mul_f32_e32 v78, 0x42800000, v42
	v_mul_f32_e32 v79, 0x42800000, v46
	v_mul_f32_e32 v66, 0x42800000, v43
	v_mul_f32_e32 v77, 0x42800000, v47
	s_sub_i32 s4, s4, s5
	v_cvt_pk_fp8_f32 v82, v78, v79 op_sel:[0,0,1]
	v_cvt_pk_fp8_f32 v83, v66, v77 op_sel:[0,0,1]
	s_and_b32 s4, s4, -16
	s_add_i32 s4, s4, s40
	s_ashr_i32 s5, s4, 31
	s_add_i32 s40, s8, s20
	ds_write2_b32 v72, v80, v81 offset1:33
	ds_write2_b32 v72, v82, v83 offset0:66 offset1:99
	s_waitcnt lgkmcnt(0)
	s_barrier
	ds_read2_b32 v[78:79], v73 offset1:1
	ds_read2_b32 v[80:81], v73 offset0:2 offset1:3
	s_and_b32 s40, s40, 64
	s_lshl_b64 s[4:5], s[4:5], 14
	s_add_u32 s4, s34, s4
	v_add_lshl_u32 v66, s40, v71, 7
	s_addc_u32 s5, s35, s5
	v_lshl_add_u64 v[82:83], s[4:5], 0, v[66:67]
	s_add_i32 s4, s21, s31
	v_lshl_add_u64 v[82:83], v[82:83], 0, v[64:65]
	s_cmp_ge_i32 s4, s97
	s_waitcnt lgkmcnt(0)
	global_store_dwordx4 v[82:83], v[78:81], off nt
	s_cbranch_scc1 .LBB0_916
	s_ashr_i32 s5, s4, 31
	s_lshr_b32 s5, s5, 23
	s_add_i32 s5, s4, s5
	s_ashr_i32 s34, s5, 9
	s_and_b32 s5, s5, 0xfffffe00
	s_sub_i32 s4, s4, s5
	s_ashr_i32 s5, s4, 31
	s_lshr_b32 s5, s5, 27
	s_add_i32 s4, s4, s5
	s_ashr_i32 s40, s4, 5
	s_ashr_i32 s35, s34, 31
	s_lshl_b64 s[4:5], s[34:35], 24
	v_lshl_add_u32 v32, s40, 7, v70
	s_add_u32 s4, s84, s4
	v_ashrrev_i32_e32 v33, 31, v32
	s_addc_u32 s5, s85, s5
	v_lshlrev_b64 v[32:33], 13, v[32:33]
	v_lshl_add_u64 v[32:33], s[4:5], 0, v[32:33]
	s_lshl_b32 s4, s40, 11
	s_lshl_b32 s5, s34, 15
	s_add_i32 s4, s4, s5
	s_add_i32 s5, s8, s22
	s_sub_i32 s4, s5, s4
	s_ashr_i32 s5, s4, 31
	v_lshl_add_u64 v[32:33], s[4:5], 2, v[32:33]
	v_lshlrev_b32_e32 v66, 2, v68
	v_lshl_add_u64 v[40:41], v[32:33], 0, v[66:67]
	v_add_co_u32_e32 v36, vcc, 0x2000, v40
	s_nop 1
	v_addc_co_u32_e32 v37, vcc, 0, v41, vcc
	v_add_co_u32_e32 v42, vcc, 0x4000, v40
	global_load_dwordx4 v[32:35], v[40:41], off nt
	s_nop 0
	global_load_dwordx4 v[36:39], v[36:37], off nt
	v_addc_co_u32_e32 v43, vcc, 0, v41, vcc
	v_add_co_u32_e32 v44, vcc, 0x6000, v40
	s_nop 1
	v_addc_co_u32_e32 v45, vcc, 0, v41, vcc
	global_load_dwordx4 v[40:43], v[42:43], off nt
	s_nop 0
	global_load_dwordx4 v[44:47], v[44:45], off nt
	s_bitset1_b32 s98, 2
.LBB0_916:
	s_add_i32 s34, s7, s31
	s_cmp_ge_i32 s34, s97
	s_mov_b64 s[4:5], -1
	s_cbranch_scc1 .LBB0_906
	s_waitcnt vmcnt(12)
	s_cmp_eq_u32 s98, 15
	s_cbranch_scc1 .Lcvw_44
	s_waitcnt vmcnt(0)
.Lcvw_44:
	s_bitset0_b32 s98, 3
	s_ashr_i32 s4, s34, 31
	s_lshr_b32 s4, s4, 23
	v_mul_f32_e32 v66, 0x42800000, v48
	v_mul_f32_e32 v77, 0x42800000, v52
	v_mov_b32_e32 v80, v67
	s_add_i32 s5, s34, s4
	v_cvt_pk_fp8_f32 v80, v66, v77
	v_mul_f32_e32 v66, 0x42800000, v49
	v_mul_f32_e32 v77, 0x42800000, v53
	v_mov_b32_e32 v81, v67
	s_ashr_i32 s4, s5, 9
	s_and_b32 s5, s5, 0xfffffe00
	v_cvt_pk_fp8_f32 v81, v66, v77
	s_sub_i32 s5, s34, s5
	s_ashr_i32 s35, s5, 31
	s_lshr_b32 s35, s35, 27
	v_mul_f32_e32 v66, 0x42800000, v57
	v_mul_f32_e32 v77, 0x42800000, v61
	s_add_i32 s5, s5, s35
	v_cvt_pk_fp8_f32 v81, v66, v77 op_sel:[0,0,1]
	v_mul_f32_e32 v66, 0x42800000, v50
	v_mul_f32_e32 v77, 0x42800000, v54
	v_mov_b32_e32 v82, v67
	s_ashr_i32 s35, s5, 5
	s_ashr_i32 s5, s4, 31
	v_cvt_pk_fp8_f32 v82, v66, v77
	v_mul_f32_e32 v66, 0x42800000, v51
	v_mul_f32_e32 v77, 0x42800000, v55
	v_mov_b32_e32 v83, v67
	s_lshl_b64 s[40:41], s[4:5], 22
	v_cvt_pk_fp8_f32 v83, v66, v77
	s_add_u32 s40, s38, s40
	s_addc_u32 s41, s39, s41
	s_lshl_b32 s5, s35, 8
	s_lshl_b32 s4, s4, 12
	v_mul_f32_e32 v78, 0x42800000, v56
	v_mul_f32_e32 v79, 0x42800000, v60
	s_add_i32 s5, s5, s4
	s_add_i32 s13, s14, s13
	v_cvt_pk_fp8_f32 v80, v78, v79 op_sel:[0,0,1]
	v_mul_f32_e32 v78, 0x42800000, v58
	v_mul_f32_e32 v79, 0x42800000, v62
	v_mul_f32_e32 v66, 0x42800000, v59
	v_mul_f32_e32 v77, 0x42800000, v63
	s_sub_i32 s4, s13, s5
	v_cvt_pk_fp8_f32 v82, v78, v79 op_sel:[0,0,1]
	v_cvt_pk_fp8_f32 v83, v66, v77 op_sel:[0,0,1]
	s_and_b32 s4, s4, -16
	s_add_i32 s4, s4, s35
	s_ashr_i32 s5, s4, 31
	s_add_i32 s35, s8, s23
	ds_write2_b32 v74, v80, v81 offset0:128 offset1:161
	ds_write2_b32 v74, v82, v83 offset0:194 offset1:227
	s_waitcnt lgkmcnt(0)
	s_barrier
	ds_read2_b32 v[74:75], v75 offset1:1
	ds_read2_b32 v[76:77], v76 offset1:1
	s_and_b32 s35, s35, 64
	s_lshl_b64 s[4:5], s[4:5], 14
	s_add_u32 s4, s40, s4
	v_add_lshl_u32 v66, s35, v71, 7
	s_addc_u32 s5, s41, s5
	v_lshl_add_u64 v[78:79], s[4:5], 0, v[66:67]
	s_add_i32 s4, s24, s31
	v_lshl_add_u64 v[78:79], v[78:79], 0, v[64:65]
	s_cmp_ge_i32 s4, s97
	s_waitcnt lgkmcnt(0)
	global_store_dwordx4 v[78:79], v[74:77], off nt
	s_cbranch_scc1 .LBB0_905
	s_ashr_i32 s5, s4, 31
	s_lshr_b32 s5, s5, 23
	s_add_i32 s5, s4, s5
	s_ashr_i32 s40, s5, 9
	s_and_b32 s5, s5, 0xfffffe00
	s_sub_i32 s4, s4, s5
	s_ashr_i32 s5, s4, 31
	s_lshr_b32 s5, s5, 27
	s_add_i32 s4, s4, s5
	s_ashr_i32 s31, s4, 5
	s_ashr_i32 s41, s40, 31
	s_lshl_b64 s[4:5], s[40:41], 24
	v_lshl_add_u32 v48, s31, 7, v70
	s_add_u32 s4, s84, s4
	v_ashrrev_i32_e32 v49, 31, v48
	s_addc_u32 s5, s85, s5
	v_lshlrev_b64 v[48:49], 13, v[48:49]
	v_lshl_add_u64 v[48:49], s[4:5], 0, v[48:49]
	s_lshl_b32 s4, s31, 11
	s_lshl_b32 s5, s40, 15
	s_add_i32 s4, s4, s5
	s_add_i32 s5, s8, s25
	s_sub_i32 s4, s5, s4
	s_ashr_i32 s5, s4, 31
	v_lshl_add_u64 v[48:49], s[4:5], 2, v[48:49]
	v_lshlrev_b32_e32 v66, 2, v68
	v_lshl_add_u64 v[56:57], v[48:49], 0, v[66:67]
	v_add_co_u32_e32 v52, vcc, 0x2000, v56
	s_nop 1
	v_addc_co_u32_e32 v53, vcc, 0, v57, vcc
	v_add_co_u32_e32 v58, vcc, 0x4000, v56
	global_load_dwordx4 v[48:51], v[56:57], off nt
	s_nop 0
	global_load_dwordx4 v[52:55], v[52:53], off nt
	v_addc_co_u32_e32 v59, vcc, 0, v57, vcc
	v_add_co_u32_e32 v60, vcc, 0x6000, v56
	s_nop 1
	v_addc_co_u32_e32 v61, vcc, 0, v57, vcc
	global_load_dwordx4 v[56:59], v[58:59], off nt
	s_nop 0
	global_load_dwordx4 v[60:63], v[60:61], off nt
	s_bitset1_b32 s98, 3
	s_branch .LBB0_905

	.amdhsa_kernel _Z4mega8MegaArgs
		.amdhsa_group_segment_fixed_size 256
		.amdhsa_private_segment_fixed_size 0
		.amdhsa_kernarg_size 424
		.amdhsa_user_sgpr_count 2
		.amdhsa_user_sgpr_dispatch_ptr 0
		.amdhsa_user_sgpr_queue_ptr 0
		.amdhsa_user_sgpr_kernarg_segment_ptr 1
		.amdhsa_user_sgpr_dispatch_id 0
		.amdhsa_user_sgpr_kernarg_preload_length 0
		.amdhsa_user_sgpr_kernarg_preload_offset 0
		.amdhsa_user_sgpr_private_segment_size 0
		.amdhsa_uses_dynamic_stack 0
		.amdhsa_enable_private_segment 0
		.amdhsa_system_sgpr_workgroup_id_x 1
		.amdhsa_system_sgpr_workgroup_id_y 0
		.amdhsa_system_sgpr_workgroup_id_z 0
		.amdhsa_system_sgpr_workgroup_info 0
		.amdhsa_system_vgpr_workitem_id 2
		.amdhsa_next_free_vgpr 251
		.amdhsa_next_free_sgpr 99
		.amdhsa_accum_offset 252
		.amdhsa_reserve_vcc 1
		.amdhsa_float_round_mode_32 0
		.amdhsa_float_round_mode_16_64 0
		.amdhsa_float_denorm_mode_32 3
		.amdhsa_float_denorm_mode_16_64 3
		.amdhsa_dx10_clamp 1
		.amdhsa_ieee_mode 1
		.amdhsa_fp16_overflow 0
		.amdhsa_tg_split 0
		.amdhsa_exception_fp_ieee_invalid_op 0
		.amdhsa_exception_fp_denorm_src 0
		.amdhsa_exception_fp_ieee_div_zero 0
		.amdhsa_exception_fp_ieee_overflow 0
		.amdhsa_exception_fp_ieee_underflow 0
		.amdhsa_exception_fp_ieee_inexact 0
		.amdhsa_exception_int_div_zero 0
	.end_amdhsa_kernel

amdhsa.kernels:
  - .agpr_count:     0
    .args:
      - .offset:         0
        .size:           168
        .value_kind:     by_value
      - .offset:         168
        .size:           4
        .value_kind:     hidden_block_count_x
      - .offset:         172
        .size:           4
        .value_kind:     hidden_block_count_y
      - .offset:         176
        .size:           4
        .value_kind:     hidden_block_count_z
      - .offset:         180
        .size:           2
        .value_kind:     hidden_group_size_x
      - .offset:         182
        .size:           2
        .value_kind:     hidden_group_size_y
      - .offset:         184
        .size:           2
        .value_kind:     hidden_group_size_z
      - .offset:         186
        .size:           2
        .value_kind:     hidden_remainder_x
      - .offset:         188
        .size:           2
        .value_kind:     hidden_remainder_y
      - .offset:         190
        .size:           2
        .value_kind:     hidden_remainder_z
      - .offset:         208
        .size:           8
        .value_kind:     hidden_global_offset_x
      - .offset:         216
        .size:           8
        .value_kind:     hidden_global_offset_y
      - .offset:         224
        .size:           8
        .value_kind:     hidden_global_offset_z
      - .offset:         232
        .size:           2
        .value_kind:     hidden_grid_dims
      - .offset:         288
        .size:           4
        .value_kind:     hidden_dynamic_lds_size
    .group_segment_fixed_size: 256
    .kernarg_segment_align: 8
    .kernarg_segment_size: 424
    .language:       OpenCL C
    .language_version:
      - 2
      - 0
    .max_flat_workgroup_size: 512
    .name:           _Z4mega8MegaArgs
    .private_segment_fixed_size: 0
    .sgpr_count:     105
    .sgpr_spill_count: 40
    .symbol:         _Z4mega8MegaArgs.kd
    .uniform_work_group_size: 1
    .uses_dynamic_stack: false
    .vgpr_count:     251
    .vgpr_spill_count: 0
    .wavefront_size: 64
